# v69 stack + lane^8 exchanges in the norm phases via v_mov_b32_dpp row_ror:8 instead of ds_swizzle(SWAP,8) (9 sites); padded
# speedup vs baseline: 1.0176x; 1.0047x over previous
; DI unsigned pk2(float lo, float hi) { const f32x2 v = {lo, hi}; return __builtin_bit_cast(unsigned, __builtin_convertvector(v, bf16x2_t)); }
; DI float wave_sum(float v) { v += shx<1>(v); v += shx<2>(v); v += shx<4>(v); v += shx<8>(v); v += shx<16>(v); v += shx<32>(v); return v; }
; template <int MODE, bool SB  > DI void norm_phase(const Params& P, const Frame& F, int L, const void* src_, const float* gain, bool combine) {
;     ...
;     for (int row = r_lo + F.wave; row < r_hi; row += NWAVES) {
;         f32x4 v[8];
; #pragma unroll
;         for (int j = 0; j < 8; ++j) { if constexpr (SB) v[j] = (f32x4){bflo(vb[j].x), bfhi(vb[j].x), bflo(vb[j].y), bfhi(vb[j].y)}; else v[j] = vn[j]; }
;         { const int rnx = (row + NWAVES < r_hi) ? row + NWAVES : row;
; #pragma unroll
;           for (int j = 0; j < 8; ++j) { if constexpr (SB) vb[j] = *(const u32x2*)(srcb + (size_t)rnx * D + 4 * F.lane + 256 * j); else vn[j] = *(const f32x4*)(src + (size_t)rnx * D + 4 * F.lane + 256 * j); } }
;         if (MODE == 3 && combine) {
;             const int* SLOT = (const int*)(ws + WS_SLOT); const float* TOPW = (const float*)(ws + WS_TOPW); const bf16* Y = (const bf16*)(ws + WS_T + T_YPERM);
;             const int s1 = SLOT[row * 2], s2 = SLOT[row * 2 + 1]; const float w1 = TOPW[row * 2], w2 = TOPW[row * 2 + 1];
;             u32x2 ya[8], yb[8];
; #pragma unroll
;             for (int j = 0; j < 8; ++j) { ya[j] = *(const u32x2*)(Y + (size_t)s1 * D + 4 * F.lane + 256 * j); yb[j] = *(const u32x2*)(Y + (size_t)s2 * D + 4 * F.lane + 256 * j); }
; #pragma unroll
;             for (int j = 0; j < 8; ++j) { const f32x4 y1 = (f32x4){bflo(ya[j].x), bfhi(ya[j].x), bflo(ya[j].y), bfhi(ya[j].y)}, y2 = (f32x4){bflo(yb[j].x), bfhi(yb[j].x), bflo(yb[j].y), bfhi(yb[j].y)};
;                 v[j] = v[j] + w1 * y1 + w2 * y2;
;                 const u32x2 hb = {pk2(v[j][0], v[j][1]), pk2(v[j][2], v[j][3])}; *(u32x2*)(const_cast<bf16*>(srcb) + (size_t)row * D + 4 * F.lane + 256 * j) = hb;
;                 v[j] = (f32x4){bflo(hb.x), bfhi(hb.x), bflo(hb.y), bfhi(hb.y)}; }
;         }
;         float ss = 0.f;
; #pragma unroll
;         for (int j = 0; j < 8; ++j) ss += (v[j][0] * v[j][0] + v[j][1] * v[j][1]) + (v[j][2] * v[j][2] + v[j][3] * v[j][3]);
;         const float rstd = 1.0f / sqrtf(wave_sum(ss) * (1.0f / D) + EPS);
.LBB0_83:
	s_waitcnt vmcnt(1)
	v_mov_b64_e32 v[90:91], v[38:39]
	s_waitcnt vmcnt(0)
	v_mov_b64_e32 v[94:95], v[34:35]
	v_mov_b64_e32 v[88:89], v[36:37]
	v_mov_b64_e32 v[92:93], v[32:33]
	v_mov_b32_e32 v114, v93
	v_mov_b32_e32 v115, v89
	v_mov_b32_e32 v112, v92
	v_mov_b32_e32 v113, v88
	v_pk_mul_f32 v[114:115], v[114:115], v[114:115]
	v_mov_b32_e32 v188, v95
	v_mov_b32_e32 v189, v91
	v_mov_b64_e32 v[86:87], v[42:43]
	v_pk_fma_f32 v[112:113], v[112:113], v[112:113], v[114:115]
	v_mov_b32_e32 v114, v94
	v_mov_b32_e32 v115, v90
	v_pk_mul_f32 v[188:189], v[188:189], v[188:189]
	v_mov_b64_e32 v[84:85], v[40:41]
	v_pk_fma_f32 v[114:115], v[114:115], v[114:115], v[188:189]
	v_pk_mul_f32 v[188:189], v[84:85], v[84:85]
	v_pk_add_f32 v[112:113], v[112:113], v[114:115]
	v_pk_mul_f32 v[114:115], v[86:87], v[86:87]
	v_mov_b64_e32 v[78:79], v[50:51]
	v_pk_mov_b32 v[190:191], v[188:189], v[114:115] op_sel:[1,0]
	v_mov_b32_e32 v189, v115
	v_mov_b64_e32 v[76:77], v[48:49]
	v_pk_add_f32 v[114:115], v[190:191], v[188:189]
	v_mov_b64_e32 v[82:83], v[46:47]
	v_mul_f32_e32 v111, v76, v76
	v_mul_f32_e32 v188, v77, v77
	v_pk_add_f32 v[112:113], v[112:113], v[112:113] op_sel:[0,1] op_sel_hi:[1,0]
	v_pk_add_f32 v[114:115], v[114:115], v[114:115] op_sel:[0,1] op_sel_hi:[1,0]
	v_mov_b64_e32 v[80:81], v[44:45]
	v_mov_b32_e32 v113, v111
	v_mov_b32_e32 v115, v188
	v_pk_add_f32 v[112:113], v[112:113], v[114:115]
	v_mul_f32_e32 v114, v81, v81
	v_mul_f32_e32 v189, v78, v78
	v_pk_fma_f32 v[114:115], v[80:81], v[80:81], v[114:115] op_sel_hi:[1,1,0]
	v_mul_f32_e32 v188, v83, v83
	v_mul_f32_e32 v190, v79, v79
	v_mov_b32_e32 v115, v189
	v_pk_fma_f32 v[188:189], v[82:83], v[82:83], v[188:189] op_sel_hi:[1,1,0]
	v_mov_b64_e32 v[74:75], v[54:55]
	v_mov_b32_e32 v189, v190
	v_mov_b64_e32 v[72:73], v[52:53]
	v_pk_add_f32 v[114:115], v[114:115], v[188:189]
	v_pk_mul_f32 v[188:189], v[72:73], v[72:73]
	v_pk_add_f32 v[112:113], v[112:113], v[114:115]
	v_pk_mul_f32 v[114:115], v[74:75], v[74:75]
	v_mov_b64_e32 v[66:67], v[62:63]
	v_pk_mov_b32 v[190:191], v[188:189], v[114:115] op_sel:[1,0]
	v_mov_b32_e32 v189, v115
	v_mov_b64_e32 v[64:65], v[60:61]
	v_pk_add_f32 v[114:115], v[190:191], v[188:189]
	v_mov_b64_e32 v[70:71], v[58:59]
	v_mul_f32_e32 v111, v64, v64
	v_mul_f32_e32 v188, v65, v65
	v_pk_add_f32 v[112:113], v[112:113], v[112:113] op_sel:[0,1] op_sel_hi:[1,0]
	v_pk_add_f32 v[114:115], v[114:115], v[114:115] op_sel:[0,1] op_sel_hi:[1,0]
	v_mov_b64_e32 v[68:69], v[56:57]
	v_mov_b32_e32 v113, v111
	v_mov_b32_e32 v115, v188
	v_pk_add_f32 v[112:113], v[112:113], v[114:115]
	v_mul_f32_e32 v114, v69, v69
	v_mul_f32_e32 v189, v66, v66
	v_pk_fma_f32 v[114:115], v[68:69], v[68:69], v[114:115] op_sel_hi:[1,1,0]
	v_mul_f32_e32 v188, v71, v71
	v_mul_f32_e32 v190, v67, v67
	v_mov_b32_e32 v115, v189
	v_pk_fma_f32 v[188:189], v[70:71], v[70:71], v[188:189] op_sel_hi:[1,1,0]
	s_mov_b32 s20, s0
	v_mov_b32_e32 v189, v190
	v_pk_add_f32 v[114:115], v[114:115], v[188:189]
	s_add_i32 s0, s0, 8
	v_pk_add_f32 v[112:113], v[112:113], v[114:115]
	s_cmp_ge_i32 s0, s3
	v_add_f32_e32 v111, v112, v113
	s_cselect_b64 s[22:23], -1, 0
	s_cmp_lt_i32 s0, s3
	v_add_f32_dpp v111, v111, v111 quad_perm:[1,0,3,2] row_mask:0xf bank_mask:0xf bound_ctrl:1
	s_cselect_b32 s20, s0, s20
	s_ashr_i32 s21, s20, 31
	v_add_f32_dpp v111, v111, v111 quad_perm:[2,3,0,1] row_mask:0xf bank_mask:0xf bound_ctrl:1
	ds_swizzle_b32 v112, v111 offset:swizzle(SWAP,4)
	s_lshl_b64 s[20:21], s[20:21], 13
	v_lshl_add_u64 v[48:49], v[96:97], 0, s[20:21]
	v_add_co_u32_e32 v60, vcc, s30, v48
	s_waitcnt lgkmcnt(0)
	v_add_f32_e32 v111, v111, v112
	s_nop 1
	v_mov_b32_dpp v112, v111 row_ror:8 row_mask:0xf bank_mask:0xf
	v_addc_co_u32_e32 v61, vcc, 0, v49, vcc
	s_mov_b32 s20, 0xf800000
	global_load_dwordx4 v[32:35], v[48:49], off
	global_load_dwordx4 v[36:39], v[48:49], off offset:1024
	global_load_dwordx4 v[40:43], v[48:49], off offset:2048
	global_load_dwordx4 v[44:47], v[48:49], off offset:3072
	s_waitcnt lgkmcnt(0)
	v_add_f32_e32 v111, v111, v112
	v_mov_b32_e32 v112, v111
	global_load_dwordx4 v[48:51], v[60:61], off
	global_load_dwordx4 v[52:55], v[60:61], off offset:1024
	global_load_dwordx4 v[56:59], v[60:61], off offset:2048
	s_nop 0
	global_load_dwordx4 v[60:63], v[60:61], off offset:3072
	s_waitcnt lgkmcnt(0)
	s_nop 1
	v_permlane16_swap_b32_e32 v111, v112
	v_add_f32_e32 v111, v111, v112
	v_mov_b32_e32 v112, v111
	s_waitcnt lgkmcnt(0)
; #define LAS __attribute__((address_space(3)))
; DI unsigned pk2(float lo, float hi) { const f32x2 v = {lo, hi}; return __builtin_bit_cast(unsigned, __builtin_convertvector(v, bf16x2_t)); }
; DI unsigned pk4_fp8(float a, float b, float c, float d) { unsigned w = 0u; w = __builtin_amdgcn_cvt_pk_fp8_f32(a, b, w, false); w = __builtin_amdgcn_cvt_pk_fp8_f32(c, d, w, true); return w; }
; DI float wave_sum(float v) { v += shx<1>(v); v += shx<2>(v); v += shx<4>(v); v += shx<8>(v); v += shx<16>(v); v += shx<32>(v); return v; }
; template <int MODE, bool SB  > DI void norm_phase(const Params& P, const Frame& F, int L, const void* src_, const float* gain, bool combine) {
;     ...
;         const float rstd = 1.0f / sqrtf(wave_sum(ss) * (1.0f / D) + EPS);
; #pragma unroll
;         for (int j = 0; j < 8; ++j) v[j] = v[j] * rstd * g[j];
;         if (MODE == 4) {
; #pragma unroll
;             for (int j = 0; j < 8; ++j) *(f32x4*)(P.out + (size_t)row * D + 4 * F.lane + 256 * j) = v[j];
;         } else if (MODE == 0 || MODE == 2 || (MODE == 3 && L == 1)) {
;             unsigned* o4 = (unsigned*)((unsigned char*)HN + (size_t)row * D) + F.lane; const float hs = (float)(1 << LS_HN);
; #pragma unroll
;             for (int j = 0; j < 8; ++j) o4[64 * j] = pk4_fp8(v[j][0] * hs, v[j][1] * hs, v[j][2] * hs, v[j][3] * hs);
;         } else {
;             unsigned long long* o8 = (unsigned long long*)(HN + (size_t)row * D) + F.lane;
; #pragma unroll
;             for (int j = 0; j < 8; ++j) o8[64 * j] = (unsigned long long)pk2(v[j][0], v[j][1]) | ((unsigned long long)pk2(v[j][2], v[j][3]) << 32);
;         }
;         if (MODE == 1) {
;             float s[16];
; #pragma unroll
;             for (int q = 0; q < 16; ++q) { float t = 0.f;
; #pragma unroll
;                 for (int j = 0; j < 8; ++j) { const f32x4 w = *(const LAS f32x4*)(F.lds + (size_t)(q * D + 256 * j + 4 * F.lane) * 4); t += (v[j][0] * w[0] + v[j][1] * w[1]) + (v[j][2] * w[2] + v[j][3] * w[3]); }
;                 s[q] = t; if ((q & 3) == 3) asm volatile("" ::: "memory"); }
	s_nop 1
	v_permlane32_swap_b32_e32 v111, v112
	v_add_f32_e32 v111, v111, v112
	v_fmamk_f32 v111, v111, 0x3a000000, v182
	v_cmp_gt_f32_e32 vcc, s20, v111
	v_mul_f32_e32 v112, 0x4f800000, v111
	s_nop 0
	v_cndmask_b32_e32 v111, v111, v112, vcc
	v_sqrt_f32_e32 v112, v111
	s_nop 0
	v_add_u32_e32 v113, -1, v112
	v_fma_f32 v114, -v113, v112, v111
	v_cmp_ge_f32_e64 s[20:21], 0, v114
	v_add_u32_e32 v114, 1, v112
	s_nop 0
	v_cndmask_b32_e64 v113, v112, v113, s[20:21]
	v_fma_f32 v112, -v114, v112, v111
	v_cmp_lt_f32_e64 s[20:21], 0, v112
	s_nop 1
	v_cndmask_b32_e64 v112, v113, v114, s[20:21]
	v_mul_f32_e32 v113, 0x37800000, v112
	v_cndmask_b32_e32 v112, v112, v113, vcc
	v_cmp_class_f32_e32 vcc, v111, v183
	s_nop 1
	v_cndmask_b32_e32 v111, v112, v111, vcc
	v_div_scale_f32 v112, s[20:21], v111, v111, 1.0
	v_rcp_f32_e32 v113, v112
	s_mov_b32 s20, 0x3d600000
	v_fma_f32 v114, -v112, v113, 1.0
	v_fmac_f32_e32 v113, v114, v113
	v_div_scale_f32 v114, vcc, 1.0, v111, 1.0
	v_mul_f32_e32 v115, v114, v113
	v_fma_f32 v188, -v112, v115, v114
	v_fmac_f32_e32 v115, v188, v113
	v_fma_f32 v112, -v112, v115, v114
	v_div_fmas_f32 v112, v112, v113, v115
	v_div_fixup_f32 v188, v112, v111, 1.0
	v_pk_mul_f32 v[94:95], v[94:95], v[188:189] op_sel_hi:[1,0]
	v_pk_mul_f32 v[88:89], v[88:89], v[188:189] op_sel_hi:[1,0]
	v_pk_mul_f32 v[86:87], v[86:87], v[188:189] op_sel_hi:[1,0]
	v_pk_mul_f32 v[80:81], v[80:81], v[188:189] op_sel_hi:[1,0]
	v_pk_mul_f32 v[78:79], v[78:79], v[188:189] op_sel_hi:[1,0]
	v_pk_mul_f32 v[72:73], v[72:73], v[188:189] op_sel_hi:[1,0]
	v_pk_mul_f32 v[70:71], v[70:71], v[188:189] op_sel_hi:[1,0]
	v_pk_mul_f32 v[64:65], v[64:65], v[188:189] op_sel_hi:[1,0]
	v_pk_mul_f32 v[92:93], v[92:93], v[188:189] op_sel_hi:[1,0]
	v_pk_mul_f32 v[112:113], v[2:3], v[94:95]
	v_pk_mul_f32 v[94:95], v[4:5], v[88:89]
	v_pk_mul_f32 v[88:89], v[10:11], v[86:87]
	v_pk_mul_f32 v[86:87], v[12:13], v[80:81]
	v_pk_mul_f32 v[80:81], v[18:19], v[78:79]
	v_pk_mul_f32 v[78:79], v[20:21], v[72:73]
	v_pk_mul_f32 v[72:73], v[26:27], v[70:71]
	v_pk_mul_f32 v[70:71], v[28:29], v[64:65]
	v_lshl_add_u64 v[64:65], s[54:55], 0, v[108:109]
	v_pk_mul_f32 v[114:115], v[0:1], v[92:93]
	v_pk_mul_f32 v[90:91], v[90:91], v[188:189] op_sel_hi:[1,0]
	v_pk_mul_f32 v[84:85], v[84:85], v[188:189] op_sel_hi:[1,0]
	v_pk_mul_f32 v[82:83], v[82:83], v[188:189] op_sel_hi:[1,0]
	v_pk_mul_f32 v[76:77], v[76:77], v[188:189] op_sel_hi:[1,0]
	v_pk_mul_f32 v[74:75], v[74:75], v[188:189] op_sel_hi:[1,0]
	v_pk_mul_f32 v[68:69], v[68:69], v[188:189] op_sel_hi:[1,0]
	v_pk_mul_f32 v[66:67], v[66:67], v[188:189] op_sel_hi:[1,0]
	v_add_co_u32_e32 v64, vcc, s20, v64
	v_pk_mul_f32 v[92:93], v[6:7], v[90:91]
	v_pk_mul_f32 v[90:91], v[8:9], v[84:85]
	v_pk_mul_f32 v[84:85], v[14:15], v[82:83]
	v_pk_mul_f32 v[82:83], v[16:17], v[76:77]
	v_pk_mul_f32 v[76:77], v[22:23], v[74:75]
	v_pk_mul_f32 v[74:75], v[24:25], v[68:69]
	v_pk_mul_f32 v[68:69], v[30:31], v[66:67]
	v_cvt_pk_bf16_f32 v66, v114, v115
	v_cvt_pk_bf16_f32 v67, v112, v113
	v_addc_co_u32_e32 v65, vcc, 0, v65, vcc
	global_store_dwordx2 v[64:65], v[66:67], off
	v_cvt_pk_bf16_f32 v66, v94, v95
	v_cvt_pk_bf16_f32 v67, v92, v93
	global_store_dwordx2 v[64:65], v[66:67], off offset:512
	v_cvt_pk_bf16_f32 v66, v90, v91
	v_cvt_pk_bf16_f32 v67, v88, v89
	global_store_dwordx2 v[64:65], v[66:67], off offset:1024
	v_cvt_pk_bf16_f32 v66, v86, v87
	v_cvt_pk_bf16_f32 v67, v84, v85
	global_store_dwordx2 v[64:65], v[66:67], off offset:1536
	v_cvt_pk_bf16_f32 v66, v82, v83
	v_cvt_pk_bf16_f32 v67, v80, v81
	global_store_dwordx2 v[64:65], v[66:67], off offset:2048
	v_cvt_pk_bf16_f32 v66, v78, v79
	v_cvt_pk_bf16_f32 v67, v76, v77
	global_store_dwordx2 v[64:65], v[66:67], off offset:2560
	v_cvt_pk_bf16_f32 v66, v74, v75
	v_cvt_pk_bf16_f32 v67, v72, v73
	global_store_dwordx2 v[64:65], v[66:67], off offset:3072
	v_cvt_pk_bf16_f32 v66, v70, v71
	v_cvt_pk_bf16_f32 v67, v68, v69
	global_store_dwordx2 v[64:65], v[66:67], off offset:3584
	ds_read_b128 v[216:219], v117
	ds_read_b128 v[220:223], v117 offset:1024
	ds_read_b128 v[224:227], v117 offset:2048
	ds_read_b128 v[228:231], v117 offset:3072
	ds_read_b128 v[232:235], v117 offset:4096
	ds_read_b128 v[236:239], v117 offset:5120
	ds_read_b128 v[240:243], v117 offset:6144
	ds_read_b128 v[248:251], v117 offset:7168
	s_waitcnt lgkmcnt(7)
	v_mul_f32_e32 v217, v217, v115
	v_fmac_f32_e32 v217, v216, v114
	v_mul_f32_e32 v216, v219, v113
	v_fmac_f32_e32 v216, v218, v112
	v_add_f32_e32 v216, v217, v216
	v_add_f32_e32 v111, 0, v216
	ds_read_b128 v[216:219], v117 offset:8192
	s_waitcnt lgkmcnt(7)
	v_mul_f32_e32 v221, v95, v221
	v_fmac_f32_e32 v221, v94, v220
	v_mul_f32_e32 v220, v93, v223
	v_fmac_f32_e32 v220, v92, v222
	v_add_f32_e32 v220, v221, v220
	v_add_f32_e32 v111, v220, v111
	ds_read_b128 v[220:223], v117 offset:9216
	s_waitcnt lgkmcnt(7)
	v_mul_f32_e32 v225, v91, v225
	v_fmac_f32_e32 v225, v90, v224
	v_mul_f32_e32 v224, v89, v227
	v_fmac_f32_e32 v224, v88, v226
	v_add_f32_e32 v224, v225, v224
	v_add_f32_e32 v111, v224, v111
	ds_read_b128 v[224:227], v117 offset:10240
	s_waitcnt lgkmcnt(7)
	v_mul_f32_e32 v229, v87, v229
	v_fmac_f32_e32 v229, v86, v228
	v_mul_f32_e32 v228, v85, v231
	v_fmac_f32_e32 v228, v84, v230
	v_add_f32_e32 v228, v229, v228
	v_add_f32_e32 v111, v228, v111
	ds_read_b128 v[228:231], v117 offset:11264
	s_waitcnt lgkmcnt(7)
	v_mul_f32_e32 v233, v83, v233
	v_fmac_f32_e32 v233, v82, v232
	v_mul_f32_e32 v232, v81, v235
	v_fmac_f32_e32 v232, v80, v234
	v_add_f32_e32 v232, v233, v232
	v_add_f32_e32 v111, v232, v111
	ds_read_b128 v[232:235], v117 offset:12288
	s_waitcnt lgkmcnt(7)
; #define LAS __attribute__((address_space(3)))
; template <int MODE, bool SB  > DI void norm_phase(const Params& P, const Frame& F, int L, const void* src_, const float* gain, bool combine) {
;     ...
;             for (int q = 0; q < 16; ++q) { float t = 0.f;
; #pragma unroll
;                 for (int j = 0; j < 8; ++j) { const f32x4 w = *(const LAS f32x4*)(F.lds + (size_t)(q * D + 256 * j + 4 * F.lane) * 4); t += (v[j][0] * w[0] + v[j][1] * w[1]) + (v[j][2] * w[2] + v[j][3] * w[3]); }
;                 s[q] = t; if ((q & 3) == 3) asm volatile("" ::: "memory"); }
	v_mul_f32_e32 v237, v79, v237
	v_fmac_f32_e32 v237, v78, v236
	v_mul_f32_e32 v236, v77, v239
	v_fmac_f32_e32 v236, v76, v238
	v_add_f32_e32 v236, v237, v236
	v_add_f32_e32 v111, v236, v111
	ds_read_b128 v[236:239], v117 offset:13312
	s_waitcnt lgkmcnt(7)
	v_mul_f32_e32 v241, v75, v241
	v_fmac_f32_e32 v241, v74, v240
	v_mul_f32_e32 v240, v73, v243
	v_fmac_f32_e32 v240, v72, v242
	v_add_f32_e32 v240, v241, v240
	v_add_f32_e32 v111, v240, v111
	ds_read_b128 v[240:243], v117 offset:14336
	s_waitcnt lgkmcnt(7)
	v_mul_f32_e32 v249, v71, v249
	v_fmac_f32_e32 v249, v70, v248
	v_mul_f32_e32 v248, v69, v251
	v_fmac_f32_e32 v248, v68, v250
	v_add_f32_e32 v248, v249, v248
	v_add_f32_e32 v111, v248, v111
	ds_read_b128 v[248:251], v117 offset:15360
	s_waitcnt lgkmcnt(7)
	v_mul_f32_e32 v217, v115, v217
	v_fmac_f32_e32 v217, v114, v216
	v_mul_f32_e32 v216, v113, v219
	v_fmac_f32_e32 v216, v112, v218
	v_add_f32_e32 v216, v217, v216
	v_add_f32_e32 v188, 0, v216
	ds_read_b128 v[216:219], v117 offset:16384
	s_waitcnt lgkmcnt(7)
	v_mul_f32_e32 v221, v95, v221
	v_fmac_f32_e32 v221, v94, v220
	v_mul_f32_e32 v220, v93, v223
	v_fmac_f32_e32 v220, v92, v222
	v_add_f32_e32 v220, v221, v220
	v_add_f32_e32 v188, v188, v220
	ds_read_b128 v[220:223], v117 offset:17408
	s_waitcnt lgkmcnt(7)
	v_mul_f32_e32 v225, v91, v225
	v_fmac_f32_e32 v225, v90, v224
	v_mul_f32_e32 v224, v89, v227
	v_fmac_f32_e32 v224, v88, v226
	v_add_f32_e32 v224, v225, v224
	v_add_f32_e32 v188, v188, v224
	ds_read_b128 v[224:227], v117 offset:18432
	s_waitcnt lgkmcnt(7)
	v_mul_f32_e32 v229, v87, v229
	v_fmac_f32_e32 v229, v86, v228
	v_mul_f32_e32 v228, v85, v231
	v_fmac_f32_e32 v228, v84, v230
	v_add_f32_e32 v228, v229, v228
	v_add_f32_e32 v188, v188, v228
	ds_read_b128 v[228:231], v117 offset:19456
	s_waitcnt lgkmcnt(7)
	v_mul_f32_e32 v233, v83, v233
	v_fmac_f32_e32 v233, v82, v232
	v_mul_f32_e32 v232, v81, v235
	v_fmac_f32_e32 v232, v80, v234
	v_add_f32_e32 v232, v233, v232
	v_add_f32_e32 v188, v188, v232
	ds_read_b128 v[232:235], v117 offset:20480
	s_waitcnt lgkmcnt(7)
	v_mul_f32_e32 v237, v79, v237
	v_fmac_f32_e32 v237, v78, v236
	v_mul_f32_e32 v236, v77, v239
	v_fmac_f32_e32 v236, v76, v238
	v_add_f32_e32 v236, v237, v236
	v_add_f32_e32 v188, v188, v236
	ds_read_b128 v[236:239], v117 offset:21504
	s_waitcnt lgkmcnt(7)
	v_mul_f32_e32 v241, v75, v241
	v_fmac_f32_e32 v241, v74, v240
	v_mul_f32_e32 v240, v73, v243
	v_fmac_f32_e32 v240, v72, v242
	v_add_f32_e32 v240, v241, v240
	v_add_f32_e32 v188, v188, v240
	ds_read_b128 v[240:243], v117 offset:22528
	s_waitcnt lgkmcnt(7)
	v_mul_f32_e32 v249, v71, v249
	v_fmac_f32_e32 v249, v70, v248
	v_mul_f32_e32 v248, v69, v251
	v_fmac_f32_e32 v248, v68, v250
	v_add_f32_e32 v248, v249, v248
	v_add_f32_e32 v188, v188, v248
	ds_read_b128 v[248:251], v117 offset:23552
	s_waitcnt lgkmcnt(7)
	v_mul_f32_e32 v217, v115, v217
	v_fmac_f32_e32 v217, v114, v216
	v_mul_f32_e32 v216, v113, v219
	v_fmac_f32_e32 v216, v112, v218
	v_add_f32_e32 v216, v217, v216
	v_add_f32_e32 v189, 0, v216
	ds_read_b128 v[216:219], v117 offset:24576
	s_waitcnt lgkmcnt(7)
	v_mul_f32_e32 v221, v95, v221
	v_fmac_f32_e32 v221, v94, v220
	v_mul_f32_e32 v220, v93, v223
	v_fmac_f32_e32 v220, v92, v222
	v_add_f32_e32 v220, v221, v220
	v_add_f32_e32 v189, v189, v220
	ds_read_b128 v[220:223], v117 offset:25600
	s_waitcnt lgkmcnt(7)
	v_mul_f32_e32 v225, v91, v225
	v_fmac_f32_e32 v225, v90, v224
	v_mul_f32_e32 v224, v89, v227
	v_fmac_f32_e32 v224, v88, v226
	v_add_f32_e32 v224, v225, v224
	v_add_f32_e32 v189, v189, v224
	ds_read_b128 v[224:227], v117 offset:26624
	s_waitcnt lgkmcnt(7)
	v_mul_f32_e32 v229, v87, v229
	v_fmac_f32_e32 v229, v86, v228
	v_mul_f32_e32 v228, v85, v231
	v_fmac_f32_e32 v228, v84, v230
	v_add_f32_e32 v228, v229, v228
	v_add_f32_e32 v189, v189, v228
	ds_read_b128 v[228:231], v117 offset:27648
	s_waitcnt lgkmcnt(7)
	v_mul_f32_e32 v233, v83, v233
	v_fmac_f32_e32 v233, v82, v232
	v_mul_f32_e32 v232, v81, v235
	v_fmac_f32_e32 v232, v80, v234
	v_add_f32_e32 v232, v233, v232
	v_add_f32_e32 v189, v189, v232
	ds_read_b128 v[232:235], v117 offset:28672
	s_waitcnt lgkmcnt(7)
	v_mul_f32_e32 v237, v79, v237
	v_fmac_f32_e32 v237, v78, v236
	v_mul_f32_e32 v236, v77, v239
	v_fmac_f32_e32 v236, v76, v238
	v_add_f32_e32 v236, v237, v236
	v_add_f32_e32 v189, v189, v236
	ds_read_b128 v[236:239], v117 offset:29696
	s_waitcnt lgkmcnt(7)
	v_mul_f32_e32 v241, v75, v241
	v_fmac_f32_e32 v241, v74, v240
	v_mul_f32_e32 v240, v73, v243
	v_fmac_f32_e32 v240, v72, v242
	v_add_f32_e32 v240, v241, v240
	v_add_f32_e32 v189, v189, v240
	ds_read_b128 v[240:243], v117 offset:30720
	s_waitcnt lgkmcnt(7)
	v_mul_f32_e32 v249, v71, v249
	v_fmac_f32_e32 v249, v70, v248
	v_mul_f32_e32 v248, v69, v251
	v_fmac_f32_e32 v248, v68, v250
	v_add_f32_e32 v248, v249, v248
	v_add_f32_e32 v189, v189, v248
	ds_read_b128 v[248:251], v117 offset:31744
	s_waitcnt lgkmcnt(7)
	v_mul_f32_e32 v217, v115, v217
	v_fmac_f32_e32 v217, v114, v216
	v_mul_f32_e32 v216, v113, v219
	v_fmac_f32_e32 v216, v112, v218
	v_add_f32_e32 v216, v217, v216
	v_add_f32_e32 v190, 0, v216
	ds_read_b128 v[216:219], v117 offset:32768
	s_waitcnt lgkmcnt(7)
	v_mul_f32_e32 v221, v95, v221
	v_fmac_f32_e32 v221, v94, v220
	v_mul_f32_e32 v220, v93, v223
	v_fmac_f32_e32 v220, v92, v222
	v_add_f32_e32 v220, v221, v220
	v_add_f32_e32 v190, v190, v220
	ds_read_b128 v[220:223], v117 offset:33792
	s_waitcnt lgkmcnt(7)
	v_mul_f32_e32 v225, v91, v225
	v_fmac_f32_e32 v225, v90, v224
	v_mul_f32_e32 v224, v89, v227
	v_fmac_f32_e32 v224, v88, v226
	v_add_f32_e32 v224, v225, v224
	v_add_f32_e32 v190, v190, v224
	ds_read_b128 v[224:227], v117 offset:34816
	s_waitcnt lgkmcnt(7)
; #define LAS __attribute__((address_space(3)))
; template <int MODE, bool SB  > DI void norm_phase(const Params& P, const Frame& F, int L, const void* src_, const float* gain, bool combine) {
;     ...
;             for (int q = 0; q < 16; ++q) { float t = 0.f;
; #pragma unroll
;                 for (int j = 0; j < 8; ++j) { const f32x4 w = *(const LAS f32x4*)(F.lds + (size_t)(q * D + 256 * j + 4 * F.lane) * 4); t += (v[j][0] * w[0] + v[j][1] * w[1]) + (v[j][2] * w[2] + v[j][3] * w[3]); }
;                 s[q] = t; if ((q & 3) == 3) asm volatile("" ::: "memory"); }
	v_mul_f32_e32 v229, v87, v229
	v_fmac_f32_e32 v229, v86, v228
	v_mul_f32_e32 v228, v85, v231
	v_fmac_f32_e32 v228, v84, v230
	v_add_f32_e32 v228, v229, v228
	v_add_f32_e32 v190, v190, v228
	ds_read_b128 v[228:231], v117 offset:35840
	s_waitcnt lgkmcnt(7)
	v_mul_f32_e32 v233, v83, v233
	v_fmac_f32_e32 v233, v82, v232
	v_mul_f32_e32 v232, v81, v235
	v_fmac_f32_e32 v232, v80, v234
	v_add_f32_e32 v232, v233, v232
	v_add_f32_e32 v190, v190, v232
	ds_read_b128 v[232:235], v117 offset:36864
	s_waitcnt lgkmcnt(7)
	v_mul_f32_e32 v237, v79, v237
	v_fmac_f32_e32 v237, v78, v236
	v_mul_f32_e32 v236, v77, v239
	v_fmac_f32_e32 v236, v76, v238
	v_add_f32_e32 v236, v237, v236
	v_add_f32_e32 v190, v190, v236
	ds_read_b128 v[236:239], v117 offset:37888
	s_waitcnt lgkmcnt(7)
	v_mul_f32_e32 v241, v75, v241
	v_fmac_f32_e32 v241, v74, v240
	v_mul_f32_e32 v240, v73, v243
	v_fmac_f32_e32 v240, v72, v242
	v_add_f32_e32 v240, v241, v240
	v_add_f32_e32 v190, v190, v240
	ds_read_b128 v[240:243], v117 offset:38912
	s_waitcnt lgkmcnt(7)
	v_mul_f32_e32 v249, v71, v249
	v_fmac_f32_e32 v249, v70, v248
	v_mul_f32_e32 v248, v69, v251
	v_fmac_f32_e32 v248, v68, v250
	v_add_f32_e32 v248, v249, v248
	v_add_f32_e32 v190, v190, v248
	ds_read_b128 v[248:251], v117 offset:39936
	s_waitcnt lgkmcnt(7)
	v_mul_f32_e32 v217, v115, v217
	v_fmac_f32_e32 v217, v114, v216
	v_mul_f32_e32 v216, v113, v219
	v_fmac_f32_e32 v216, v112, v218
	v_add_f32_e32 v216, v217, v216
	v_add_f32_e32 v191, 0, v216
	ds_read_b128 v[216:219], v117 offset:40960
	s_waitcnt lgkmcnt(7)
	v_mul_f32_e32 v221, v95, v221
	v_fmac_f32_e32 v221, v94, v220
	v_mul_f32_e32 v220, v93, v223
	v_fmac_f32_e32 v220, v92, v222
	v_add_f32_e32 v220, v221, v220
	v_add_f32_e32 v191, v191, v220
	ds_read_b128 v[220:223], v117 offset:41984
	s_waitcnt lgkmcnt(7)
	v_mul_f32_e32 v225, v91, v225
	v_fmac_f32_e32 v225, v90, v224
	v_mul_f32_e32 v224, v89, v227
	v_fmac_f32_e32 v224, v88, v226
	v_add_f32_e32 v224, v225, v224
	v_add_f32_e32 v191, v191, v224
	ds_read_b128 v[224:227], v117 offset:43008
	s_waitcnt lgkmcnt(7)
	v_mul_f32_e32 v229, v87, v229
	v_fmac_f32_e32 v229, v86, v228
	v_mul_f32_e32 v228, v85, v231
	v_fmac_f32_e32 v228, v84, v230
	v_add_f32_e32 v228, v229, v228
	v_add_f32_e32 v191, v191, v228
	ds_read_b128 v[228:231], v117 offset:44032
	s_waitcnt lgkmcnt(7)
	v_mul_f32_e32 v233, v83, v233
	v_fmac_f32_e32 v233, v82, v232
	v_mul_f32_e32 v232, v81, v235
	v_fmac_f32_e32 v232, v80, v234
	v_add_f32_e32 v232, v233, v232
	v_add_f32_e32 v191, v191, v232
	ds_read_b128 v[232:235], v117 offset:45056
	s_waitcnt lgkmcnt(7)
	v_mul_f32_e32 v237, v79, v237
	v_fmac_f32_e32 v237, v78, v236
	v_mul_f32_e32 v236, v77, v239
	v_fmac_f32_e32 v236, v76, v238
	v_add_f32_e32 v236, v237, v236
	v_add_f32_e32 v191, v191, v236
	ds_read_b128 v[236:239], v117 offset:46080
	s_waitcnt lgkmcnt(7)
	v_mul_f32_e32 v241, v75, v241
	v_fmac_f32_e32 v241, v74, v240
	v_mul_f32_e32 v240, v73, v243
	v_fmac_f32_e32 v240, v72, v242
	v_add_f32_e32 v240, v241, v240
	v_add_f32_e32 v191, v191, v240
	ds_read_b128 v[240:243], v117 offset:47104
	s_waitcnt lgkmcnt(7)
	v_mul_f32_e32 v249, v71, v249
	v_fmac_f32_e32 v249, v70, v248
	v_mul_f32_e32 v248, v69, v251
	v_fmac_f32_e32 v248, v68, v250
	v_add_f32_e32 v248, v249, v248
	v_add_f32_e32 v191, v191, v248
	ds_read_b128 v[248:251], v117 offset:48128
	s_waitcnt lgkmcnt(7)
	v_mul_f32_e32 v217, v115, v217
	v_fmac_f32_e32 v217, v114, v216
	v_mul_f32_e32 v216, v113, v219
	v_fmac_f32_e32 v216, v112, v218
	v_add_f32_e32 v216, v217, v216
	v_add_f32_e32 v192, 0, v216
	ds_read_b128 v[216:219], v117 offset:49152
	s_waitcnt lgkmcnt(7)
	v_mul_f32_e32 v221, v95, v221
	v_fmac_f32_e32 v221, v94, v220
	v_mul_f32_e32 v220, v93, v223
	v_fmac_f32_e32 v220, v92, v222
	v_add_f32_e32 v220, v221, v220
	v_add_f32_e32 v192, v192, v220
	ds_read_b128 v[220:223], v117 offset:50176
	s_waitcnt lgkmcnt(7)
	v_mul_f32_e32 v225, v91, v225
	v_fmac_f32_e32 v225, v90, v224
	v_mul_f32_e32 v224, v89, v227
	v_fmac_f32_e32 v224, v88, v226
	v_add_f32_e32 v224, v225, v224
	v_add_f32_e32 v192, v192, v224
	ds_read_b128 v[224:227], v117 offset:51200
	s_waitcnt lgkmcnt(7)
	v_mul_f32_e32 v229, v87, v229
	v_fmac_f32_e32 v229, v86, v228
	v_mul_f32_e32 v228, v85, v231
	v_fmac_f32_e32 v228, v84, v230
	v_add_f32_e32 v228, v229, v228
	v_add_f32_e32 v192, v192, v228
	ds_read_b128 v[228:231], v117 offset:52224
	s_waitcnt lgkmcnt(7)
	v_mul_f32_e32 v233, v83, v233
	v_fmac_f32_e32 v233, v82, v232
	v_mul_f32_e32 v232, v81, v235
	v_fmac_f32_e32 v232, v80, v234
	v_add_f32_e32 v232, v233, v232
	v_add_f32_e32 v192, v192, v232
	ds_read_b128 v[232:235], v117 offset:53248
	s_waitcnt lgkmcnt(7)
	v_mul_f32_e32 v237, v79, v237
	v_fmac_f32_e32 v237, v78, v236
	v_mul_f32_e32 v236, v77, v239
	v_fmac_f32_e32 v236, v76, v238
	v_add_f32_e32 v236, v237, v236
	v_add_f32_e32 v192, v192, v236
	ds_read_b128 v[236:239], v117 offset:54272
	s_waitcnt lgkmcnt(7)
	v_mul_f32_e32 v241, v75, v241
	v_fmac_f32_e32 v241, v74, v240
	v_mul_f32_e32 v240, v73, v243
	v_fmac_f32_e32 v240, v72, v242
	v_add_f32_e32 v240, v241, v240
	v_add_f32_e32 v192, v192, v240
	ds_read_b128 v[240:243], v117 offset:55296
	s_waitcnt lgkmcnt(7)
	v_mul_f32_e32 v249, v71, v249
	v_fmac_f32_e32 v249, v70, v248
	v_mul_f32_e32 v248, v69, v251
	v_fmac_f32_e32 v248, v68, v250
	v_add_f32_e32 v248, v249, v248
	v_add_f32_e32 v193, v192, v248
	ds_read_b128 v[248:251], v117 offset:56320
	s_waitcnt lgkmcnt(7)
	v_mul_f32_e32 v217, v115, v217
	v_fmac_f32_e32 v217, v114, v216
	v_mul_f32_e32 v216, v113, v219
	v_fmac_f32_e32 v216, v112, v218
	v_add_f32_e32 v216, v217, v216
	v_add_f32_e32 v192, 0, v216
	ds_read_b128 v[216:219], v117 offset:57344
	s_waitcnt lgkmcnt(7)
; #define LAS __attribute__((address_space(3)))
; template <int MODE, bool SB  > DI void norm_phase(const Params& P, const Frame& F, int L, const void* src_, const float* gain, bool combine) {
;     ...
;             for (int q = 0; q < 16; ++q) { float t = 0.f;
; #pragma unroll
;                 for (int j = 0; j < 8; ++j) { const f32x4 w = *(const LAS f32x4*)(F.lds + (size_t)(q * D + 256 * j + 4 * F.lane) * 4); t += (v[j][0] * w[0] + v[j][1] * w[1]) + (v[j][2] * w[2] + v[j][3] * w[3]); }
;                 s[q] = t; if ((q & 3) == 3) asm volatile("" ::: "memory"); }
	v_mul_f32_e32 v221, v95, v221
	v_fmac_f32_e32 v221, v94, v220
	v_mul_f32_e32 v220, v93, v223
	v_fmac_f32_e32 v220, v92, v222
	v_add_f32_e32 v220, v221, v220
	v_add_f32_e32 v192, v192, v220
	ds_read_b128 v[220:223], v117 offset:58368
	s_waitcnt lgkmcnt(7)
	v_mul_f32_e32 v225, v91, v225
	v_fmac_f32_e32 v225, v90, v224
	v_mul_f32_e32 v224, v89, v227
	v_fmac_f32_e32 v224, v88, v226
	v_add_f32_e32 v224, v225, v224
	v_add_f32_e32 v192, v192, v224
	ds_read_b128 v[224:227], v117 offset:59392
	s_waitcnt lgkmcnt(7)
	v_mul_f32_e32 v229, v87, v229
	v_fmac_f32_e32 v229, v86, v228
	v_mul_f32_e32 v228, v85, v231
	v_fmac_f32_e32 v228, v84, v230
	v_add_f32_e32 v228, v229, v228
	v_add_f32_e32 v192, v192, v228
	ds_read_b128 v[228:231], v117 offset:60416
	s_waitcnt lgkmcnt(7)
	v_mul_f32_e32 v233, v83, v233
	v_fmac_f32_e32 v233, v82, v232
	v_mul_f32_e32 v232, v81, v235
	v_fmac_f32_e32 v232, v80, v234
	v_add_f32_e32 v232, v233, v232
	v_add_f32_e32 v192, v192, v232
	ds_read_b128 v[232:235], v117 offset:61440
	s_waitcnt lgkmcnt(7)
	v_mul_f32_e32 v237, v79, v237
	v_fmac_f32_e32 v237, v78, v236
	v_mul_f32_e32 v236, v77, v239
	v_fmac_f32_e32 v236, v76, v238
	v_add_f32_e32 v236, v237, v236
	v_add_f32_e32 v192, v192, v236
	ds_read_b128 v[236:239], v117 offset:62464
	s_waitcnt lgkmcnt(7)
	v_mul_f32_e32 v241, v75, v241
	v_fmac_f32_e32 v241, v74, v240
	v_mul_f32_e32 v240, v73, v243
	v_fmac_f32_e32 v240, v72, v242
	v_add_f32_e32 v240, v241, v240
	v_add_f32_e32 v192, v192, v240
	ds_read_b128 v[240:243], v117 offset:63488
	s_waitcnt lgkmcnt(7)
	v_mul_f32_e32 v249, v71, v249
	v_fmac_f32_e32 v249, v70, v248
	v_mul_f32_e32 v248, v69, v251
	v_fmac_f32_e32 v248, v68, v250
	v_add_f32_e32 v248, v249, v248
	v_add_f32_e32 v194, v192, v248
	ds_read_b128 v[248:251], v117 offset:64512
	s_waitcnt lgkmcnt(7)
	v_mul_f32_e32 v217, v115, v217
	v_fmac_f32_e32 v217, v114, v216
	v_mul_f32_e32 v216, v113, v219
	v_fmac_f32_e32 v216, v112, v218
	v_add_f32_e32 v216, v217, v216
	v_add_f32_e32 v192, 0, v216
	ds_read_b128 v[216:219], v118
	s_waitcnt lgkmcnt(7)
	v_mul_f32_e32 v221, v95, v221
	v_fmac_f32_e32 v221, v94, v220
	v_mul_f32_e32 v220, v93, v223
	v_fmac_f32_e32 v220, v92, v222
	v_add_f32_e32 v220, v221, v220
	v_add_f32_e32 v192, v192, v220
	ds_read_b128 v[220:223], v119
	s_waitcnt lgkmcnt(7)
	v_mul_f32_e32 v225, v91, v225
	v_fmac_f32_e32 v225, v90, v224
	v_mul_f32_e32 v224, v89, v227
	v_fmac_f32_e32 v224, v88, v226
	v_add_f32_e32 v224, v225, v224
	v_add_f32_e32 v192, v192, v224
	ds_read_b128 v[224:227], v120
	s_waitcnt lgkmcnt(7)
	v_mul_f32_e32 v229, v87, v229
	v_fmac_f32_e32 v229, v86, v228
	v_mul_f32_e32 v228, v85, v231
	v_fmac_f32_e32 v228, v84, v230
	v_add_f32_e32 v228, v229, v228
	v_add_f32_e32 v192, v192, v228
	ds_read_b128 v[228:231], v121
	s_waitcnt lgkmcnt(7)
	v_mul_f32_e32 v233, v83, v233
	v_fmac_f32_e32 v233, v82, v232
	v_mul_f32_e32 v232, v81, v235
	v_fmac_f32_e32 v232, v80, v234
	v_add_f32_e32 v232, v233, v232
	v_add_f32_e32 v192, v192, v232
	ds_read_b128 v[232:235], v122
	s_waitcnt lgkmcnt(7)
	v_mul_f32_e32 v237, v79, v237
	v_fmac_f32_e32 v237, v78, v236
	v_mul_f32_e32 v236, v77, v239
	v_fmac_f32_e32 v236, v76, v238
	v_add_f32_e32 v236, v237, v236
	v_add_f32_e32 v192, v192, v236
	ds_read_b128 v[236:239], v123
	s_waitcnt lgkmcnt(7)
	v_mul_f32_e32 v241, v75, v241
	v_fmac_f32_e32 v241, v74, v240
	v_mul_f32_e32 v240, v73, v243
	v_fmac_f32_e32 v240, v72, v242
	v_add_f32_e32 v240, v241, v240
	v_add_f32_e32 v192, v192, v240
	ds_read_b128 v[240:243], v124
	s_waitcnt lgkmcnt(7)
	v_mul_f32_e32 v249, v71, v249
	v_fmac_f32_e32 v249, v70, v248
	v_mul_f32_e32 v248, v69, v251
	v_fmac_f32_e32 v248, v68, v250
	v_add_f32_e32 v248, v249, v248
	v_add_f32_e32 v195, v192, v248
	ds_read_b128 v[248:251], v125
	s_waitcnt lgkmcnt(7)
	v_mul_f32_e32 v217, v115, v217
	v_fmac_f32_e32 v217, v114, v216
	v_mul_f32_e32 v216, v113, v219
	v_fmac_f32_e32 v216, v112, v218
	v_add_f32_e32 v216, v217, v216
	v_add_f32_e32 v192, 0, v216
	ds_read_b128 v[216:219], v126
	s_waitcnt lgkmcnt(7)
	v_mul_f32_e32 v221, v95, v221
	v_fmac_f32_e32 v221, v94, v220
	v_mul_f32_e32 v220, v93, v223
	v_fmac_f32_e32 v220, v92, v222
	v_add_f32_e32 v220, v221, v220
	v_add_f32_e32 v192, v192, v220
	ds_read_b128 v[220:223], v127
	s_waitcnt lgkmcnt(7)
	v_mul_f32_e32 v225, v91, v225
	v_fmac_f32_e32 v225, v90, v224
	v_mul_f32_e32 v224, v89, v227
	v_fmac_f32_e32 v224, v88, v226
	v_add_f32_e32 v224, v225, v224
	v_add_f32_e32 v192, v192, v224
	ds_read_b128 v[224:227], v128
	s_waitcnt lgkmcnt(7)
	v_mul_f32_e32 v229, v87, v229
	v_fmac_f32_e32 v229, v86, v228
	v_mul_f32_e32 v228, v85, v231
	v_fmac_f32_e32 v228, v84, v230
	v_add_f32_e32 v228, v229, v228
	v_add_f32_e32 v192, v192, v228
	ds_read_b128 v[228:231], v129
	s_waitcnt lgkmcnt(7)
	v_mul_f32_e32 v233, v83, v233
	v_fmac_f32_e32 v233, v82, v232
	v_mul_f32_e32 v232, v81, v235
	v_fmac_f32_e32 v232, v80, v234
	v_add_f32_e32 v232, v233, v232
	v_add_f32_e32 v192, v192, v232
	ds_read_b128 v[232:235], v130
	s_waitcnt lgkmcnt(7)
	v_mul_f32_e32 v237, v79, v237
	v_fmac_f32_e32 v237, v78, v236
	v_mul_f32_e32 v236, v77, v239
	v_fmac_f32_e32 v236, v76, v238
	v_add_f32_e32 v236, v237, v236
	v_add_f32_e32 v192, v192, v236
	ds_read_b128 v[236:239], v131
	s_waitcnt lgkmcnt(7)
	v_mul_f32_e32 v241, v75, v241
	v_fmac_f32_e32 v241, v74, v240
	v_mul_f32_e32 v240, v73, v243
	v_fmac_f32_e32 v240, v72, v242
	v_add_f32_e32 v240, v241, v240
	v_add_f32_e32 v192, v192, v240
	ds_read_b128 v[240:243], v132
	s_waitcnt lgkmcnt(7)
	v_mul_f32_e32 v249, v71, v249
	v_fmac_f32_e32 v249, v70, v248
	v_mul_f32_e32 v248, v69, v251
	v_fmac_f32_e32 v248, v68, v250
	v_add_f32_e32 v248, v249, v248
	v_add_f32_e32 v196, v192, v248
	ds_read_b128 v[248:251], v133
	s_waitcnt lgkmcnt(7)
; #define LAS __attribute__((address_space(3)))
; template <int MODE, bool SB  > DI void norm_phase(const Params& P, const Frame& F, int L, const void* src_, const float* gain, bool combine) {
;     ...
;             for (int q = 0; q < 16; ++q) { float t = 0.f;
; #pragma unroll
;                 for (int j = 0; j < 8; ++j) { const f32x4 w = *(const LAS f32x4*)(F.lds + (size_t)(q * D + 256 * j + 4 * F.lane) * 4); t += (v[j][0] * w[0] + v[j][1] * w[1]) + (v[j][2] * w[2] + v[j][3] * w[3]); }
;                 s[q] = t; if ((q & 3) == 3) asm volatile("" ::: "memory"); }
	v_mul_f32_e32 v217, v115, v217
	v_fmac_f32_e32 v217, v114, v216
	v_mul_f32_e32 v216, v113, v219
	v_fmac_f32_e32 v216, v112, v218
	v_add_f32_e32 v216, v217, v216
	v_add_f32_e32 v192, 0, v216
	ds_read_b128 v[216:219], v134
	s_waitcnt lgkmcnt(7)
	v_mul_f32_e32 v221, v95, v221
	v_fmac_f32_e32 v221, v94, v220
	v_mul_f32_e32 v220, v93, v223
	v_fmac_f32_e32 v220, v92, v222
	v_add_f32_e32 v220, v221, v220
	v_add_f32_e32 v192, v192, v220
	ds_read_b128 v[220:223], v135
	s_waitcnt lgkmcnt(7)
	v_mul_f32_e32 v225, v91, v225
	v_fmac_f32_e32 v225, v90, v224
	v_mul_f32_e32 v224, v89, v227
	v_fmac_f32_e32 v224, v88, v226
	v_add_f32_e32 v224, v225, v224
	v_add_f32_e32 v192, v192, v224
	ds_read_b128 v[224:227], v136
	s_waitcnt lgkmcnt(7)
	v_mul_f32_e32 v229, v87, v229
	v_fmac_f32_e32 v229, v86, v228
	v_mul_f32_e32 v228, v85, v231
	v_fmac_f32_e32 v228, v84, v230
	v_add_f32_e32 v228, v229, v228
	v_add_f32_e32 v192, v192, v228
	ds_read_b128 v[228:231], v137
	s_waitcnt lgkmcnt(7)
	v_mul_f32_e32 v233, v83, v233
	v_fmac_f32_e32 v233, v82, v232
	v_mul_f32_e32 v232, v81, v235
	v_fmac_f32_e32 v232, v80, v234
	v_add_f32_e32 v232, v233, v232
	v_add_f32_e32 v192, v192, v232
	ds_read_b128 v[232:235], v138
	s_waitcnt lgkmcnt(7)
	v_mul_f32_e32 v237, v79, v237
	v_fmac_f32_e32 v237, v78, v236
	v_mul_f32_e32 v236, v77, v239
	v_fmac_f32_e32 v236, v76, v238
	v_add_f32_e32 v236, v237, v236
	v_add_f32_e32 v192, v192, v236
	ds_read_b128 v[236:239], v139
	s_waitcnt lgkmcnt(7)
	v_mul_f32_e32 v241, v75, v241
	v_fmac_f32_e32 v241, v74, v240
	v_mul_f32_e32 v240, v73, v243
	v_fmac_f32_e32 v240, v72, v242
	v_add_f32_e32 v240, v241, v240
	v_add_f32_e32 v192, v192, v240
	ds_read_b128 v[240:243], v140
	s_waitcnt lgkmcnt(7)
	v_mul_f32_e32 v249, v71, v249
	v_fmac_f32_e32 v249, v70, v248
	v_mul_f32_e32 v248, v69, v251
	v_fmac_f32_e32 v248, v68, v250
	v_add_f32_e32 v248, v249, v248
	v_add_f32_e32 v197, v192, v248
	ds_read_b128 v[248:251], v141
	s_waitcnt lgkmcnt(7)
	v_mul_f32_e32 v217, v115, v217
	v_fmac_f32_e32 v217, v114, v216
	v_mul_f32_e32 v216, v113, v219
	v_fmac_f32_e32 v216, v112, v218
	v_add_f32_e32 v216, v217, v216
	v_add_f32_e32 v192, 0, v216
	ds_read_b128 v[216:219], v142
	s_waitcnt lgkmcnt(7)
	v_mul_f32_e32 v221, v95, v221
	v_fmac_f32_e32 v221, v94, v220
	v_mul_f32_e32 v220, v93, v223
	v_fmac_f32_e32 v220, v92, v222
	v_add_f32_e32 v220, v221, v220
	v_add_f32_e32 v192, v192, v220
	ds_read_b128 v[220:223], v143
	s_waitcnt lgkmcnt(7)
	v_mul_f32_e32 v225, v91, v225
	v_fmac_f32_e32 v225, v90, v224
	v_mul_f32_e32 v224, v89, v227
	v_fmac_f32_e32 v224, v88, v226
	v_add_f32_e32 v224, v225, v224
	v_add_f32_e32 v192, v192, v224
	ds_read_b128 v[224:227], v144
	s_waitcnt lgkmcnt(7)
	v_mul_f32_e32 v229, v87, v229
	v_fmac_f32_e32 v229, v86, v228
	v_mul_f32_e32 v228, v85, v231
	v_fmac_f32_e32 v228, v84, v230
	v_add_f32_e32 v228, v229, v228
	v_add_f32_e32 v192, v192, v228
	ds_read_b128 v[228:231], v145
	s_waitcnt lgkmcnt(7)
	v_mul_f32_e32 v233, v83, v233
	v_fmac_f32_e32 v233, v82, v232
	v_mul_f32_e32 v232, v81, v235
	v_fmac_f32_e32 v232, v80, v234
	v_add_f32_e32 v232, v233, v232
	v_add_f32_e32 v192, v192, v232
	ds_read_b128 v[232:235], v146
	s_waitcnt lgkmcnt(7)
	v_mul_f32_e32 v237, v79, v237
	v_fmac_f32_e32 v237, v78, v236
	v_mul_f32_e32 v236, v77, v239
	v_fmac_f32_e32 v236, v76, v238
	v_add_f32_e32 v236, v237, v236
	v_add_f32_e32 v192, v192, v236
	ds_read_b128 v[236:239], v147
	s_waitcnt lgkmcnt(7)
	v_mul_f32_e32 v241, v75, v241
	v_fmac_f32_e32 v241, v74, v240
	v_mul_f32_e32 v240, v73, v243
	v_fmac_f32_e32 v240, v72, v242
	v_add_f32_e32 v240, v241, v240
	v_add_f32_e32 v192, v192, v240
	ds_read_b128 v[240:243], v148
	s_waitcnt lgkmcnt(7)
	v_mul_f32_e32 v249, v71, v249
	v_fmac_f32_e32 v249, v70, v248
	v_mul_f32_e32 v248, v69, v251
	v_fmac_f32_e32 v248, v68, v250
	v_add_f32_e32 v248, v249, v248
	v_add_f32_e32 v198, v192, v248
	ds_read_b128 v[248:251], v149
	s_waitcnt lgkmcnt(7)
	v_mul_f32_e32 v217, v115, v217
	v_fmac_f32_e32 v217, v114, v216
	v_mul_f32_e32 v216, v113, v219
	v_fmac_f32_e32 v216, v112, v218
	v_add_f32_e32 v216, v217, v216
	v_add_f32_e32 v192, 0, v216
	ds_read_b128 v[216:219], v150
	s_waitcnt lgkmcnt(7)
	v_mul_f32_e32 v221, v95, v221
	v_fmac_f32_e32 v221, v94, v220
	v_mul_f32_e32 v220, v93, v223
	v_fmac_f32_e32 v220, v92, v222
	v_add_f32_e32 v220, v221, v220
	v_add_f32_e32 v192, v192, v220
	ds_read_b128 v[220:223], v151
	s_waitcnt lgkmcnt(7)
	v_mul_f32_e32 v225, v91, v225
	v_fmac_f32_e32 v225, v90, v224
	v_mul_f32_e32 v224, v89, v227
	v_fmac_f32_e32 v224, v88, v226
	v_add_f32_e32 v224, v225, v224
	v_add_f32_e32 v192, v192, v224
	ds_read_b128 v[224:227], v152
	s_waitcnt lgkmcnt(7)
	v_mul_f32_e32 v229, v87, v229
	v_fmac_f32_e32 v229, v86, v228
	v_mul_f32_e32 v228, v85, v231
	v_fmac_f32_e32 v228, v84, v230
	v_add_f32_e32 v228, v229, v228
	v_add_f32_e32 v192, v192, v228
	ds_read_b128 v[228:231], v153
	s_waitcnt lgkmcnt(7)
	v_mul_f32_e32 v233, v83, v233
	v_fmac_f32_e32 v233, v82, v232
	v_mul_f32_e32 v232, v81, v235
	v_fmac_f32_e32 v232, v80, v234
	v_add_f32_e32 v232, v233, v232
	v_add_f32_e32 v192, v192, v232
	ds_read_b128 v[232:235], v154
	s_waitcnt lgkmcnt(7)
	v_mul_f32_e32 v237, v79, v237
	v_fmac_f32_e32 v237, v78, v236
	v_mul_f32_e32 v236, v77, v239
	v_fmac_f32_e32 v236, v76, v238
	v_add_f32_e32 v236, v237, v236
	v_add_f32_e32 v192, v192, v236
	ds_read_b128 v[236:239], v155
	s_waitcnt lgkmcnt(7)
	v_mul_f32_e32 v241, v75, v241
	v_fmac_f32_e32 v241, v74, v240
	v_mul_f32_e32 v240, v73, v243
	v_fmac_f32_e32 v240, v72, v242
	v_add_f32_e32 v240, v241, v240
	v_add_f32_e32 v192, v192, v240
	ds_read_b128 v[240:243], v156
	s_waitcnt lgkmcnt(7)
; #define LAS __attribute__((address_space(3)))
; template <int MODE, bool SB  > DI void norm_phase(const Params& P, const Frame& F, int L, const void* src_, const float* gain, bool combine) {
;     ...
;             for (int q = 0; q < 16; ++q) { float t = 0.f;
; #pragma unroll
;                 for (int j = 0; j < 8; ++j) { const f32x4 w = *(const LAS f32x4*)(F.lds + (size_t)(q * D + 256 * j + 4 * F.lane) * 4); t += (v[j][0] * w[0] + v[j][1] * w[1]) + (v[j][2] * w[2] + v[j][3] * w[3]); }
;                 s[q] = t; if ((q & 3) == 3) asm volatile("" ::: "memory"); }
	v_mul_f32_e32 v249, v71, v249
	v_fmac_f32_e32 v249, v70, v248
	v_mul_f32_e32 v248, v69, v251
	v_fmac_f32_e32 v248, v68, v250
	v_add_f32_e32 v248, v249, v248
	v_add_f32_e32 v199, v192, v248
	ds_read_b128 v[248:251], v157
	s_waitcnt lgkmcnt(7)
	v_mul_f32_e32 v217, v115, v217
	v_fmac_f32_e32 v217, v114, v216
	v_mul_f32_e32 v216, v113, v219
	v_fmac_f32_e32 v216, v112, v218
	v_add_f32_e32 v216, v217, v216
	v_add_f32_e32 v192, 0, v216
	ds_read_b128 v[216:219], v158
	s_waitcnt lgkmcnt(7)
	v_mul_f32_e32 v221, v95, v221
	v_fmac_f32_e32 v221, v94, v220
	v_mul_f32_e32 v220, v93, v223
	v_fmac_f32_e32 v220, v92, v222
	v_add_f32_e32 v220, v221, v220
	v_add_f32_e32 v192, v192, v220
	ds_read_b128 v[220:223], v159
	s_waitcnt lgkmcnt(7)
	v_mul_f32_e32 v225, v91, v225
	v_fmac_f32_e32 v225, v90, v224
	v_mul_f32_e32 v224, v89, v227
	v_fmac_f32_e32 v224, v88, v226
	v_add_f32_e32 v224, v225, v224
	v_add_f32_e32 v192, v192, v224
	ds_read_b128 v[224:227], v160
	s_waitcnt lgkmcnt(7)
	v_mul_f32_e32 v229, v87, v229
	v_fmac_f32_e32 v229, v86, v228
	v_mul_f32_e32 v228, v85, v231
	v_fmac_f32_e32 v228, v84, v230
	v_add_f32_e32 v228, v229, v228
	v_add_f32_e32 v192, v192, v228
	ds_read_b128 v[228:231], v161
	s_waitcnt lgkmcnt(7)
	v_mul_f32_e32 v233, v83, v233
	v_fmac_f32_e32 v233, v82, v232
	v_mul_f32_e32 v232, v81, v235
	v_fmac_f32_e32 v232, v80, v234
	v_add_f32_e32 v232, v233, v232
	v_add_f32_e32 v192, v192, v232
	ds_read_b128 v[232:235], v162
	s_waitcnt lgkmcnt(7)
	v_mul_f32_e32 v237, v79, v237
	v_fmac_f32_e32 v237, v78, v236
	v_mul_f32_e32 v236, v77, v239
	v_fmac_f32_e32 v236, v76, v238
	v_add_f32_e32 v236, v237, v236
	v_add_f32_e32 v192, v192, v236
	ds_read_b128 v[236:239], v163
	s_waitcnt lgkmcnt(7)
	v_mul_f32_e32 v241, v75, v241
	v_fmac_f32_e32 v241, v74, v240
	v_mul_f32_e32 v240, v73, v243
	v_fmac_f32_e32 v240, v72, v242
	v_add_f32_e32 v240, v241, v240
	v_add_f32_e32 v192, v192, v240
	ds_read_b128 v[240:243], v164
	s_waitcnt lgkmcnt(7)
	v_mul_f32_e32 v249, v71, v249
	v_fmac_f32_e32 v249, v70, v248
	v_mul_f32_e32 v248, v69, v251
	v_fmac_f32_e32 v248, v68, v250
	v_add_f32_e32 v248, v249, v248
	v_add_f32_e32 v200, v192, v248
	ds_read_b128 v[248:251], v165
	s_waitcnt lgkmcnt(7)
	v_mul_f32_e32 v217, v115, v217
	v_fmac_f32_e32 v217, v114, v216
	v_mul_f32_e32 v216, v113, v219
	v_fmac_f32_e32 v216, v112, v218
	v_add_f32_e32 v216, v217, v216
	v_add_f32_e32 v192, 0, v216
	ds_read_b128 v[216:219], v166
	s_waitcnt lgkmcnt(7)
	v_mul_f32_e32 v221, v95, v221
	v_fmac_f32_e32 v221, v94, v220
	v_mul_f32_e32 v220, v93, v223
	v_fmac_f32_e32 v220, v92, v222
	v_add_f32_e32 v220, v221, v220
	v_add_f32_e32 v192, v192, v220
	ds_read_b128 v[220:223], v167
	s_waitcnt lgkmcnt(7)
	v_mul_f32_e32 v225, v91, v225
	v_fmac_f32_e32 v225, v90, v224
	v_mul_f32_e32 v224, v89, v227
	v_fmac_f32_e32 v224, v88, v226
	v_add_f32_e32 v224, v225, v224
	v_add_f32_e32 v192, v192, v224
	ds_read_b128 v[224:227], v168
	s_waitcnt lgkmcnt(7)
	v_mul_f32_e32 v229, v87, v229
	v_fmac_f32_e32 v229, v86, v228
	v_mul_f32_e32 v228, v85, v231
	v_fmac_f32_e32 v228, v84, v230
	v_add_f32_e32 v228, v229, v228
	v_add_f32_e32 v192, v192, v228
	ds_read_b128 v[228:231], v169
	s_waitcnt lgkmcnt(7)
	v_mul_f32_e32 v233, v83, v233
	v_fmac_f32_e32 v233, v82, v232
	v_mul_f32_e32 v232, v81, v235
	v_fmac_f32_e32 v232, v80, v234
	v_add_f32_e32 v232, v233, v232
	v_add_f32_e32 v192, v192, v232
	ds_read_b128 v[232:235], v170
	s_waitcnt lgkmcnt(7)
	v_mul_f32_e32 v237, v79, v237
	v_fmac_f32_e32 v237, v78, v236
	v_mul_f32_e32 v236, v77, v239
	v_fmac_f32_e32 v236, v76, v238
	v_add_f32_e32 v236, v237, v236
	v_add_f32_e32 v192, v192, v236
	ds_read_b128 v[236:239], v171
	s_waitcnt lgkmcnt(7)
	v_mul_f32_e32 v241, v75, v241
	v_fmac_f32_e32 v241, v74, v240
	v_mul_f32_e32 v240, v73, v243
	v_fmac_f32_e32 v240, v72, v242
	v_add_f32_e32 v240, v241, v240
	v_add_f32_e32 v192, v192, v240
	ds_read_b128 v[240:243], v172
	s_waitcnt lgkmcnt(7)
	v_mul_f32_e32 v249, v71, v249
	v_fmac_f32_e32 v249, v70, v248
	v_mul_f32_e32 v248, v69, v251
	v_fmac_f32_e32 v248, v68, v250
	v_add_f32_e32 v248, v249, v248
	v_add_f32_e32 v201, v192, v248
	ds_read_b128 v[248:251], v173
	s_waitcnt lgkmcnt(7)
	v_mul_f32_e32 v217, v115, v217
	v_fmac_f32_e32 v217, v114, v216
	v_mul_f32_e32 v216, v113, v219
	v_fmac_f32_e32 v216, v112, v218
	v_add_f32_e32 v216, v217, v216
	v_add_f32_e32 v192, 0, v216
	ds_read_b128 v[216:219], v174
	s_waitcnt lgkmcnt(7)
	v_mul_f32_e32 v221, v95, v221
	v_fmac_f32_e32 v221, v94, v220
	v_mul_f32_e32 v220, v93, v223
	v_fmac_f32_e32 v220, v92, v222
	v_add_f32_e32 v220, v221, v220
	v_add_f32_e32 v192, v192, v220
	ds_read_b128 v[220:223], v175
	s_waitcnt lgkmcnt(7)
	v_mul_f32_e32 v225, v91, v225
	v_fmac_f32_e32 v225, v90, v224
	v_mul_f32_e32 v224, v89, v227
	v_fmac_f32_e32 v224, v88, v226
	v_add_f32_e32 v224, v225, v224
	v_add_f32_e32 v192, v192, v224
	ds_read_b128 v[224:227], v176
	s_waitcnt lgkmcnt(7)
	v_mul_f32_e32 v229, v87, v229
	v_fmac_f32_e32 v229, v86, v228
	v_mul_f32_e32 v228, v85, v231
	v_fmac_f32_e32 v228, v84, v230
	v_add_f32_e32 v228, v229, v228
	v_add_f32_e32 v192, v192, v228
	ds_read_b128 v[228:231], v177
	s_waitcnt lgkmcnt(7)
; #define LAS __attribute__((address_space(3)))
; DI float sigmoidf_(float x) { return __builtin_amdgcn_rcpf(1.0f + __expf(-x)); }
; DI float softplusf_(float x) { return fmaxf(x, 0.f) + log1pf(__expf(-fabsf(x))); }
; template <int MODE, bool SB  > DI void norm_phase(const Params& P, const Frame& F, int L, const void* src_, const float* gain, bool combine) {
;     ...
;                 for (int j = 0; j < 8; ++j) { const f32x4 w = *(const LAS f32x4*)(F.lds + (size_t)(q * D + 256 * j + 4 * F.lane) * 4); t += (v[j][0] * w[0] + v[j][1] * w[1]) + (v[j][2] * w[2] + v[j][3] * w[3]); }
;                 s[q] = t; if ((q & 3) == 3) asm volatile("" ::: "memory"); }
; #pragma unroll
;             for (int i = 0; i < 8; ++i) { const bool hi = (F.lane & 32) != 0; const float send = hi ? s[i] : s[i + 8], keep = hi ? s[i + 8] : s[i]; s[i] = keep + shx<32>(send); }
; #pragma unroll
;             for (int i = 0; i < 4; ++i) { const bool hi = (F.lane & 16) != 0; const float send = hi ? s[i] : s[i + 4], keep = hi ? s[i + 4] : s[i]; s[i] = keep + shx<16>(send); }
; #pragma unroll
;             for (int i = 0; i < 2; ++i) { const bool hi = (F.lane & 8) != 0; const float send = hi ? s[i] : s[i + 2], keep = hi ? s[i + 2] : s[i]; s[i] = keep + shx<8>(send); }
;             { const bool hi = (F.lane & 4) != 0; const float send = hi ? s[0] : s[1], keep = hi ? s[1] : s[0]; s[0] = keep + shx<4>(send); }
;             float mine = s[0]; mine += shx<2>(mine); mine += shx<1>(mine);
;             if ((F.lane & 3) == 0) { const int gi = ((F.lane >> 5) & 1) * 8 + ((F.lane >> 4) & 1) * 4 + ((F.lane >> 3) & 1) * 2 + ((F.lane >> 2) & 1), h = gi & 3; float r;
;                 if (gi < 4) r = sigmoidf_(mine);
;                 else if (gi < 8) r = -__expf(P.in[I_DN_A_LOG][L * 4 + h]) * softplusf_(mine + P.in[I_DN_DT_BIAS][L * 4 + h]);
;                 else if (gi < 12) r = mine + P.in[I_ML_I_BIAS][L * 4 + h];
;                 else r = -softplusf_(-(mine + P.in[I_ML_F_BIAS][L * 4 + h]));
;                 ((float*)(ws + WS_GD))[(size_t)row * 16 + gi] = r; }
	v_mul_f32_e32 v233, v83, v233
	v_fmac_f32_e32 v233, v82, v232
	v_mul_f32_e32 v232, v81, v235
	v_fmac_f32_e32 v232, v80, v234
	v_add_f32_e32 v232, v233, v232
	v_add_f32_e32 v192, v192, v232
	ds_read_b128 v[232:235], v178
	s_waitcnt lgkmcnt(7)
	v_mul_f32_e32 v237, v79, v237
	v_fmac_f32_e32 v237, v78, v236
	v_mul_f32_e32 v236, v77, v239
	v_fmac_f32_e32 v236, v76, v238
	v_add_f32_e32 v236, v237, v236
	v_add_f32_e32 v192, v192, v236
	ds_read_b128 v[236:239], v179
	s_waitcnt lgkmcnt(7)
	v_mul_f32_e32 v241, v75, v241
	v_fmac_f32_e32 v241, v74, v240
	v_mul_f32_e32 v240, v73, v243
	v_fmac_f32_e32 v240, v72, v242
	v_add_f32_e32 v240, v241, v240
	v_add_f32_e32 v192, v192, v240
	ds_read_b128 v[240:243], v180
	s_waitcnt lgkmcnt(7)
	v_mul_f32_e32 v249, v71, v249
	v_fmac_f32_e32 v249, v70, v248
	v_mul_f32_e32 v248, v69, v251
	v_fmac_f32_e32 v248, v68, v250
	v_add_f32_e32 v248, v249, v248
	v_add_f32_e32 v202, v192, v248
	ds_read_b128 v[64:67], v181
	s_waitcnt lgkmcnt(7)
	v_mul_f32_e32 v217, v115, v217
	v_fmac_f32_e32 v217, v114, v216
	v_mul_f32_e32 v216, v113, v219
	v_fmac_f32_e32 v216, v112, v218
	v_add_f32_e32 v216, v217, v216
	v_add_f32_e32 v112, 0, v216
	s_waitcnt lgkmcnt(6)
	v_mul_f32_e32 v221, v95, v221
	v_fmac_f32_e32 v221, v94, v220
	v_mul_f32_e32 v220, v93, v223
	v_fmac_f32_e32 v220, v92, v222
	v_add_f32_e32 v220, v221, v220
	v_add_f32_e32 v92, v112, v220
	s_waitcnt lgkmcnt(5)
	v_mul_f32_e32 v225, v91, v225
	v_fmac_f32_e32 v225, v90, v224
	v_mul_f32_e32 v224, v89, v227
	v_fmac_f32_e32 v224, v88, v226
	v_add_f32_e32 v224, v225, v224
	v_add_f32_e32 v88, v92, v224
	s_waitcnt lgkmcnt(4)
	v_mul_f32_e32 v229, v87, v229
	v_fmac_f32_e32 v229, v86, v228
	v_mul_f32_e32 v228, v85, v231
	v_fmac_f32_e32 v228, v84, v230
	v_add_f32_e32 v228, v229, v228
	v_add_f32_e32 v84, v88, v228
	s_waitcnt lgkmcnt(3)
	v_mul_f32_e32 v233, v83, v233
	v_fmac_f32_e32 v233, v82, v232
	v_mul_f32_e32 v232, v81, v235
	v_fmac_f32_e32 v232, v80, v234
	v_add_f32_e32 v232, v233, v232
	v_add_f32_e32 v80, v84, v232
	s_waitcnt lgkmcnt(2)
	v_mul_f32_e32 v237, v79, v237
	v_fmac_f32_e32 v237, v78, v236
	v_mul_f32_e32 v236, v77, v239
	v_fmac_f32_e32 v236, v76, v238
	v_add_f32_e32 v236, v237, v236
	v_add_f32_e32 v76, v80, v236
	s_waitcnt lgkmcnt(1)
	v_mul_f32_e32 v241, v75, v241
	v_fmac_f32_e32 v241, v74, v240
	v_mul_f32_e32 v240, v73, v243
	v_fmac_f32_e32 v240, v72, v242
	v_add_f32_e32 v240, v241, v240
	v_add_f32_e32 v72, v76, v240
	s_waitcnt lgkmcnt(0)
	v_mul_f32_e32 v65, v71, v65
	v_fmac_f32_e32 v65, v70, v64
	v_mul_f32_e32 v64, v69, v67
	v_fmac_f32_e32 v64, v68, v66
	v_add_f32_e32 v64, v65, v64
	s_waitcnt lgkmcnt(0)
	s_nop 1
	v_permlane32_swap_b32_e32 v111, v196
	v_add_f32_e32 v65, v111, v196
	v_add_f32_e32 v64, v72, v64
	s_waitcnt lgkmcnt(0)
	s_nop 1
	v_permlane32_swap_b32_e32 v188, v197
	v_add_f32_e32 v66, v188, v197
	s_waitcnt lgkmcnt(0)
	s_nop 1
	v_permlane32_swap_b32_e32 v189, v198
	v_add_f32_e32 v67, v189, v198
	s_waitcnt lgkmcnt(0)
	s_nop 1
	v_permlane32_swap_b32_e32 v190, v199
	v_add_f32_e32 v68, v190, v199
	s_waitcnt lgkmcnt(0)
	s_nop 1
	v_permlane32_swap_b32_e32 v191, v200
	v_add_f32_e32 v69, v191, v200
	s_waitcnt lgkmcnt(0)
	s_nop 1
	v_permlane32_swap_b32_e32 v193, v201
	v_add_f32_e32 v70, v193, v201
	s_waitcnt lgkmcnt(0)
	s_nop 1
	v_permlane32_swap_b32_e32 v194, v202
	v_add_f32_e32 v71, v194, v202
	s_waitcnt lgkmcnt(0)
	s_nop 1
	v_permlane32_swap_b32_e32 v195, v64
	v_add_f32_e32 v64, v195, v64
	s_waitcnt lgkmcnt(0)
	s_nop 1
	v_permlane16_swap_b32_e32 v65, v69
	v_add_f32_e32 v65, v65, v69
	s_waitcnt lgkmcnt(0)
	s_nop 1
	v_permlane16_swap_b32_e32 v66, v70
	v_add_f32_e32 v66, v66, v70
	s_waitcnt lgkmcnt(0)
	s_nop 1
	v_permlane16_swap_b32_e32 v67, v71
	v_add_f32_e32 v67, v67, v71
	s_waitcnt lgkmcnt(0)
	s_nop 1
	v_permlane16_swap_b32_e32 v68, v64
	v_add_f32_e32 v64, v68, v64
	v_cndmask_b32_e64 v68, v65, v67, s[10:11]
	v_cndmask_b32_e64 v65, v67, v65, s[10:11]
	s_nop 1
	v_mov_b32_dpp v67, v68 row_ror:8 row_mask:0xf bank_mask:0xf
	s_waitcnt lgkmcnt(0)
	v_add_f32_e32 v65, v65, v67
	v_cndmask_b32_e64 v67, v66, v64, s[10:11]
	v_cndmask_b32_e64 v64, v64, v66, s[10:11]
	s_nop 1
	v_mov_b32_dpp v66, v67 row_ror:8 row_mask:0xf bank_mask:0xf
	s_waitcnt lgkmcnt(0)
	v_add_f32_e32 v64, v64, v66
	v_cndmask_b32_e64 v66, v65, v64, s[12:13]
	v_cndmask_b32_e64 v64, v64, v65, s[12:13]
	ds_swizzle_b32 v65, v66 offset:swizzle(SWAP,4)
	s_waitcnt lgkmcnt(0)
	v_add_f32_e32 v64, v64, v65
	s_nop 1
	v_add_f32_dpp v64, v64, v64 quad_perm:[2,3,0,1] row_mask:0xf bank_mask:0xf bound_ctrl:1
	s_nop 1
	v_mov_b32_dpp v65, v64 quad_perm:[1,0,3,2] row_mask:0xf bank_mask:0xf bound_ctrl:1
	s_and_saveexec_b64 s[20:21], s[14:15]
	s_cbranch_execz .LBB0_82
	v_add_f32_e32 v65, v64, v65
	s_and_saveexec_b64 s[24:25], s[16:17]
	s_xor_b64 s[24:25], exec, s[24:25]
	s_cbranch_execz .LBB0_94
	s_and_saveexec_b64 s[26:27], s[6:7]
	s_xor_b64 s[26:27], exec, s[26:27]
	s_cbranch_execz .LBB0_91
	s_and_saveexec_b64 s[28:29], s[18:19]
	s_xor_b64 s[28:29], exec, s[28:29]
	s_cbranch_execz .LBB0_88
	v_mov_b32_e32 v64, v203
	v_add_f32_e32 v64, v65, v64

.LBB0_139:
	global_load_dword v1, v0, s[10:11] sc1
	s_waitcnt vmcnt(0)
	v_cmp_eq_u32_e32 vcc, 0, v1
	s_cbranch_vccnz .LBB0_141
	s_mov_b64 s[18:19], -1
	s_mov_b64 s[22:23], -1
	s_branch .LBB0_135
	s_nop 0
	s_nop 0
	s_nop 0
	s_nop 0
	s_nop 0
	s_nop 0
	s_nop 0
	s_nop 0
	s_nop 0
	s_nop 0
	s_nop 0
	s_nop 0
	s_nop 0
	s_nop 0
	s_nop 0
	s_nop 0
	s_nop 0
	s_nop 0
	s_nop 0
	s_nop 0
	s_nop 0
	s_nop 0
	s_nop 0
	s_nop 0
	s_nop 0
	s_nop 0
	s_nop 0
	s_nop 0
	s_nop 0
	s_nop 0
	s_nop 0
	s_nop 0
	s_nop 0
	s_nop 0
	s_nop 0
	s_nop 0
	s_nop 0
	s_nop 0
	s_nop 0
	s_nop 0
	s_nop 0
	s_nop 0
	s_nop 0
.LBB0_141:
	s_cmp_lt_u32 s3, 0x40001
	s_mov_b64 s[18:19], 0
	s_cselect_b64 s[20:21], -1, 0
	s_mov_b64 s[22:23], -1
	s_and_b64 vcc, exec, s[20:21]
	s_cbranch_vccnz .LBB0_138
	s_branch .LBB0_135
	s_nop 0
	s_nop 0
	s_nop 0

; template <int MODE, bool SB  > DI void norm_phase(const Params& P, const Frame& F, int L, const void* src_, const float* gain, bool combine) {
;     ...
;     for (int row = r_lo + F.wave; row < r_hi; row += NWAVES) {
;         f32x4 v[8];
; #pragma unroll
;         for (int j = 0; j < 8; ++j) { if constexpr (SB) v[j] = (f32x4){bflo(vb[j].x), bfhi(vb[j].x), bflo(vb[j].y), bfhi(vb[j].y)}; else v[j] = vn[j]; }
;         { const int rnx = (row + NWAVES < r_hi) ? row + NWAVES : row;
; #pragma unroll
;           for (int j = 0; j < 8; ++j) { if constexpr (SB) vb[j] = *(const u32x2*)(srcb + (size_t)rnx * D + 4 * F.lane + 256 * j); else vn[j] = *(const f32x4*)(src + (size_t)rnx * D + 4 * F.lane + 256 * j); } }
;         if (MODE == 3 && combine) {
;             const int* SLOT = (const int*)(ws + WS_SLOT); const float* TOPW = (const float*)(ws + WS_TOPW); const bf16* Y = (const bf16*)(ws + WS_T + T_YPERM);
;             const int s1 = SLOT[row * 2], s2 = SLOT[row * 2 + 1]; const float w1 = TOPW[row * 2], w2 = TOPW[row * 2 + 1];
;             u32x2 ya[8], yb[8];
; #pragma unroll
;             for (int j = 0; j < 8; ++j) { ya[j] = *(const u32x2*)(Y + (size_t)s1 * D + 4 * F.lane + 256 * j); yb[j] = *(const u32x2*)(Y + (size_t)s2 * D + 4 * F.lane + 256 * j); }
; #pragma unroll
;             for (int j = 0; j < 8; ++j) { const f32x4 y1 = (f32x4){bflo(ya[j].x), bfhi(ya[j].x), bflo(ya[j].y), bfhi(ya[j].y)}, y2 = (f32x4){bflo(yb[j].x), bfhi(yb[j].x), bflo(yb[j].y), bfhi(yb[j].y)};
;                 v[j] = v[j] + w1 * y1 + w2 * y2;
;                 const u32x2 hb = {pk2(v[j][0], v[j][1]), pk2(v[j][2], v[j][3])}; *(u32x2*)(const_cast<bf16*>(srcb) + (size_t)row * D + 4 * F.lane + 256 * j) = hb;
;                 v[j] = (f32x4){bflo(hb.x), bfhi(hb.x), bflo(hb.y), bfhi(hb.y)}; }
;         }
;         float ss = 0.f;
; #pragma unroll
;         for (int j = 0; j < 8; ++j) ss += (v[j][0] * v[j][0] + v[j][1] * v[j][1]) + (v[j][2] * v[j][2] + v[j][3] * v[j][3]);
;         const float rstd = 1.0f / sqrtf(wave_sum(ss) * (1.0f / D) + EPS);
; #pragma unroll
;         for (int j = 0; j < 8; ++j) v[j] = v[j] * rstd * g[j];
;         if (MODE == 4) {
; #pragma unroll
;             for (int j = 0; j < 8; ++j) *(f32x4*)(P.out + (size_t)row * D + 4 * F.lane + 256 * j) = v[j];
;         } else if (MODE == 0 || MODE == 2 || (MODE == 3 && L == 1)) {
.LBB0_1308:
	s_add_i32 s6, s10, 8
	s_waitcnt vmcnt(3)
	v_lshlrev_b32_e32 v42, 16, v40
	v_and_b32_e32 v43, 0xffff0000, v40
	v_lshlrev_b32_e32 v40, 16, v62
	v_and_b32_e32 v71, 0xffff0000, v62
	v_lshlrev_b32_e32 v46, 16, v63
	v_and_b32_e32 v47, 0xffff0000, v63
	v_lshlrev_b32_e32 v38, 16, v36
	v_and_b32_e32 v39, 0xffff0000, v36
	v_lshlrev_b32_e32 v36, 16, v60
	v_and_b32_e32 v89, 0xffff0000, v60
	v_lshlrev_b32_e32 v44, 16, v61
	v_and_b32_e32 v45, 0xffff0000, v61
	s_waitcnt vmcnt(0)
	v_and_b32_e32 v61, 0xffff0000, v58
	v_and_b32_e32 v60, 0xffff0000, v54
	v_and_b32_e32 v63, 0xffff0000, v59
	v_and_b32_e32 v62, 0xffff0000, v55
	s_cmp_lt_i32 s6, s3
	v_lshlrev_b32_e32 v49, 16, v58
	v_lshlrev_b32_e32 v48, 16, v54
	v_lshlrev_b32_e32 v51, 16, v59
	v_lshlrev_b32_e32 v50, 16, v55
	v_lshlrev_b32_e32 v65, 16, v53
	v_lshlrev_b32_e32 v64, 16, v52
	v_and_b32_e32 v53, 0xffff0000, v53
	v_and_b32_e32 v52, 0xffff0000, v52
	v_pk_mul_f32 v[72:73], v[60:61], v[60:61]
	v_pk_mul_f32 v[74:75], v[62:63], v[62:63]
	s_cselect_b64 s[4:5], -1, 0
	v_lshlrev_b32_e32 v54, 16, v41
	v_pk_mul_f32 v[76:77], v[52:53], v[52:53]
	v_pk_fma_f32 v[72:73], v[48:49], v[48:49], v[72:73]
	v_pk_fma_f32 v[74:75], v[50:51], v[50:51], v[74:75]
	s_and_b64 s[4:5], s[4:5], exec
	v_and_b32_e32 v55, 0xffff0000, v41
	v_lshlrev_b32_e32 v67, 16, v57
	v_lshlrev_b32_e32 v66, 16, v56
	v_and_b32_e32 v57, 0xffff0000, v57
	v_and_b32_e32 v56, 0xffff0000, v56
	v_lshlrev_b32_e32 v58, 16, v37
	v_mul_f32_e32 v41, v42, v42
	v_mul_f32_e32 v79, v43, v43
	v_mul_f32_e32 v80, v54, v54
	v_mov_b32_e32 v78, v40
	v_mov_b32_e32 v92, v49
	v_mov_b32_e32 v93, v61
	v_mov_b32_e32 v96, v64
	v_mov_b32_e32 v97, v52
	v_mov_b32_e32 v52, v65
	v_pk_fma_f32 v[64:65], v[64:65], v[64:65], v[76:77]
	v_mov_b32_e32 v49, v60
	v_pk_add_f32 v[60:61], v[72:73], v[74:75]
	s_cselect_b32 s14, s6, s10
	v_and_b32_e32 v59, 0xffff0000, v37
	v_pk_mul_f32 v[84:85], v[56:57], v[56:57]
	v_mul_f32_e32 v37, v38, v38
	v_mul_f32_e32 v87, v39, v39
	v_mul_f32_e32 v88, v58, v58
	v_mov_b32_e32 v86, v36
	v_mov_b32_e32 v94, v51
	v_mov_b32_e32 v95, v63
	v_pk_fma_f32 v[76:77], v[54:55], v[54:55], v[80:81] op_sel_hi:[1,1,0]
	v_pk_add_f32 v[78:79], v[40:41], v[78:79]
	v_mov_b32_e32 v51, v62
	v_pk_add_f32 v[62:63], v[64:65], v[64:65] op_sel_hi:[0,1]
	v_pk_add_f32 v[60:61], v[60:61], v[60:61] op_sel_hi:[0,1]
	s_ashr_i32 s15, s14, 31
	v_mul_f32_e32 v82, v40, v40
	v_mov_b32_e32 v98, v66
	v_mov_b32_e32 v99, v56
	v_mov_b32_e32 v56, v67
	v_pk_fma_f32 v[66:67], v[66:67], v[66:67], v[84:85]
	v_pk_fma_f32 v[80:81], v[58:59], v[58:59], v[88:89] op_sel_hi:[1,1,0]
	v_pk_add_f32 v[84:85], v[36:37], v[86:87]
	v_mul_f32_e32 v76, v71, v71
	v_mov_b32_e32 v83, v79
	v_mul_f32_e32 v62, v46, v46
	s_mov_b32 s10, s6
	v_mul_f32_e32 v60, v47, v47
	s_lshl_b64 s[6:7], s[14:15], 12
	v_mul_f32_e32 v90, v36, v36
	v_pk_add_f32 v[64:65], v[66:67], v[66:67] op_sel_hi:[0,1]
	v_mul_f32_e32 v80, v89, v89
	v_mov_b32_e32 v91, v85
	v_pk_add_f32 v[66:67], v[82:83], v[76:77]
	v_pk_add_f32 v[60:61], v[62:63], v[60:61]
	v_lshl_add_u64 v[74:75], v[32:33], 0, s[6:7]
	v_pk_add_f32 v[72:73], v[90:91], v[80:81]
	v_pk_add_f32 v[66:67], v[66:67], v[60:61]
	global_load_dwordx2 v[76:77], v[74:75], off
	global_load_dwordx2 v[78:79], v[74:75], off offset:512
	global_load_dwordx2 v[80:81], v[74:75], off offset:1024
	global_load_dwordx2 v[82:83], v[74:75], off offset:1536
	global_load_dwordx2 v[62:63], v[74:75], off offset:2048
	global_load_dwordx2 v[84:85], v[74:75], off offset:2560
	global_load_dwordx2 v[86:87], v[74:75], off offset:3072
	global_load_dwordx2 v[60:61], v[74:75], off offset:3584
	v_pk_add_f32 v[66:67], v[66:67], v[66:67] op_sel_hi:[0,1]
	v_mul_f32_e32 v64, v44, v44
	v_mul_f32_e32 v66, v45, v45
	v_pk_add_f32 v[64:65], v[64:65], v[66:67]
	v_mov_b32_e32 v41, v71
	v_pk_add_f32 v[64:65], v[72:73], v[64:65]
	v_mov_b32_e32 v100, 0
	v_add_f32_e32 v64, v64, v65
	v_mov_b32_e32 v37, v89
	v_mov_b32_e32 v101, 0
	v_add_f32_dpp v64, v64, v64 quad_perm:[1,0,3,2] row_mask:0xf bank_mask:0xf bound_ctrl:1
	v_mov_b32_e32 v102, 0
	v_mov_b32_e32 v103, 0
	v_add_f32_dpp v64, v64, v64 quad_perm:[2,3,0,1] row_mask:0xf bank_mask:0xf bound_ctrl:1
	ds_swizzle_b32 v65, v64 offset:swizzle(SWAP,4)
	v_mov_b32_e32 v104, 0
	v_mov_b32_e32 v105, 0
	v_mov_b32_e32 v106, 0
	v_mov_b32_e32 v107, 0
	s_waitcnt lgkmcnt(0)
	v_add_f32_e32 v64, v64, v65
	s_nop 1
	v_mov_b32_dpp v65, v64 row_ror:8 row_mask:0xf bank_mask:0xf
	s_waitcnt lgkmcnt(0)
	v_add_f32_e32 v64, v64, v65
	v_mov_b32_e32 v65, v64
	s_waitcnt lgkmcnt(0)
	s_nop 1
	v_permlane16_swap_b32_e32 v64, v65
	v_add_f32_e32 v64, v64, v65
	v_mov_b32_e32 v65, v64
	s_waitcnt lgkmcnt(0)
; DI unsigned pk4_fp8(float a, float b, float c, float d) { unsigned w = 0u; w = __builtin_amdgcn_cvt_pk_fp8_f32(a, b, w, false); w = __builtin_amdgcn_cvt_pk_fp8_f32(c, d, w, true); return w; }
; DI float wave_sum(float v) { v += shx<1>(v); v += shx<2>(v); v += shx<4>(v); v += shx<8>(v); v += shx<16>(v); v += shx<32>(v); return v; }
; template <int MODE, bool SB  > DI void norm_phase(const Params& P, const Frame& F, int L, const void* src_, const float* gain, bool combine) {
;     ...
;         const float rstd = 1.0f / sqrtf(wave_sum(ss) * (1.0f / D) + EPS);
; #pragma unroll
;         for (int j = 0; j < 8; ++j) v[j] = v[j] * rstd * g[j];
;         if (MODE == 4) {
; #pragma unroll
;             for (int j = 0; j < 8; ++j) *(f32x4*)(P.out + (size_t)row * D + 4 * F.lane + 256 * j) = v[j];
;         } else if (MODE == 0 || MODE == 2 || (MODE == 3 && L == 1)) {
;             unsigned* o4 = (unsigned*)((unsigned char*)HN + (size_t)row * D) + F.lane; const float hs = (float)(1 << LS_HN);
; #pragma unroll
;             for (int j = 0; j < 8; ++j) o4[64 * j] = pk4_fp8(v[j][0] * hs, v[j][1] * hs, v[j][2] * hs, v[j][3] * hs);
	s_nop 1
	v_permlane32_swap_b32_e32 v64, v65
	v_add_f32_e32 v64, v64, v65
	v_fmamk_f32 v64, v64, 0x3a000000, v69
	v_mul_f32_e32 v65, 0x4f800000, v64
	v_cmp_gt_f32_e32 vcc, s9, v64
	s_nop 1
	v_cndmask_b32_e32 v64, v64, v65, vcc
	v_sqrt_f32_e32 v65, v64
	s_nop 0
	v_add_u32_e32 v66, -1, v65
	v_add_u32_e32 v67, 1, v65
	v_fma_f32 v71, -v66, v65, v64
	v_fma_f32 v72, -v67, v65, v64
	v_cmp_ge_f32_e64 s[6:7], 0, v71
	s_nop 1
	v_cndmask_b32_e64 v65, v65, v66, s[6:7]
	v_cmp_lt_f32_e64 s[6:7], 0, v72
	s_nop 1
	v_cndmask_b32_e64 v65, v65, v67, s[6:7]
	v_mul_f32_e32 v66, 0x37800000, v65
	v_cndmask_b32_e32 v65, v65, v66, vcc
	v_cmp_class_f32_e32 vcc, v64, v70
	s_nop 1
	v_cndmask_b32_e32 v64, v65, v64, vcc
	v_div_scale_f32 v65, s[6:7], v64, v64, 1.0
	v_rcp_f32_e32 v67, v65
	v_div_scale_f32 v66, vcc, 1.0, v64, 1.0
	v_fma_f32 v71, -v65, v67, 1.0
	v_fmac_f32_e32 v67, v71, v67
	v_mul_f32_e32 v71, v66, v67
	v_fma_f32 v72, -v65, v71, v66
	v_fmac_f32_e32 v71, v72, v67
	v_fma_f32 v65, -v65, v71, v66
	v_div_fmas_f32 v65, v65, v67, v71
	v_div_fixup_f32 v64, v65, v64, 1.0
	v_pk_mul_f32 v[66:67], v[92:93], v[64:65] op_sel_hi:[1,0]
	v_pk_mul_f32 v[48:49], v[48:49], v[64:65] op_sel_hi:[1,0]
	v_pk_mul_f32 v[66:67], v[0:1], v[66:67]
	v_pk_mul_f32 v[72:73], v[94:95], v[64:65] op_sel_hi:[1,0]
	v_pk_mul_f32 v[74:75], v[64:65], v[96:97] op_sel_hi:[0,1]
	v_pk_mul_f32 v[48:49], v[4:5], v[48:49]
	v_mul_f32_e32 v66, 4.0, v66
	v_mul_f32_e32 v67, 4.0, v67
	v_pk_mul_f32 v[50:51], v[50:51], v[64:65] op_sel_hi:[1,0]
	v_pk_mul_f32 v[52:53], v[64:65], v[52:53] op_sel_hi:[0,1]
	v_pk_mul_f32 v[42:43], v[42:43], v[64:65] op_sel_hi:[1,0]
	v_pk_mul_f32 v[54:55], v[54:55], v[64:65] op_sel_hi:[1,0]
	v_pk_mul_f32 v[40:41], v[40:41], v[64:65] op_sel_hi:[1,0]
	v_pk_mul_f32 v[46:47], v[46:47], v[64:65] op_sel_hi:[1,0]
	v_pk_mul_f32 v[88:89], v[64:65], v[98:99] op_sel_hi:[0,1]
	v_pk_mul_f32 v[56:57], v[64:65], v[56:57] op_sel_hi:[0,1]
	v_pk_mul_f32 v[38:39], v[38:39], v[64:65] op_sel_hi:[1,0]
	v_pk_mul_f32 v[58:59], v[58:59], v[64:65] op_sel_hi:[1,0]
	v_pk_mul_f32 v[36:37], v[36:37], v[64:65] op_sel_hi:[1,0]
	v_pk_mul_f32 v[44:45], v[44:45], v[64:65] op_sel_hi:[1,0]
	v_pk_mul_f32 v[64:65], v[2:3], v[72:73]
	v_pk_mul_f32 v[72:73], v[8:9], v[74:75]
	v_mul_f32_e32 v48, 4.0, v48
	v_mul_f32_e32 v49, 4.0, v49
	v_cvt_pk_fp8_f32 v100, v66, v67
	v_pk_mul_f32 v[42:43], v[12:13], v[42:43]
	v_mul_f32_e32 v71, 4.0, v72
	v_mul_f32_e32 v72, 4.0, v73
	v_cvt_pk_fp8_f32 v101, v48, v49
	v_pk_mul_f32 v[40:41], v[16:17], v[40:41]
	v_pk_mul_f32 v[74:75], v[20:21], v[88:89]
	v_pk_mul_f32 v[38:39], v[24:25], v[38:39]
	v_pk_mul_f32 v[36:37], v[28:29], v[36:37]
	v_mul_f32_e32 v42, 4.0, v42
	v_mul_f32_e32 v43, 4.0, v43
	v_cvt_pk_fp8_f32 v102, v71, v72
	v_pk_mul_f32 v[50:51], v[6:7], v[50:51]
	v_mul_f32_e32 v64, 4.0, v64
	v_mul_f32_e32 v65, 4.0, v65
	v_mul_f32_e32 v40, 4.0, v40
	v_mul_f32_e32 v41, 4.0, v41
	v_mul_f32_e32 v73, 4.0, v74
	v_mul_f32_e32 v74, 4.0, v75
	v_mul_f32_e32 v38, 4.0, v38
	v_mul_f32_e32 v39, 4.0, v39
	v_mul_f32_e32 v36, 4.0, v36
	v_mul_f32_e32 v37, 4.0, v37
	v_cvt_pk_fp8_f32 v103, v42, v43
	v_pk_mul_f32 v[52:53], v[10:11], v[52:53]
	v_mul_f32_e32 v50, 4.0, v50
	v_mul_f32_e32 v51, 4.0, v51
	v_cvt_pk_fp8_f32 v104, v40, v41
	v_cvt_pk_fp8_f32 v105, v73, v74
	v_cvt_pk_fp8_f32 v106, v38, v39
	v_cvt_pk_fp8_f32 v107, v36, v37
	v_cvt_pk_fp8_f32 v100, v64, v65 op_sel:[0,0,1]
	v_pk_mul_f32 v[54:55], v[14:15], v[54:55]
	v_mul_f32_e32 v52, 4.0, v52
	v_mul_f32_e32 v53, 4.0, v53
	v_cvt_pk_fp8_f32 v101, v50, v51 op_sel:[0,0,1]
	v_pk_mul_f32 v[46:47], v[18:19], v[46:47]
	v_pk_mul_f32 v[56:57], v[22:23], v[56:57]
	v_pk_mul_f32 v[58:59], v[26:27], v[58:59]
	v_pk_mul_f32 v[44:45], v[30:31], v[44:45]
	v_mul_f32_e32 v54, 4.0, v54
	v_mul_f32_e32 v55, 4.0, v55
	v_cvt_pk_fp8_f32 v102, v52, v53 op_sel:[0,0,1]
	v_mul_f32_e32 v46, 4.0, v46
	v_mul_f32_e32 v47, 4.0, v47
	v_mul_f32_e32 v56, 4.0, v56
	v_mul_f32_e32 v57, 4.0, v57
	v_mul_f32_e32 v58, 4.0, v58
	v_mul_f32_e32 v59, 4.0, v59
	v_mul_f32_e32 v44, 4.0, v44
	v_mul_f32_e32 v45, 4.0, v45
	v_cvt_pk_fp8_f32 v103, v54, v55 op_sel:[0,0,1]
	v_cvt_pk_fp8_f32 v104, v46, v47 op_sel:[0,0,1]
	v_cvt_pk_fp8_f32 v105, v56, v57 op_sel:[0,0,1]
	v_cvt_pk_fp8_f32 v106, v58, v59 op_sel:[0,0,1]
	v_cvt_pk_fp8_f32 v107, v44, v45 op_sel:[0,0,1]
	global_store_dword v[34:35], v100, off
	global_store_dword v[34:35], v101, off offset:256
	global_store_dword v[34:35], v102, off offset:512
	global_store_dword v[34:35], v103, off offset:768
	global_store_dword v[34:35], v104, off offset:1024
	global_store_dword v[34:35], v105, off offset:1280
	global_store_dword v[34:35], v106, off offset:1536
	global_store_dword v[34:35], v107, off offset:1792
	v_lshl_add_u64 v[34:35], v[34:35], 0, s[12:13]
	s_waitcnt vmcnt(9)
	v_mov_b64_e32 v[36:37], v[86:87]
	v_mov_b64_e32 v[56:57], v[84:85]
	v_mov_b64_e32 v[40:41], v[82:83]
	v_mov_b64_e32 v[52:53], v[80:81]
	v_mov_b64_e32 v[54:55], v[78:79]
	v_mov_b64_e32 v[58:59], v[76:77]
	s_mov_b64 vcc, s[4:5]
	s_cbranch_vccnz .LBB0_1308

.LBB0_1354:
	s_cmp_lt_u32 s3, 0x40001
	s_mov_b64 s[22:23], 0
	s_cselect_b64 s[24:25], -1, 0
	s_mov_b64 s[26:27], -1
	s_and_b64 vcc, exec, s[24:25]
	s_cbranch_vccnz .LBB0_1351
	s_branch .LBB0_1348
	s_nop 0
	s_nop 0
	s_nop 0
	s_nop 0
	s_nop 0
	s_nop 0
	s_nop 0
	s_nop 0
	s_nop 0
	s_nop 0
	s_nop 0
	s_nop 0
	s_nop 0
	s_nop 0
	s_nop 0
	s_nop 0
	s_nop 0
	s_nop 0
	s_nop 0
	s_nop 0
	s_nop 0
	s_nop 0
	s_nop 0
	s_nop 0
	s_nop 0
	s_nop 0
	s_nop 0
	s_nop 0
	s_nop 0
	s_nop 0
	s_nop 0
	s_nop 0
	s_nop 0
	s_nop 0
	s_nop 0
	s_nop 0
	s_nop 0
	s_nop 0
	s_nop 0
	s_nop 0
	s_nop 0
	s_nop 0
	s_nop 0
	s_nop 0
	s_nop 0
	s_nop 0
	s_nop 0
	s_nop 0
	s_nop 0
	s_nop 0
	s_nop 0
	s_nop 0
	s_nop 0
	s_nop 0
	s_nop 0
	s_nop 0
	s_nop 0
	s_nop 0
	s_nop 0
	s_nop 0
	s_nop 0
.LBB0_1355:
	s_or_b64 exec, exec, s[18:19]
	s_and_b64 s[18:19], s[20:21], exec

; DI unsigned pk2(float lo, float hi) { const f32x2 v = {lo, hi}; return __builtin_bit_cast(unsigned, __builtin_convertvector(v, bf16x2_t)); }
; template <int MODE, bool SB  > DI void norm_phase(const Params& P, const Frame& F, int L, const void* src_, const float* gain, bool combine) {
;     ...
;     for (int row = r_lo + F.wave; row < r_hi; row += NWAVES) {
;         f32x4 v[8];
; #pragma unroll
;         for (int j = 0; j < 8; ++j) { if constexpr (SB) v[j] = (f32x4){bflo(vb[j].x), bfhi(vb[j].x), bflo(vb[j].y), bfhi(vb[j].y)}; else v[j] = vn[j]; }
;         { const int rnx = (row + NWAVES < r_hi) ? row + NWAVES : row;
; #pragma unroll
;           for (int j = 0; j < 8; ++j) { if constexpr (SB) vb[j] = *(const u32x2*)(srcb + (size_t)rnx * D + 4 * F.lane + 256 * j); else vn[j] = *(const f32x4*)(src + (size_t)rnx * D + 4 * F.lane + 256 * j); } }
;         if (MODE == 3 && combine) {
;             const int* SLOT = (const int*)(ws + WS_SLOT); const float* TOPW = (const float*)(ws + WS_TOPW); const bf16* Y = (const bf16*)(ws + WS_T + T_YPERM);
;             const int s1 = SLOT[row * 2], s2 = SLOT[row * 2 + 1]; const float w1 = TOPW[row * 2], w2 = TOPW[row * 2 + 1];
;             u32x2 ya[8], yb[8];
; #pragma unroll
;             for (int j = 0; j < 8; ++j) { ya[j] = *(const u32x2*)(Y + (size_t)s1 * D + 4 * F.lane + 256 * j); yb[j] = *(const u32x2*)(Y + (size_t)s2 * D + 4 * F.lane + 256 * j); }
; #pragma unroll
;             for (int j = 0; j < 8; ++j) { const f32x4 y1 = (f32x4){bflo(ya[j].x), bfhi(ya[j].x), bflo(ya[j].y), bfhi(ya[j].y)}, y2 = (f32x4){bflo(yb[j].x), bfhi(yb[j].x), bflo(yb[j].y), bfhi(yb[j].y)};
;                 v[j] = v[j] + w1 * y1 + w2 * y2;
;                 const u32x2 hb = {pk2(v[j][0], v[j][1]), pk2(v[j][2], v[j][3])}; *(u32x2*)(const_cast<bf16*>(srcb) + (size_t)row * D + 4 * F.lane + 256 * j) = hb;
;                 v[j] = (f32x4){bflo(hb.x), bfhi(hb.x), bflo(hb.y), bfhi(hb.y)}; }
;         }
;         float ss = 0.f;
; #pragma unroll
;         for (int j = 0; j < 8; ++j) ss += (v[j][0] * v[j][0] + v[j][1] * v[j][1]) + (v[j][2] * v[j][2] + v[j][3] * v[j][3]);
;         const float rstd = 1.0f / sqrtf(wave_sum(ss) * (1.0f / D) + EPS);
; #pragma unroll
;         for (int j = 0; j < 8; ++j) v[j] = v[j] * rstd * g[j];
.LBB0_1648:
	s_waitcnt vmcnt(0)
	v_and_b32_e32 v75, 0xffff0000, v50
	v_and_b32_e32 v77, 0xffff0000, v51
	v_lshlrev_b32_e32 v65, 16, v48
	v_and_b32_e32 v69, 0xffff0000, v48
	v_lshlrev_b32_e32 v74, 16, v50
	v_lshlrev_b32_e32 v76, 16, v51
	v_mul_f32_e32 v48, v77, v77
	v_lshlrev_b32_e32 v78, 16, v52
	v_and_b32_e32 v81, 0xffff0000, v53
	v_and_b32_e32 v80, 0xffff0000, v52
	v_mul_f32_e32 v52, v75, v75
	v_lshlrev_b32_e32 v72, 16, v49
	v_and_b32_e32 v73, 0xffff0000, v49
	v_pk_fma_f32 v[48:49], v[76:77], v[76:77], v[48:49] op_sel_hi:[1,1,0]
	v_lshlrev_b32_e32 v79, 16, v53
	v_pk_mul_f32 v[50:51], v[80:81], v[80:81]
	v_pk_fma_f32 v[52:53], v[74:75], v[74:75], v[52:53] op_sel_hi:[1,1,0]
	v_pk_fma_f32 v[50:51], v[78:79], v[78:79], v[50:51]
	v_lshlrev_b32_e32 v82, 16, v54
	v_and_b32_e32 v83, 0xffff0000, v54
	v_lshlrev_b32_e32 v84, 16, v55
	v_and_b32_e32 v85, 0xffff0000, v55
	v_mov_b32_e32 v64, v52
	v_mov_b32_e32 v54, v48
	v_mov_b32_e32 v55, v65
	v_mul_f32_e32 v47, v69, v69
	v_pk_add_f32 v[48:49], v[52:53], v[48:49]
	v_pk_mul_f32 v[52:53], v[64:65], v[54:55]
	v_pk_add_f32 v[50:51], v[50:51], v[50:51] op_sel:[0,1] op_sel_hi:[1,0]
	v_mov_b32_e32 v49, v53
	v_mov_b32_e32 v51, v47
	v_pk_add_f32 v[48:49], v[48:49], v[50:51]
	v_mul_f32_e32 v50, v83, v83
	v_mul_f32_e32 v52, v85, v85
	v_lshlrev_b32_e32 v97, 16, v56
	v_and_b32_e32 v71, 0xffff0000, v56
	v_lshlrev_b32_e32 v66, 16, v57
	v_and_b32_e32 v67, 0xffff0000, v57
	v_mul_f32_e32 v56, v72, v72
	v_mul_f32_e32 v57, v73, v73
	v_pk_fma_f32 v[50:51], v[82:83], v[82:83], v[50:51] op_sel_hi:[1,1,0]
	v_pk_fma_f32 v[52:53], v[84:85], v[84:85], v[52:53] op_sel_hi:[1,1,0]
	v_mov_b32_e32 v51, v56
	v_mov_b32_e32 v53, v57
	v_pk_add_f32 v[50:51], v[50:51], v[52:53]
	v_and_b32_e32 v173, 0xffff0000, v59
	v_and_b32_e32 v172, 0xffff0000, v58
	v_pk_add_f32 v[48:49], v[48:49], v[50:51]
	v_lshlrev_b32_e32 v171, 16, v59
	v_lshlrev_b32_e32 v170, 16, v58
	v_pk_mul_f32 v[50:51], v[172:173], v[172:173]
	v_and_b32_e32 v177, 0xffff0000, v61
	v_pk_fma_f32 v[50:51], v[170:171], v[170:171], v[50:51]
	v_and_b32_e32 v176, 0xffff0000, v60
	v_pk_add_f32 v[50:51], v[50:51], v[50:51] op_sel:[0,1] op_sel_hi:[1,0]
	v_pk_add_f32 v[48:49], v[48:49], v[48:49] op_sel:[0,1] op_sel_hi:[1,0]
	v_lshlrev_b32_e32 v175, 16, v61
	v_lshlrev_b32_e32 v174, 16, v60
	v_pk_mul_f32 v[52:53], v[176:177], v[176:177]
	v_mov_b32_e32 v96, v48
	v_mov_b32_e32 v54, v50
	v_mov_b32_e32 v55, v97
	v_pk_fma_f32 v[52:53], v[174:175], v[174:175], v[52:53]
	v_pk_add_f32 v[48:49], v[48:49], v[50:51]
	v_pk_mul_f32 v[50:51], v[96:97], v[54:55]
	v_mul_f32_e32 v47, v71, v71
	v_mov_b32_e32 v49, v51
	v_pk_add_f32 v[50:51], v[52:53], v[52:53] op_sel:[0,1] op_sel_hi:[1,0]
	v_and_b32_e32 v179, 0xffff0000, v62
	v_and_b32_e32 v181, 0xffff0000, v63
	v_mov_b32_e32 v51, v47
	v_lshlrev_b32_e32 v178, 16, v62
	v_lshlrev_b32_e32 v180, 16, v63
	v_pk_add_f32 v[48:49], v[48:49], v[50:51]
	v_mul_f32_e32 v50, v179, v179
	v_mul_f32_e32 v52, v181, v181
	v_mul_f32_e32 v56, v66, v66
	v_mul_f32_e32 v57, v67, v67
	v_pk_fma_f32 v[50:51], v[178:179], v[178:179], v[50:51] op_sel_hi:[1,1,0]
	v_pk_fma_f32 v[52:53], v[180:181], v[180:181], v[52:53] op_sel_hi:[1,1,0]
	v_mov_b32_e32 v51, v56
	v_mov_b32_e32 v53, v57
	v_pk_add_f32 v[50:51], v[50:51], v[52:53]
	s_mov_b32 s20, s0
	v_pk_add_f32 v[48:49], v[48:49], v[50:51]
	s_add_i32 s0, s0, 8
	v_add_f32_e32 v47, v48, v49
	s_cmp_ge_i32 s0, s3
	s_cselect_b64 s[22:23], -1, 0
	v_add_f32_dpp v47, v47, v47 quad_perm:[1,0,3,2] row_mask:0xf bank_mask:0xf bound_ctrl:1
	s_cmp_lt_i32 s0, s3
	s_cselect_b32 s20, s0, s20
	v_add_f32_dpp v47, v47, v47 quad_perm:[2,3,0,1] row_mask:0xf bank_mask:0xf bound_ctrl:1
	ds_swizzle_b32 v48, v47 offset:swizzle(SWAP,4)
	s_ashr_i32 s21, s20, 31
	s_lshl_b64 s[20:21], s[20:21], 12
	v_lshl_add_u64 v[56:57], v[32:33], 0, s[20:21]
	s_mov_b32 s20, 0xf800000
	s_waitcnt lgkmcnt(0)
	v_add_f32_e32 v47, v47, v48
	s_nop 1
	v_mov_b32_dpp v48, v47 row_ror:8 row_mask:0xf bank_mask:0xf
	s_waitcnt lgkmcnt(0)
	v_add_f32_e32 v47, v47, v48
	v_mov_b32_e32 v48, v47
	s_waitcnt lgkmcnt(0)
	s_nop 1
	v_permlane16_swap_b32_e32 v47, v48
	v_add_f32_e32 v47, v47, v48
	v_mov_b32_e32 v48, v47
	s_waitcnt lgkmcnt(0)
	s_nop 1
	v_permlane32_swap_b32_e32 v47, v48
	v_add_f32_e32 v47, v47, v48
	v_fmamk_f32 v47, v47, 0x3a000000, v164
	v_mul_f32_e32 v48, 0x4f800000, v47
	v_cmp_gt_f32_e32 vcc, s20, v47
	s_nop 1
	v_cndmask_b32_e32 v47, v47, v48, vcc
	v_sqrt_f32_e32 v58, v47
	global_load_dwordx2 v[50:51], v[56:57], off
	global_load_dwordx2 v[52:53], v[56:57], off offset:512
	global_load_dwordx2 v[54:55], v[56:57], off offset:1024
	global_load_dwordx2 v[48:49], v[56:57], off offset:1536
	v_add_u32_e32 v59, -1, v58
	v_fma_f32 v60, -v59, v58, v47
	v_cmp_ge_f32_e64 s[20:21], 0, v60
	v_add_u32_e32 v60, 1, v58
	s_nop 0
	v_cndmask_b32_e64 v59, v58, v59, s[20:21]
	v_fma_f32 v58, -v60, v58, v47
	v_cmp_lt_f32_e64 s[20:21], 0, v58
	s_nop 1
	v_cndmask_b32_e64 v58, v59, v60, s[20:21]
	v_mul_f32_e32 v59, 0x37800000, v58
	v_cndmask_b32_e32 v58, v58, v59, vcc
	v_cmp_class_f32_e32 vcc, v47, v165
	s_nop 1
	v_cndmask_b32_e32 v47, v58, v47, vcc
	v_div_scale_f32 v64, s[20:21], v47, v47, 1.0
	v_rcp_f32_e32 v68, v64
	s_mov_b32 s20, 0x3d600000
	global_load_dwordx2 v[58:59], v[56:57], off offset:2048
	global_load_dwordx2 v[60:61], v[56:57], off offset:2560
	global_load_dwordx2 v[62:63], v[56:57], off offset:3072
	s_nop 0
	global_load_dwordx2 v[56:57], v[56:57], off offset:3584
	v_fma_f32 v70, -v64, v68, 1.0
	v_fmac_f32_e32 v68, v70, v68
	v_div_scale_f32 v70, vcc, 1.0, v47, 1.0
	v_mul_f32_e32 v86, v70, v68
	v_fma_f32 v87, -v64, v86, v70
	v_fmac_f32_e32 v86, v87, v68
	v_fma_f32 v64, -v64, v86, v70
	v_div_fmas_f32 v64, v64, v68, v86
; #define LAS __attribute__((address_space(3)))
; DI unsigned pk2(float lo, float hi) { const f32x2 v = {lo, hi}; return __builtin_bit_cast(unsigned, __builtin_convertvector(v, bf16x2_t)); }
; DI unsigned pk4_fp8(float a, float b, float c, float d) { unsigned w = 0u; w = __builtin_amdgcn_cvt_pk_fp8_f32(a, b, w, false); w = __builtin_amdgcn_cvt_pk_fp8_f32(c, d, w, true); return w; }
; template <int MODE, bool SB  > DI void norm_phase(const Params& P, const Frame& F, int L, const void* src_, const float* gain, bool combine) {
;     ...
;         for (int j = 0; j < 8; ++j) v[j] = v[j] * rstd * g[j];
;         if (MODE == 4) {
; #pragma unroll
;             for (int j = 0; j < 8; ++j) *(f32x4*)(P.out + (size_t)row * D + 4 * F.lane + 256 * j) = v[j];
;         } else if (MODE == 0 || MODE == 2 || (MODE == 3 && L == 1)) {
;             unsigned* o4 = (unsigned*)((unsigned char*)HN + (size_t)row * D) + F.lane; const float hs = (float)(1 << LS_HN);
; #pragma unroll
;             for (int j = 0; j < 8; ++j) o4[64 * j] = pk4_fp8(v[j][0] * hs, v[j][1] * hs, v[j][2] * hs, v[j][3] * hs);
;         } else {
;             unsigned long long* o8 = (unsigned long long*)(HN + (size_t)row * D) + F.lane;
; #pragma unroll
;             for (int j = 0; j < 8; ++j) o8[64 * j] = (unsigned long long)pk2(v[j][0], v[j][1]) | ((unsigned long long)pk2(v[j][2], v[j][3]) << 32);
;         }
;         if (MODE == 1) {
;             float s[16];
; #pragma unroll
;             for (int q = 0; q < 16; ++q) { float t = 0.f;
; #pragma unroll
;                 for (int j = 0; j < 8; ++j) { const f32x4 w = *(const LAS f32x4*)(F.lds + (size_t)(q * D + 256 * j + 4 * F.lane) * 4); t += (v[j][0] * w[0] + v[j][1] * w[1]) + (v[j][2] * w[2] + v[j][3] * w[3]); }
;                 s[q] = t; if ((q & 3) == 3) asm volatile("" ::: "memory"); }
	v_div_fixup_f32 v96, v64, v47, 1.0
	v_pk_mul_f32 v[74:75], v[96:97], v[74:75] op_sel_hi:[0,1]
	v_mov_b32_e32 v68, v65
	v_pk_mul_f32 v[76:77], v[96:97], v[76:77] op_sel_hi:[0,1]
	v_pk_mul_f32 v[92:93], v[8:9], v[74:75]
	v_mov_b32_e32 v75, v80
	v_mov_b32_e32 v80, v79
	v_pk_mul_f32 v[64:65], v[68:69], v[96:97] op_sel_hi:[1,0]
	v_pk_mul_f32 v[90:91], v[10:11], v[76:77]
	v_mov_b32_e32 v74, v78
	v_pk_mul_f32 v[76:77], v[96:97], v[80:81] op_sel_hi:[0,1]
	v_pk_mul_f32 v[86:87], v[12:13], v[64:65]
	v_mov_b32_e32 v64, v170
	v_mov_b32_e32 v65, v172
	v_pk_mul_f32 v[74:75], v[96:97], v[74:75] op_sel_hi:[0,1]
	v_pk_mul_f32 v[88:89], v[2:3], v[76:77]
	v_pk_mul_f32 v[76:77], v[96:97], v[84:85] op_sel_hi:[0,1]
	v_pk_mul_f32 v[68:69], v[72:73], v[96:97] op_sel_hi:[1,0]
	v_pk_mul_f32 v[64:65], v[96:97], v[64:65] op_sel_hi:[0,1]
	v_mov_b32_e32 v172, v171
	v_pk_mul_f32 v[94:95], v[0:1], v[74:75]
	v_pk_mul_f32 v[74:75], v[96:97], v[82:83] op_sel_hi:[0,1]
	v_pk_mul_f32 v[82:83], v[6:7], v[76:77]
	v_pk_mul_f32 v[78:79], v[14:15], v[68:69]
	v_pk_mul_f32 v[68:69], v[96:97], v[172:173] op_sel_hi:[0,1]
	v_pk_mul_f32 v[76:77], v[16:17], v[64:65]
	v_mov_b32_e32 v64, v174
	v_mov_b32_e32 v65, v176
	v_mov_b32_e32 v176, v175
	v_pk_mul_f32 v[84:85], v[4:5], v[74:75]
	v_pk_mul_f32 v[74:75], v[18:19], v[68:69]
	v_pk_mul_f32 v[64:65], v[96:97], v[64:65] op_sel_hi:[0,1]
	v_pk_mul_f32 v[68:69], v[96:97], v[176:177] op_sel_hi:[0,1]
	v_mov_b32_e32 v70, v97
	v_pk_mul_f32 v[72:73], v[22:23], v[68:69]
	v_pk_mul_f32 v[80:81], v[20:21], v[64:65]
	v_pk_mul_f32 v[68:69], v[96:97], v[178:179] op_sel_hi:[0,1]
	v_pk_mul_f32 v[64:65], v[96:97], v[180:181] op_sel_hi:[0,1]
	v_pk_mul_f32 v[70:71], v[70:71], v[96:97] op_sel_hi:[1,0]
	v_pk_mul_f32 v[66:67], v[66:67], v[96:97] op_sel_hi:[1,0]
	v_lshl_add_u64 v[96:97], s[54:55], 0, v[44:45]
	v_add_co_u32_e32 v96, vcc, s20, v96
	v_cvt_pk_bf16_f32 v170, v92, v93
	v_cvt_pk_bf16_f32 v171, v90, v91
	v_addc_co_u32_e32 v97, vcc, 0, v97, vcc
	global_store_dwordx2 v[96:97], v[170:171], off
	v_cvt_pk_bf16_f32 v170, v94, v95
	v_cvt_pk_bf16_f32 v171, v88, v89
	global_store_dwordx2 v[96:97], v[170:171], off offset:512
	v_cvt_pk_bf16_f32 v170, v84, v85
	v_cvt_pk_bf16_f32 v171, v82, v83
	global_store_dwordx2 v[96:97], v[170:171], off offset:1024
	v_cvt_pk_bf16_f32 v170, v86, v87
	v_cvt_pk_bf16_f32 v171, v78, v79
	global_store_dwordx2 v[96:97], v[170:171], off offset:1536
	v_cvt_pk_bf16_f32 v170, v76, v77
	v_cvt_pk_bf16_f32 v171, v74, v75
	v_pk_mul_f32 v[64:65], v[26:27], v[64:65]
	v_pk_mul_f32 v[68:69], v[24:25], v[68:69]
	global_store_dwordx2 v[96:97], v[170:171], off offset:2048
	v_cvt_pk_bf16_f32 v170, v80, v81
	v_cvt_pk_bf16_f32 v171, v72, v73
	global_store_dwordx2 v[96:97], v[170:171], off offset:2560
	v_cvt_pk_bf16_f32 v170, v68, v69
	v_cvt_pk_bf16_f32 v171, v64, v65
	global_store_dwordx2 v[96:97], v[170:171], off offset:3072
	ds_read_b128 v[196:199], v99
	ds_read_b128 v[200:203], v99 offset:1024
	ds_read_b128 v[204:207], v99 offset:2048
	ds_read_b128 v[208:211], v99 offset:3072
	ds_read_b128 v[212:215], v99 offset:4096
	ds_read_b128 v[216:219], v99 offset:5120
	ds_read_b128 v[220:223], v99 offset:6144
	ds_read_b128 v[224:227], v99 offset:7168
	v_pk_mul_f32 v[66:67], v[30:31], v[66:67]
	v_pk_mul_f32 v[70:71], v[28:29], v[70:71]
	v_cvt_pk_bf16_f32 v175, v66, v67
	v_cvt_pk_bf16_f32 v174, v70, v71
	global_store_dwordx2 v[96:97], v[174:175], off offset:3584
	s_waitcnt lgkmcnt(7)
	v_mul_f32_e32 v47, v197, v93
	v_mul_f32_e32 v96, v199, v91
	v_fmac_f32_e32 v47, v196, v92
	v_fmac_f32_e32 v96, v198, v90
	ds_read_b128 v[196:199], v99 offset:8192
	v_add_f32_e32 v47, v47, v96
	s_waitcnt lgkmcnt(7)
	v_mul_f32_e32 v96, v95, v201
	v_mul_f32_e32 v97, v89, v203
	v_fmac_f32_e32 v96, v94, v200
	v_fmac_f32_e32 v97, v88, v202
	ds_read_b128 v[200:203], v99 offset:9216
	v_add_f32_e32 v47, 0, v47
	v_add_f32_e32 v96, v96, v97
	v_add_f32_e32 v47, v96, v47
	s_waitcnt lgkmcnt(7)
	v_mul_f32_e32 v96, v85, v205
	v_mul_f32_e32 v97, v83, v207
	v_fmac_f32_e32 v96, v84, v204
	v_fmac_f32_e32 v97, v82, v206
	ds_read_b128 v[204:207], v99 offset:10240
	v_add_f32_e32 v96, v96, v97
	v_add_f32_e32 v47, v96, v47
	s_waitcnt lgkmcnt(7)
	v_mul_f32_e32 v96, v87, v209
	v_mul_f32_e32 v97, v79, v211
	v_fmac_f32_e32 v96, v86, v208
	v_fmac_f32_e32 v97, v78, v210
	ds_read_b128 v[208:211], v99 offset:11264
	v_add_f32_e32 v96, v96, v97
	v_add_f32_e32 v47, v96, v47
	s_waitcnt lgkmcnt(7)
	v_mul_f32_e32 v96, v77, v213
	v_mul_f32_e32 v97, v75, v215
	v_fmac_f32_e32 v96, v76, v212
	v_fmac_f32_e32 v97, v74, v214
	ds_read_b128 v[212:215], v99 offset:12288
	v_add_f32_e32 v96, v96, v97
	v_add_f32_e32 v47, v96, v47
	s_waitcnt lgkmcnt(7)
	v_mul_f32_e32 v96, v81, v217
	v_mul_f32_e32 v97, v73, v219
	v_fmac_f32_e32 v96, v80, v216
	v_fmac_f32_e32 v97, v72, v218
	ds_read_b128 v[216:219], v99 offset:13312
	v_add_f32_e32 v96, v96, v97
	v_add_f32_e32 v47, v96, v47
	s_waitcnt lgkmcnt(7)
	v_mul_f32_e32 v96, v69, v221
	v_mul_f32_e32 v97, v65, v223
	v_fmac_f32_e32 v96, v68, v220
	v_fmac_f32_e32 v97, v64, v222
	ds_read_b128 v[220:223], v99 offset:14336
	v_add_f32_e32 v96, v96, v97
	v_add_f32_e32 v47, v96, v47
	s_waitcnt lgkmcnt(7)
	v_mul_f32_e32 v96, v71, v225
	v_mul_f32_e32 v97, v67, v227
	v_fmac_f32_e32 v96, v70, v224
	v_fmac_f32_e32 v97, v66, v226
	ds_read_b128 v[224:227], v99 offset:15360
	v_add_f32_e32 v96, v96, v97
	v_add_f32_e32 v47, v96, v47
	s_waitcnt lgkmcnt(7)
	v_mul_f32_e32 v96, v93, v197
	v_mul_f32_e32 v97, v91, v199
	v_fmac_f32_e32 v96, v92, v196
	v_fmac_f32_e32 v97, v90, v198
	ds_read_b128 v[196:199], v99 offset:16384
	v_add_f32_e32 v96, v96, v97
	s_waitcnt lgkmcnt(7)
; #define LAS __attribute__((address_space(3)))
; template <int MODE, bool SB  > DI void norm_phase(const Params& P, const Frame& F, int L, const void* src_, const float* gain, bool combine) {
;     ...
;         if (MODE == 1) {
;             float s[16];
; #pragma unroll
;             for (int q = 0; q < 16; ++q) { float t = 0.f;
; #pragma unroll
;                 for (int j = 0; j < 8; ++j) { const f32x4 w = *(const LAS f32x4*)(F.lds + (size_t)(q * D + 256 * j + 4 * F.lane) * 4); t += (v[j][0] * w[0] + v[j][1] * w[1]) + (v[j][2] * w[2] + v[j][3] * w[3]); }
;                 s[q] = t; if ((q & 3) == 3) asm volatile("" ::: "memory"); }
	v_mul_f32_e32 v97, v95, v201
	v_fmac_f32_e32 v97, v94, v200
	v_mul_f32_e32 v174, v89, v203
	v_fmac_f32_e32 v174, v88, v202
	ds_read_b128 v[200:203], v99 offset:17408
	v_add_f32_e32 v96, 0, v96
	v_add_f32_e32 v97, v97, v174
	v_add_f32_e32 v96, v96, v97
	s_waitcnt lgkmcnt(7)
	v_mul_f32_e32 v97, v85, v205
	v_fmac_f32_e32 v97, v84, v204
	v_mul_f32_e32 v170, v83, v207
	v_fmac_f32_e32 v170, v82, v206
	ds_read_b128 v[204:207], v99 offset:18432
	v_add_f32_e32 v97, v97, v170
	v_add_f32_e32 v96, v96, v97
	s_waitcnt lgkmcnt(7)
	v_mul_f32_e32 v97, v87, v209
	v_fmac_f32_e32 v97, v86, v208
	v_mul_f32_e32 v174, v79, v211
	v_fmac_f32_e32 v174, v78, v210
	ds_read_b128 v[208:211], v99 offset:19456
	v_add_f32_e32 v97, v97, v174
	v_add_f32_e32 v96, v96, v97
	s_waitcnt lgkmcnt(7)
	v_mul_f32_e32 v97, v77, v213
	v_fmac_f32_e32 v97, v76, v212
	v_mul_f32_e32 v170, v75, v215
	v_fmac_f32_e32 v170, v74, v214
	ds_read_b128 v[212:215], v99 offset:20480
	v_add_f32_e32 v97, v97, v170
	v_add_f32_e32 v96, v96, v97
	s_waitcnt lgkmcnt(7)
	v_mul_f32_e32 v97, v81, v217
	v_fmac_f32_e32 v97, v80, v216
	v_mul_f32_e32 v174, v73, v219
	v_fmac_f32_e32 v174, v72, v218
	ds_read_b128 v[216:219], v99 offset:21504
	v_add_f32_e32 v97, v97, v174
	v_add_f32_e32 v96, v96, v97
	s_waitcnt lgkmcnt(7)
	v_mul_f32_e32 v97, v69, v221
	v_fmac_f32_e32 v97, v68, v220
	v_mul_f32_e32 v170, v65, v223
	v_fmac_f32_e32 v170, v64, v222
	ds_read_b128 v[220:223], v99 offset:22528
	v_add_f32_e32 v97, v97, v170
	v_add_f32_e32 v96, v96, v97
	s_waitcnt lgkmcnt(7)
	v_mul_f32_e32 v97, v71, v225
	v_fmac_f32_e32 v97, v70, v224
	v_mul_f32_e32 v174, v67, v227
	v_fmac_f32_e32 v174, v66, v226
	ds_read_b128 v[224:227], v99 offset:23552
	v_add_f32_e32 v97, v97, v174
	v_add_f32_e32 v96, v96, v97
	s_waitcnt lgkmcnt(7)
	v_mul_f32_e32 v97, v93, v197
	v_fmac_f32_e32 v97, v92, v196
	v_mul_f32_e32 v170, v91, v199
	v_fmac_f32_e32 v170, v90, v198
	ds_read_b128 v[196:199], v99 offset:24576
	s_waitcnt lgkmcnt(7)
	v_mul_f32_e32 v175, v95, v201
	v_add_f32_e32 v97, v97, v170
	v_fmac_f32_e32 v175, v94, v200
	v_mul_f32_e32 v174, v89, v203
	v_fmac_f32_e32 v174, v88, v202
	ds_read_b128 v[200:203], v99 offset:25600
	v_add_f32_e32 v97, 0, v97
	v_add_f32_e32 v174, v175, v174
	v_add_f32_e32 v97, v97, v174
	s_waitcnt lgkmcnt(7)
	v_mul_f32_e32 v171, v85, v205
	v_fmac_f32_e32 v171, v84, v204
	v_mul_f32_e32 v170, v83, v207
	v_fmac_f32_e32 v170, v82, v206
	ds_read_b128 v[204:207], v99 offset:26624
	v_add_f32_e32 v170, v171, v170
	s_waitcnt lgkmcnt(7)
	v_mul_f32_e32 v175, v87, v209
	v_add_f32_e32 v97, v97, v170
	v_fmac_f32_e32 v175, v86, v208
	v_mul_f32_e32 v174, v79, v211
	v_fmac_f32_e32 v174, v78, v210
	ds_read_b128 v[208:211], v99 offset:27648
	v_add_f32_e32 v174, v175, v174
	v_add_f32_e32 v97, v97, v174
	s_waitcnt lgkmcnt(7)
	v_mul_f32_e32 v171, v77, v213
	v_fmac_f32_e32 v171, v76, v212
	v_mul_f32_e32 v170, v75, v215
	v_fmac_f32_e32 v170, v74, v214
	ds_read_b128 v[212:215], v99 offset:28672
	v_add_f32_e32 v170, v171, v170
	s_waitcnt lgkmcnt(7)
	v_mul_f32_e32 v175, v81, v217
	v_add_f32_e32 v97, v97, v170
	v_fmac_f32_e32 v175, v80, v216
	v_mul_f32_e32 v174, v73, v219
	v_fmac_f32_e32 v174, v72, v218
	ds_read_b128 v[216:219], v99 offset:29696
	v_add_f32_e32 v174, v175, v174
	v_add_f32_e32 v97, v97, v174
	s_waitcnt lgkmcnt(7)
	v_mul_f32_e32 v171, v69, v221
	v_fmac_f32_e32 v171, v68, v220
	v_mul_f32_e32 v170, v65, v223
	v_fmac_f32_e32 v170, v64, v222
	ds_read_b128 v[220:223], v99 offset:30720
	v_add_f32_e32 v170, v171, v170
	s_waitcnt lgkmcnt(7)
	v_mul_f32_e32 v175, v71, v225
	v_add_f32_e32 v97, v97, v170
	v_fmac_f32_e32 v175, v70, v224
	v_mul_f32_e32 v174, v67, v227
	v_fmac_f32_e32 v174, v66, v226
	ds_read_b128 v[224:227], v99 offset:31744
	v_add_f32_e32 v174, v175, v174
	v_add_f32_e32 v97, v97, v174
	s_waitcnt lgkmcnt(7)
	v_mul_f32_e32 v171, v93, v197
	v_fmac_f32_e32 v171, v92, v196
	v_mul_f32_e32 v170, v91, v199
	v_fmac_f32_e32 v170, v90, v198
	ds_read_b128 v[196:199], v99 offset:32768
	v_add_f32_e32 v170, v171, v170
	s_waitcnt lgkmcnt(7)
	v_mul_f32_e32 v175, v95, v201
	v_add_f32_e32 v178, 0, v170
	v_fmac_f32_e32 v175, v94, v200
	v_mul_f32_e32 v174, v89, v203
	v_fmac_f32_e32 v174, v88, v202
	ds_read_b128 v[200:203], v99 offset:33792
	v_add_f32_e32 v174, v175, v174
	v_add_f32_e32 v178, v178, v174
	s_waitcnt lgkmcnt(7)
	v_mul_f32_e32 v171, v85, v205
	v_fmac_f32_e32 v171, v84, v204
	v_mul_f32_e32 v170, v83, v207
	v_fmac_f32_e32 v170, v82, v206
	ds_read_b128 v[204:207], v99 offset:34816
	v_add_f32_e32 v170, v171, v170
	s_waitcnt lgkmcnt(7)
	v_mul_f32_e32 v175, v87, v209
	v_add_f32_e32 v178, v178, v170
	v_fmac_f32_e32 v175, v86, v208
	v_mul_f32_e32 v174, v79, v211
	v_fmac_f32_e32 v174, v78, v210
	ds_read_b128 v[208:211], v99 offset:35840
	v_add_f32_e32 v174, v175, v174
	v_add_f32_e32 v178, v178, v174
	s_waitcnt lgkmcnt(7)
	v_mul_f32_e32 v171, v77, v213
	v_fmac_f32_e32 v171, v76, v212
	v_mul_f32_e32 v170, v75, v215
	v_fmac_f32_e32 v170, v74, v214
	ds_read_b128 v[212:215], v99 offset:36864
	v_add_f32_e32 v170, v171, v170
	s_waitcnt lgkmcnt(7)
	v_mul_f32_e32 v175, v81, v217
	v_add_f32_e32 v178, v178, v170
	v_fmac_f32_e32 v175, v80, v216
	v_mul_f32_e32 v174, v73, v219
	v_fmac_f32_e32 v174, v72, v218
	ds_read_b128 v[216:219], v99 offset:37888
	v_add_f32_e32 v174, v175, v174
	v_add_f32_e32 v178, v178, v174
	s_waitcnt lgkmcnt(7)
	v_mul_f32_e32 v171, v69, v221
	v_fmac_f32_e32 v171, v68, v220
	v_mul_f32_e32 v170, v65, v223
	v_fmac_f32_e32 v170, v64, v222
	ds_read_b128 v[220:223], v99 offset:38912
	v_add_f32_e32 v170, v171, v170
	s_waitcnt lgkmcnt(7)
; #define LAS __attribute__((address_space(3)))
; template <int MODE, bool SB  > DI void norm_phase(const Params& P, const Frame& F, int L, const void* src_, const float* gain, bool combine) {
;     ...
;         if (MODE == 1) {
;             float s[16];
; #pragma unroll
;             for (int q = 0; q < 16; ++q) { float t = 0.f;
; #pragma unroll
;                 for (int j = 0; j < 8; ++j) { const f32x4 w = *(const LAS f32x4*)(F.lds + (size_t)(q * D + 256 * j + 4 * F.lane) * 4); t += (v[j][0] * w[0] + v[j][1] * w[1]) + (v[j][2] * w[2] + v[j][3] * w[3]); }
;                 s[q] = t; if ((q & 3) == 3) asm volatile("" ::: "memory"); }
	v_mul_f32_e32 v171, v71, v225
	v_fmac_f32_e32 v171, v70, v224
	v_mul_f32_e32 v177, v67, v227
	v_fmac_f32_e32 v177, v66, v226
	ds_read_b128 v[224:227], v99 offset:39936
	v_add_f32_e32 v170, v178, v170
	v_add_f32_e32 v171, v171, v177
	v_add_f32_e32 v170, v170, v171
	s_waitcnt lgkmcnt(7)
	v_mul_f32_e32 v171, v93, v197
	v_fmac_f32_e32 v171, v92, v196
	v_mul_f32_e32 v172, v91, v199
	v_fmac_f32_e32 v172, v90, v198
	ds_read_b128 v[196:199], v99 offset:40960
	s_waitcnt lgkmcnt(7)
	v_mul_f32_e32 v177, v95, v201
	v_add_f32_e32 v171, v171, v172
	v_fmac_f32_e32 v177, v94, v200
	v_mul_f32_e32 v176, v89, v203
	v_fmac_f32_e32 v176, v88, v202
	ds_read_b128 v[200:203], v99 offset:41984
	v_add_f32_e32 v171, 0, v171
	v_add_f32_e32 v176, v177, v176
	v_add_f32_e32 v171, v171, v176
	s_waitcnt lgkmcnt(7)
	v_mul_f32_e32 v173, v85, v205
	v_fmac_f32_e32 v173, v84, v204
	v_mul_f32_e32 v172, v83, v207
	v_fmac_f32_e32 v172, v82, v206
	ds_read_b128 v[204:207], v99 offset:43008
	v_add_f32_e32 v172, v173, v172
	s_waitcnt lgkmcnt(7)
	v_mul_f32_e32 v177, v87, v209
	v_add_f32_e32 v171, v171, v172
	v_fmac_f32_e32 v177, v86, v208
	v_mul_f32_e32 v176, v79, v211
	v_fmac_f32_e32 v176, v78, v210
	ds_read_b128 v[208:211], v99 offset:44032
	v_add_f32_e32 v176, v177, v176
	v_add_f32_e32 v171, v171, v176
	s_waitcnt lgkmcnt(7)
	v_mul_f32_e32 v173, v77, v213
	v_fmac_f32_e32 v173, v76, v212
	v_mul_f32_e32 v172, v75, v215
	v_fmac_f32_e32 v172, v74, v214
	ds_read_b128 v[212:215], v99 offset:45056
	v_add_f32_e32 v172, v173, v172
	s_waitcnt lgkmcnt(7)
	v_mul_f32_e32 v177, v81, v217
	v_add_f32_e32 v171, v171, v172
	v_fmac_f32_e32 v177, v80, v216
	v_mul_f32_e32 v176, v73, v219
	v_fmac_f32_e32 v176, v72, v218
	ds_read_b128 v[216:219], v99 offset:46080
	v_add_f32_e32 v176, v177, v176
	v_add_f32_e32 v171, v171, v176
	s_waitcnt lgkmcnt(7)
	v_mul_f32_e32 v173, v69, v221
	v_fmac_f32_e32 v173, v68, v220
	v_mul_f32_e32 v172, v65, v223
	v_fmac_f32_e32 v172, v64, v222
	ds_read_b128 v[220:223], v99 offset:47104
	v_add_f32_e32 v172, v173, v172
	s_waitcnt lgkmcnt(7)
	v_mul_f32_e32 v177, v71, v225
	v_add_f32_e32 v171, v171, v172
	v_fmac_f32_e32 v177, v70, v224
	v_mul_f32_e32 v176, v67, v227
	v_fmac_f32_e32 v176, v66, v226
	ds_read_b128 v[224:227], v99 offset:48128
	v_add_f32_e32 v176, v177, v176
	v_add_f32_e32 v171, v171, v176
	s_waitcnt lgkmcnt(7)
	v_mul_f32_e32 v173, v93, v197
	v_fmac_f32_e32 v173, v92, v196
	v_mul_f32_e32 v172, v91, v199
	v_fmac_f32_e32 v172, v90, v198
	ds_read_b128 v[196:199], v99 offset:49152
	v_add_f32_e32 v172, v173, v172
	s_waitcnt lgkmcnt(7)
	v_mul_f32_e32 v177, v95, v201
	v_add_f32_e32 v180, 0, v172
	v_fmac_f32_e32 v177, v94, v200
	v_mul_f32_e32 v176, v89, v203
	v_fmac_f32_e32 v176, v88, v202
	ds_read_b128 v[200:203], v99 offset:50176
	v_add_f32_e32 v176, v177, v176
	v_add_f32_e32 v180, v180, v176
	s_waitcnt lgkmcnt(7)
	v_mul_f32_e32 v173, v85, v205
	v_fmac_f32_e32 v173, v84, v204
	v_mul_f32_e32 v172, v83, v207
	v_fmac_f32_e32 v172, v82, v206
	ds_read_b128 v[204:207], v99 offset:51200
	v_add_f32_e32 v172, v173, v172
	s_waitcnt lgkmcnt(7)
	v_mul_f32_e32 v177, v87, v209
	v_add_f32_e32 v180, v180, v172
	v_fmac_f32_e32 v177, v86, v208
	v_mul_f32_e32 v176, v79, v211
	v_fmac_f32_e32 v176, v78, v210
	ds_read_b128 v[208:211], v99 offset:52224
	v_add_f32_e32 v176, v177, v176
	v_add_f32_e32 v180, v180, v176
	s_waitcnt lgkmcnt(7)
	v_mul_f32_e32 v173, v77, v213
	v_fmac_f32_e32 v173, v76, v212
	v_mul_f32_e32 v172, v75, v215
	v_fmac_f32_e32 v172, v74, v214
	ds_read_b128 v[212:215], v99 offset:53248
	v_add_f32_e32 v172, v173, v172
	s_waitcnt lgkmcnt(7)
	v_mul_f32_e32 v177, v81, v217
	v_add_f32_e32 v180, v180, v172
	v_fmac_f32_e32 v177, v80, v216
	v_mul_f32_e32 v176, v73, v219
	v_fmac_f32_e32 v176, v72, v218
	ds_read_b128 v[216:219], v99 offset:54272
	v_add_f32_e32 v176, v177, v176
	v_add_f32_e32 v180, v180, v176
	s_waitcnt lgkmcnt(7)
	v_mul_f32_e32 v173, v69, v221
	v_fmac_f32_e32 v173, v68, v220
	v_mul_f32_e32 v172, v65, v223
	v_fmac_f32_e32 v172, v64, v222
	ds_read_b128 v[220:223], v99 offset:55296
	v_add_f32_e32 v172, v173, v172
	s_waitcnt lgkmcnt(7)
	v_mul_f32_e32 v173, v71, v225
	v_fmac_f32_e32 v173, v70, v224
	v_mul_f32_e32 v179, v67, v227
	v_fmac_f32_e32 v179, v66, v226
	ds_read_b128 v[224:227], v99 offset:56320
	v_add_f32_e32 v172, v180, v172
	v_add_f32_e32 v173, v173, v179
	v_add_f32_e32 v172, v172, v173
	s_waitcnt lgkmcnt(7)
	v_mul_f32_e32 v173, v93, v197
	v_fmac_f32_e32 v173, v92, v196
	v_mul_f32_e32 v174, v91, v199
	v_fmac_f32_e32 v174, v90, v198
	ds_read_b128 v[196:199], v99 offset:57344
	s_waitcnt lgkmcnt(7)
	v_mul_f32_e32 v179, v95, v201
	v_add_f32_e32 v173, v173, v174
	v_fmac_f32_e32 v179, v94, v200
	v_mul_f32_e32 v178, v89, v203
	v_fmac_f32_e32 v178, v88, v202
	ds_read_b128 v[200:203], v99 offset:58368
	v_add_f32_e32 v173, 0, v173
	v_add_f32_e32 v178, v179, v178
	v_add_f32_e32 v173, v173, v178
	s_waitcnt lgkmcnt(7)
	v_mul_f32_e32 v175, v85, v205
	v_fmac_f32_e32 v175, v84, v204
	v_mul_f32_e32 v174, v83, v207
	v_fmac_f32_e32 v174, v82, v206
	ds_read_b128 v[204:207], v99 offset:59392
	v_add_f32_e32 v174, v175, v174
	s_waitcnt lgkmcnt(7)
	v_mul_f32_e32 v179, v87, v209
	v_add_f32_e32 v173, v173, v174
	v_fmac_f32_e32 v179, v86, v208
	v_mul_f32_e32 v178, v79, v211
	v_fmac_f32_e32 v178, v78, v210
	ds_read_b128 v[208:211], v99 offset:60416
	v_add_f32_e32 v178, v179, v178
	v_add_f32_e32 v173, v173, v178
	s_waitcnt lgkmcnt(7)
	v_mul_f32_e32 v175, v77, v213
	v_fmac_f32_e32 v175, v76, v212
	v_mul_f32_e32 v174, v75, v215
	v_fmac_f32_e32 v174, v74, v214
	ds_read_b128 v[212:215], v99 offset:61440
	v_add_f32_e32 v174, v175, v174
	s_waitcnt lgkmcnt(7)
; #define LAS __attribute__((address_space(3)))
; template <int MODE, bool SB  > DI void norm_phase(const Params& P, const Frame& F, int L, const void* src_, const float* gain, bool combine) {
;     ...
;         if (MODE == 1) {
;             float s[16];
; #pragma unroll
;             for (int q = 0; q < 16; ++q) { float t = 0.f;
; #pragma unroll
;                 for (int j = 0; j < 8; ++j) { const f32x4 w = *(const LAS f32x4*)(F.lds + (size_t)(q * D + 256 * j + 4 * F.lane) * 4); t += (v[j][0] * w[0] + v[j][1] * w[1]) + (v[j][2] * w[2] + v[j][3] * w[3]); }
;                 s[q] = t; if ((q & 3) == 3) asm volatile("" ::: "memory"); }
	v_mul_f32_e32 v179, v81, v217
	v_add_f32_e32 v173, v173, v174
	v_fmac_f32_e32 v179, v80, v216
	v_mul_f32_e32 v178, v73, v219
	v_fmac_f32_e32 v178, v72, v218
	ds_read_b128 v[216:219], v99 offset:62464
	v_add_f32_e32 v178, v179, v178
	v_add_f32_e32 v173, v173, v178
	s_waitcnt lgkmcnt(7)
	v_mul_f32_e32 v175, v69, v221
	v_fmac_f32_e32 v175, v68, v220
	v_mul_f32_e32 v174, v65, v223
	v_fmac_f32_e32 v174, v64, v222
	ds_read_b128 v[220:223], v99 offset:63488
	v_add_f32_e32 v174, v175, v174
	s_waitcnt lgkmcnt(7)
	v_mul_f32_e32 v179, v71, v225
	v_add_f32_e32 v173, v173, v174
	v_fmac_f32_e32 v179, v70, v224
	v_mul_f32_e32 v178, v67, v227
	v_fmac_f32_e32 v178, v66, v226
	ds_read_b128 v[224:227], v99 offset:64512
	v_add_f32_e32 v178, v179, v178
	v_add_f32_e32 v173, v173, v178
	s_waitcnt lgkmcnt(7)
	v_mul_f32_e32 v175, v93, v197
	v_fmac_f32_e32 v175, v92, v196
	v_mul_f32_e32 v174, v91, v199
	v_fmac_f32_e32 v174, v90, v198
	ds_read_b128 v[196:199], v100
	v_add_f32_e32 v174, v175, v174
	s_waitcnt lgkmcnt(7)
	v_mul_f32_e32 v179, v95, v201
	v_add_f32_e32 v182, 0, v174
	v_fmac_f32_e32 v179, v94, v200
	v_mul_f32_e32 v178, v89, v203
	v_fmac_f32_e32 v178, v88, v202
	ds_read_b128 v[200:203], v101
	v_add_f32_e32 v178, v179, v178
	v_add_f32_e32 v182, v182, v178
	s_waitcnt lgkmcnt(7)
	v_mul_f32_e32 v175, v85, v205
	v_fmac_f32_e32 v175, v84, v204
	v_mul_f32_e32 v174, v83, v207
	v_fmac_f32_e32 v174, v82, v206
	ds_read_b128 v[204:207], v102
	v_add_f32_e32 v174, v175, v174
	s_waitcnt lgkmcnt(7)
	v_mul_f32_e32 v179, v87, v209
	v_add_f32_e32 v182, v182, v174
	v_fmac_f32_e32 v179, v86, v208
	v_mul_f32_e32 v178, v79, v211
	v_fmac_f32_e32 v178, v78, v210
	ds_read_b128 v[208:211], v103
	v_add_f32_e32 v178, v179, v178
	v_add_f32_e32 v182, v182, v178
	s_waitcnt lgkmcnt(7)
	v_mul_f32_e32 v175, v77, v213
	v_fmac_f32_e32 v175, v76, v212
	v_mul_f32_e32 v174, v75, v215
	v_fmac_f32_e32 v174, v74, v214
	ds_read_b128 v[212:215], v104
	v_add_f32_e32 v174, v175, v174
	s_waitcnt lgkmcnt(7)
	v_mul_f32_e32 v179, v81, v217
	v_add_f32_e32 v182, v182, v174
	v_fmac_f32_e32 v179, v80, v216
	v_mul_f32_e32 v178, v73, v219
	v_fmac_f32_e32 v178, v72, v218
	ds_read_b128 v[216:219], v105
	v_add_f32_e32 v178, v179, v178
	v_add_f32_e32 v182, v182, v178
	s_waitcnt lgkmcnt(7)
	v_mul_f32_e32 v175, v69, v221
	v_fmac_f32_e32 v175, v68, v220
	v_mul_f32_e32 v174, v65, v223
	v_fmac_f32_e32 v174, v64, v222
	ds_read_b128 v[220:223], v106
	v_add_f32_e32 v174, v175, v174
	s_waitcnt lgkmcnt(7)
	v_mul_f32_e32 v175, v71, v225
	v_fmac_f32_e32 v175, v70, v224
	v_mul_f32_e32 v181, v67, v227
	v_fmac_f32_e32 v181, v66, v226
	ds_read_b128 v[224:227], v107
	v_add_f32_e32 v174, v182, v174
	v_add_f32_e32 v175, v175, v181
	v_add_f32_e32 v174, v174, v175
	s_waitcnt lgkmcnt(7)
	v_mul_f32_e32 v175, v93, v197
	v_fmac_f32_e32 v175, v92, v196
	v_mul_f32_e32 v176, v91, v199
	v_fmac_f32_e32 v176, v90, v198
	ds_read_b128 v[196:199], v108
	s_waitcnt lgkmcnt(7)
	v_mul_f32_e32 v181, v95, v201
	v_add_f32_e32 v175, v175, v176
	v_fmac_f32_e32 v181, v94, v200
	v_mul_f32_e32 v180, v89, v203
	v_fmac_f32_e32 v180, v88, v202
	ds_read_b128 v[200:203], v109
	v_add_f32_e32 v175, 0, v175
	v_add_f32_e32 v180, v181, v180
	v_add_f32_e32 v175, v175, v180
	s_waitcnt lgkmcnt(7)
	v_mul_f32_e32 v177, v85, v205
	v_fmac_f32_e32 v177, v84, v204
	v_mul_f32_e32 v176, v83, v207
	v_fmac_f32_e32 v176, v82, v206
	ds_read_b128 v[204:207], v110
	v_add_f32_e32 v176, v177, v176
	s_waitcnt lgkmcnt(7)
	v_mul_f32_e32 v181, v87, v209
	v_add_f32_e32 v175, v175, v176
	v_fmac_f32_e32 v181, v86, v208
	v_mul_f32_e32 v180, v79, v211
	v_fmac_f32_e32 v180, v78, v210
	ds_read_b128 v[208:211], v111
	v_add_f32_e32 v180, v181, v180
	v_add_f32_e32 v175, v175, v180
	s_waitcnt lgkmcnt(7)
	v_mul_f32_e32 v177, v77, v213
	v_fmac_f32_e32 v177, v76, v212
	v_mul_f32_e32 v176, v75, v215
	v_fmac_f32_e32 v176, v74, v214
	ds_read_b128 v[212:215], v112
	v_add_f32_e32 v176, v177, v176
	s_waitcnt lgkmcnt(7)
	v_mul_f32_e32 v181, v81, v217
	v_add_f32_e32 v175, v175, v176
	v_fmac_f32_e32 v181, v80, v216
	v_mul_f32_e32 v180, v73, v219
	v_fmac_f32_e32 v180, v72, v218
	ds_read_b128 v[216:219], v113
	v_add_f32_e32 v180, v181, v180
	v_add_f32_e32 v175, v175, v180
	s_waitcnt lgkmcnt(7)
	v_mul_f32_e32 v177, v69, v221
	v_fmac_f32_e32 v177, v68, v220
	v_mul_f32_e32 v176, v65, v223
	v_fmac_f32_e32 v176, v64, v222
	ds_read_b128 v[220:223], v114
	v_add_f32_e32 v176, v177, v176
	s_waitcnt lgkmcnt(7)
	v_mul_f32_e32 v181, v71, v225
	v_add_f32_e32 v175, v175, v176
	v_fmac_f32_e32 v181, v70, v224
	v_mul_f32_e32 v180, v67, v227
	v_fmac_f32_e32 v180, v66, v226
	ds_read_b128 v[224:227], v115
	v_add_f32_e32 v180, v181, v180
	v_add_f32_e32 v175, v175, v180
	s_waitcnt lgkmcnt(7)
	v_mul_f32_e32 v177, v93, v197
	v_fmac_f32_e32 v177, v92, v196
	v_mul_f32_e32 v176, v91, v199
	v_fmac_f32_e32 v176, v90, v198
	ds_read_b128 v[196:199], v116
	v_add_f32_e32 v176, v177, v176
	s_waitcnt lgkmcnt(7)
	v_mul_f32_e32 v181, v95, v201
	v_add_f32_e32 v184, 0, v176
	v_fmac_f32_e32 v181, v94, v200
	v_mul_f32_e32 v180, v89, v203
	v_fmac_f32_e32 v180, v88, v202
	ds_read_b128 v[200:203], v117
	v_add_f32_e32 v180, v181, v180
	v_add_f32_e32 v184, v184, v180
	s_waitcnt lgkmcnt(7)
	v_mul_f32_e32 v177, v85, v205
	v_fmac_f32_e32 v177, v84, v204
	v_mul_f32_e32 v176, v83, v207
	v_fmac_f32_e32 v176, v82, v206
	ds_read_b128 v[204:207], v118
	v_add_f32_e32 v176, v177, v176
	s_waitcnt lgkmcnt(7)
	v_mul_f32_e32 v181, v87, v209
	v_add_f32_e32 v184, v184, v176
	v_fmac_f32_e32 v181, v86, v208
	v_mul_f32_e32 v180, v79, v211
	v_fmac_f32_e32 v180, v78, v210
	ds_read_b128 v[208:211], v119
	v_add_f32_e32 v180, v181, v180
	v_add_f32_e32 v184, v184, v180
	s_waitcnt lgkmcnt(7)
; #define LAS __attribute__((address_space(3)))
; template <int MODE, bool SB  > DI void norm_phase(const Params& P, const Frame& F, int L, const void* src_, const float* gain, bool combine) {
;     ...
;         if (MODE == 1) {
;             float s[16];
; #pragma unroll
;             for (int q = 0; q < 16; ++q) { float t = 0.f;
; #pragma unroll
;                 for (int j = 0; j < 8; ++j) { const f32x4 w = *(const LAS f32x4*)(F.lds + (size_t)(q * D + 256 * j + 4 * F.lane) * 4); t += (v[j][0] * w[0] + v[j][1] * w[1]) + (v[j][2] * w[2] + v[j][3] * w[3]); }
;                 s[q] = t; if ((q & 3) == 3) asm volatile("" ::: "memory"); }
	v_mul_f32_e32 v177, v77, v213
	v_fmac_f32_e32 v177, v76, v212
	v_mul_f32_e32 v176, v75, v215
	v_fmac_f32_e32 v176, v74, v214
	ds_read_b128 v[212:215], v120
	v_add_f32_e32 v176, v177, v176
	s_waitcnt lgkmcnt(7)
	v_mul_f32_e32 v181, v81, v217
	v_add_f32_e32 v184, v184, v176
	v_fmac_f32_e32 v181, v80, v216
	v_mul_f32_e32 v180, v73, v219
	v_fmac_f32_e32 v180, v72, v218
	ds_read_b128 v[216:219], v121
	v_add_f32_e32 v180, v181, v180
	v_add_f32_e32 v184, v184, v180
	s_waitcnt lgkmcnt(7)
	v_mul_f32_e32 v177, v69, v221
	v_fmac_f32_e32 v177, v68, v220
	v_mul_f32_e32 v176, v65, v223
	v_fmac_f32_e32 v176, v64, v222
	ds_read_b128 v[220:223], v122
	v_add_f32_e32 v176, v177, v176
	s_waitcnt lgkmcnt(7)
	v_mul_f32_e32 v177, v71, v225
	v_mul_f32_e32 v183, v67, v227
	v_fmac_f32_e32 v177, v70, v224
	v_fmac_f32_e32 v183, v66, v226
	ds_read_b128 v[224:227], v123
	v_add_f32_e32 v176, v184, v176
	v_add_f32_e32 v177, v177, v183
	v_add_f32_e32 v176, v176, v177
	s_waitcnt lgkmcnt(7)
	v_mul_f32_e32 v177, v93, v197
	v_fmac_f32_e32 v177, v92, v196
	v_mul_f32_e32 v178, v91, v199
	s_waitcnt lgkmcnt(6)
	v_mul_f32_e32 v183, v95, v201
	v_fmac_f32_e32 v178, v90, v198
	ds_read_b128 v[196:199], v124
	v_fmac_f32_e32 v183, v94, v200
	v_mul_f32_e32 v182, v89, v203
	v_add_f32_e32 v177, v177, v178
	v_fmac_f32_e32 v182, v88, v202
	ds_read_b128 v[200:203], v125
	v_add_f32_e32 v177, 0, v177
	v_add_f32_e32 v182, v183, v182
	v_add_f32_e32 v177, v177, v182
	s_waitcnt lgkmcnt(7)
	v_mul_f32_e32 v179, v85, v205
	v_fmac_f32_e32 v179, v84, v204
	v_mul_f32_e32 v178, v83, v207
	v_fmac_f32_e32 v178, v82, v206
	ds_read_b128 v[204:207], v126
	s_waitcnt lgkmcnt(7)
	v_mul_f32_e32 v183, v87, v209
	v_add_f32_e32 v178, v179, v178
	v_fmac_f32_e32 v183, v86, v208
	v_mul_f32_e32 v182, v79, v211
	v_add_f32_e32 v177, v177, v178
	v_fmac_f32_e32 v182, v78, v210
	ds_read_b128 v[208:211], v127
	v_add_f32_e32 v182, v183, v182
	v_add_f32_e32 v177, v177, v182
	s_waitcnt lgkmcnt(7)
	v_mul_f32_e32 v179, v77, v213
	v_fmac_f32_e32 v179, v76, v212
	v_mul_f32_e32 v178, v75, v215
	v_fmac_f32_e32 v178, v74, v214
	ds_read_b128 v[212:215], v128
	s_waitcnt lgkmcnt(7)
	v_mul_f32_e32 v183, v81, v217
	v_add_f32_e32 v178, v179, v178
	v_fmac_f32_e32 v183, v80, v216
	v_mul_f32_e32 v182, v73, v219
	v_add_f32_e32 v177, v177, v178
	v_fmac_f32_e32 v182, v72, v218
	ds_read_b128 v[216:219], v129
	v_add_f32_e32 v182, v183, v182
	v_add_f32_e32 v177, v177, v182
	s_waitcnt lgkmcnt(7)
	v_mul_f32_e32 v179, v69, v221
	v_fmac_f32_e32 v179, v68, v220
	v_mul_f32_e32 v178, v65, v223
	v_fmac_f32_e32 v178, v64, v222
	ds_read_b128 v[220:223], v130
	s_waitcnt lgkmcnt(7)
	v_mul_f32_e32 v183, v71, v225
	v_add_f32_e32 v178, v179, v178
	v_fmac_f32_e32 v183, v70, v224
	v_mul_f32_e32 v182, v67, v227
	v_add_f32_e32 v177, v177, v178
	v_fmac_f32_e32 v182, v66, v226
	ds_read_b128 v[224:227], v131
	v_add_f32_e32 v182, v183, v182
	v_add_f32_e32 v177, v177, v182
	s_waitcnt lgkmcnt(7)
	v_mul_f32_e32 v179, v93, v197
	v_fmac_f32_e32 v179, v92, v196
	v_mul_f32_e32 v178, v91, v199
	v_fmac_f32_e32 v178, v90, v198
	ds_read_b128 v[196:199], v132
	s_waitcnt lgkmcnt(7)
	v_mul_f32_e32 v183, v95, v201
	v_add_f32_e32 v178, v179, v178
	v_fmac_f32_e32 v183, v94, v200
	v_mul_f32_e32 v182, v89, v203
	v_add_f32_e32 v186, 0, v178
	v_fmac_f32_e32 v182, v88, v202
	ds_read_b128 v[200:203], v133
	v_add_f32_e32 v182, v183, v182
	v_add_f32_e32 v186, v186, v182
	s_waitcnt lgkmcnt(7)
	v_mul_f32_e32 v179, v85, v205
	v_fmac_f32_e32 v179, v84, v204
	v_mul_f32_e32 v178, v83, v207
	v_fmac_f32_e32 v178, v82, v206
	ds_read_b128 v[204:207], v134
	s_waitcnt lgkmcnt(7)
	v_mul_f32_e32 v183, v87, v209
	v_add_f32_e32 v178, v179, v178
	v_fmac_f32_e32 v183, v86, v208
	v_mul_f32_e32 v182, v79, v211
	v_add_f32_e32 v186, v186, v178
	v_fmac_f32_e32 v182, v78, v210
	ds_read_b128 v[208:211], v135
	v_add_f32_e32 v182, v183, v182
	v_add_f32_e32 v186, v186, v182
	s_waitcnt lgkmcnt(7)
	v_mul_f32_e32 v179, v77, v213
	v_fmac_f32_e32 v179, v76, v212
	v_mul_f32_e32 v178, v75, v215
	v_fmac_f32_e32 v178, v74, v214
	ds_read_b128 v[212:215], v136
	s_waitcnt lgkmcnt(7)
	v_mul_f32_e32 v183, v81, v217
	v_add_f32_e32 v178, v179, v178
	v_fmac_f32_e32 v183, v80, v216
	v_mul_f32_e32 v182, v73, v219
	v_add_f32_e32 v186, v186, v178
	v_fmac_f32_e32 v182, v72, v218
	ds_read_b128 v[216:219], v137
	v_add_f32_e32 v182, v183, v182
	v_add_f32_e32 v186, v186, v182
	s_waitcnt lgkmcnt(7)
	v_mul_f32_e32 v179, v69, v221
	v_fmac_f32_e32 v179, v68, v220
	v_mul_f32_e32 v178, v65, v223
	v_fmac_f32_e32 v178, v64, v222
	ds_read_b128 v[220:223], v138
	s_waitcnt lgkmcnt(7)
	v_mul_f32_e32 v183, v71, v225
	v_add_f32_e32 v178, v179, v178
	v_fmac_f32_e32 v183, v70, v224
	v_mul_f32_e32 v182, v67, v227
	v_add_f32_e32 v186, v186, v178
	v_fmac_f32_e32 v182, v66, v226
	ds_read_b128 v[224:227], v139
	v_add_f32_e32 v182, v183, v182
	v_add_f32_e32 v186, v186, v182
	s_waitcnt lgkmcnt(7)
	v_mul_f32_e32 v179, v93, v197
	v_fmac_f32_e32 v179, v92, v196
	v_mul_f32_e32 v178, v91, v199
	v_fmac_f32_e32 v178, v90, v198
	ds_read_b128 v[196:199], v140
	s_waitcnt lgkmcnt(7)
	v_mul_f32_e32 v183, v95, v201
	v_add_f32_e32 v178, v179, v178
	v_fmac_f32_e32 v183, v94, v200
	v_mul_f32_e32 v182, v89, v203
	v_add_f32_e32 v187, 0, v178
	v_fmac_f32_e32 v182, v88, v202
	ds_read_b128 v[200:203], v141
	v_add_f32_e32 v182, v183, v182
	v_add_f32_e32 v187, v187, v182
	s_waitcnt lgkmcnt(7)
	v_mul_f32_e32 v179, v85, v205
	v_fmac_f32_e32 v179, v84, v204
	v_mul_f32_e32 v178, v83, v207
	v_fmac_f32_e32 v178, v82, v206
	ds_read_b128 v[204:207], v142
	s_waitcnt lgkmcnt(7)
; #define LAS __attribute__((address_space(3)))
; template <int MODE, bool SB  > DI void norm_phase(const Params& P, const Frame& F, int L, const void* src_, const float* gain, bool combine) {
;     ...
;         if (MODE == 1) {
;             float s[16];
; #pragma unroll
;             for (int q = 0; q < 16; ++q) { float t = 0.f;
; #pragma unroll
;                 for (int j = 0; j < 8; ++j) { const f32x4 w = *(const LAS f32x4*)(F.lds + (size_t)(q * D + 256 * j + 4 * F.lane) * 4); t += (v[j][0] * w[0] + v[j][1] * w[1]) + (v[j][2] * w[2] + v[j][3] * w[3]); }
;                 s[q] = t; if ((q & 3) == 3) asm volatile("" ::: "memory"); }
	v_mul_f32_e32 v183, v87, v209
	v_add_f32_e32 v178, v179, v178
	v_fmac_f32_e32 v183, v86, v208
	v_mul_f32_e32 v182, v79, v211
	v_add_f32_e32 v187, v187, v178
	v_fmac_f32_e32 v182, v78, v210
	ds_read_b128 v[208:211], v143
	v_add_f32_e32 v182, v183, v182
	v_add_f32_e32 v187, v187, v182
	s_waitcnt lgkmcnt(7)
	v_mul_f32_e32 v179, v77, v213
	v_fmac_f32_e32 v179, v76, v212
	v_mul_f32_e32 v178, v75, v215
	v_fmac_f32_e32 v178, v74, v214
	ds_read_b128 v[212:215], v144
	s_waitcnt lgkmcnt(7)
	v_mul_f32_e32 v183, v81, v217
	v_add_f32_e32 v178, v179, v178
	v_fmac_f32_e32 v183, v80, v216
	v_mul_f32_e32 v182, v73, v219
	v_add_f32_e32 v187, v187, v178
	v_fmac_f32_e32 v182, v72, v218
	ds_read_b128 v[216:219], v145
	v_add_f32_e32 v182, v183, v182
	v_add_f32_e32 v187, v187, v182
	s_waitcnt lgkmcnt(7)
	v_mul_f32_e32 v179, v69, v221
	v_fmac_f32_e32 v179, v68, v220
	v_mul_f32_e32 v178, v65, v223
	v_fmac_f32_e32 v178, v64, v222
	ds_read_b128 v[220:223], v146
	s_waitcnt lgkmcnt(7)
	v_mul_f32_e32 v183, v71, v225
	v_add_f32_e32 v178, v179, v178
	v_fmac_f32_e32 v183, v70, v224
	v_mul_f32_e32 v182, v67, v227
	v_add_f32_e32 v187, v187, v178
	v_fmac_f32_e32 v182, v66, v226
	ds_read_b128 v[224:227], v147
	v_add_f32_e32 v182, v183, v182
	v_add_f32_e32 v187, v187, v182
	s_waitcnt lgkmcnt(7)
	v_mul_f32_e32 v179, v93, v197
	v_fmac_f32_e32 v179, v92, v196
	v_mul_f32_e32 v178, v91, v199
	v_fmac_f32_e32 v178, v90, v198
	ds_read_b128 v[196:199], v148
	s_waitcnt lgkmcnt(7)
	v_mul_f32_e32 v183, v95, v201
	v_add_f32_e32 v178, v179, v178
	v_fmac_f32_e32 v183, v94, v200
	v_mul_f32_e32 v182, v89, v203
	v_add_f32_e32 v188, 0, v178
	v_fmac_f32_e32 v182, v88, v202
	ds_read_b128 v[200:203], v149
	v_add_f32_e32 v182, v183, v182
	v_add_f32_e32 v188, v188, v182
	s_waitcnt lgkmcnt(7)
	v_mul_f32_e32 v179, v85, v205
	v_fmac_f32_e32 v179, v84, v204
	v_mul_f32_e32 v178, v83, v207
	v_fmac_f32_e32 v178, v82, v206
	ds_read_b128 v[204:207], v150
	s_waitcnt lgkmcnt(7)
	v_mul_f32_e32 v183, v87, v209
	v_add_f32_e32 v178, v179, v178
	v_fmac_f32_e32 v183, v86, v208
	v_mul_f32_e32 v182, v79, v211
	v_add_f32_e32 v188, v188, v178
	v_fmac_f32_e32 v182, v78, v210
	ds_read_b128 v[208:211], v151
	v_add_f32_e32 v182, v183, v182
	v_add_f32_e32 v188, v188, v182
	s_waitcnt lgkmcnt(7)
	v_mul_f32_e32 v179, v77, v213
	v_fmac_f32_e32 v179, v76, v212
	v_mul_f32_e32 v178, v75, v215
	v_fmac_f32_e32 v178, v74, v214
	ds_read_b128 v[212:215], v152
	s_waitcnt lgkmcnt(7)
	v_mul_f32_e32 v183, v81, v217
	v_add_f32_e32 v178, v179, v178
	v_fmac_f32_e32 v183, v80, v216
	v_mul_f32_e32 v182, v73, v219
	v_add_f32_e32 v188, v188, v178
	v_fmac_f32_e32 v182, v72, v218
	ds_read_b128 v[216:219], v153
	v_add_f32_e32 v182, v183, v182
	v_add_f32_e32 v188, v188, v182
	s_waitcnt lgkmcnt(7)
	v_mul_f32_e32 v179, v69, v221
	v_fmac_f32_e32 v179, v68, v220
	v_mul_f32_e32 v178, v65, v223
	v_fmac_f32_e32 v178, v64, v222
	ds_read_b128 v[220:223], v154
	s_waitcnt lgkmcnt(7)
	v_mul_f32_e32 v183, v71, v225
	v_add_f32_e32 v178, v179, v178
	v_fmac_f32_e32 v183, v70, v224
	v_mul_f32_e32 v182, v67, v227
	v_add_f32_e32 v188, v188, v178
	v_fmac_f32_e32 v182, v66, v226
	ds_read_b128 v[224:227], v155
	v_add_f32_e32 v182, v183, v182
	v_add_f32_e32 v188, v188, v182
	s_waitcnt lgkmcnt(7)
	v_mul_f32_e32 v179, v93, v197
	v_fmac_f32_e32 v179, v92, v196
	v_mul_f32_e32 v178, v91, v199
	v_fmac_f32_e32 v178, v90, v198
	ds_read_b128 v[196:199], v156
	s_waitcnt lgkmcnt(7)
	v_mul_f32_e32 v183, v95, v201
	v_add_f32_e32 v178, v179, v178
	v_fmac_f32_e32 v183, v94, v200
	v_mul_f32_e32 v182, v89, v203
	v_add_f32_e32 v189, 0, v178
	v_fmac_f32_e32 v182, v88, v202
	ds_read_b128 v[200:203], v157
	v_add_f32_e32 v182, v183, v182
	v_add_f32_e32 v189, v189, v182
	s_waitcnt lgkmcnt(7)
	v_mul_f32_e32 v179, v85, v205
	v_fmac_f32_e32 v179, v84, v204
	v_mul_f32_e32 v178, v83, v207
	v_fmac_f32_e32 v178, v82, v206
	ds_read_b128 v[204:207], v158
	s_waitcnt lgkmcnt(7)
	v_mul_f32_e32 v183, v87, v209
	v_add_f32_e32 v178, v179, v178
	v_fmac_f32_e32 v183, v86, v208
	v_mul_f32_e32 v182, v79, v211
	v_add_f32_e32 v189, v189, v178
	v_fmac_f32_e32 v182, v78, v210
	ds_read_b128 v[208:211], v159
	v_add_f32_e32 v182, v183, v182
	v_add_f32_e32 v189, v189, v182
	s_waitcnt lgkmcnt(7)
	v_mul_f32_e32 v179, v77, v213
	v_fmac_f32_e32 v179, v76, v212
	v_mul_f32_e32 v178, v75, v215
	v_fmac_f32_e32 v178, v74, v214
	ds_read_b128 v[212:215], v160
	s_waitcnt lgkmcnt(7)
	v_mul_f32_e32 v183, v81, v217
	v_add_f32_e32 v178, v179, v178
	v_fmac_f32_e32 v183, v80, v216
	v_mul_f32_e32 v182, v73, v219
	v_add_f32_e32 v189, v189, v178
	v_fmac_f32_e32 v182, v72, v218
	ds_read_b128 v[216:219], v161
	v_add_f32_e32 v182, v183, v182
	v_add_f32_e32 v189, v189, v182
	s_waitcnt lgkmcnt(7)
	v_mul_f32_e32 v179, v69, v221
	v_fmac_f32_e32 v179, v68, v220
	v_mul_f32_e32 v178, v65, v223
	v_fmac_f32_e32 v178, v64, v222
	ds_read_b128 v[220:223], v162
	s_waitcnt lgkmcnt(7)
	v_mul_f32_e32 v183, v71, v225
	v_add_f32_e32 v178, v179, v178
	v_fmac_f32_e32 v183, v70, v224
	v_mul_f32_e32 v182, v67, v227
	v_add_f32_e32 v189, v189, v178
	v_fmac_f32_e32 v182, v66, v226
	ds_read_b128 v[224:227], v163
	v_add_f32_e32 v182, v183, v182
	v_add_f32_e32 v189, v189, v182
	s_waitcnt lgkmcnt(7)
; #define LAS __attribute__((address_space(3)))
; template <int MODE, bool SB  > DI void norm_phase(const Params& P, const Frame& F, int L, const void* src_, const float* gain, bool combine) {
;     ...
;             for (int q = 0; q < 16; ++q) { float t = 0.f;
; #pragma unroll
;                 for (int j = 0; j < 8; ++j) { const f32x4 w = *(const LAS f32x4*)(F.lds + (size_t)(q * D + 256 * j + 4 * F.lane) * 4); t += (v[j][0] * w[0] + v[j][1] * w[1]) + (v[j][2] * w[2] + v[j][3] * w[3]); }
;                 s[q] = t; if ((q & 3) == 3) asm volatile("" ::: "memory"); }
; #pragma unroll
;             for (int i = 0; i < 8; ++i) { const bool hi = (F.lane & 32) != 0; const float send = hi ? s[i] : s[i + 8], keep = hi ? s[i + 8] : s[i]; s[i] = keep + shx<32>(send); }
; #pragma unroll
;             for (int i = 0; i < 4; ++i) { const bool hi = (F.lane & 16) != 0; const float send = hi ? s[i] : s[i + 4], keep = hi ? s[i + 4] : s[i]; s[i] = keep + shx<16>(send); }
; #pragma unroll
;             for (int i = 0; i < 2; ++i) { const bool hi = (F.lane & 8) != 0; const float send = hi ? s[i] : s[i + 2], keep = hi ? s[i + 2] : s[i]; s[i] = keep + shx<8>(send); }
;             { const bool hi = (F.lane & 4) != 0; const float send = hi ? s[0] : s[1], keep = hi ? s[1] : s[0]; s[0] = keep + shx<4>(send); }
;             float mine = s[0]; mine += shx<2>(mine); mine += shx<1>(mine);
;             if ((F.lane & 3) == 0) { const int gi = ((F.lane >> 5) & 1) * 8 + ((F.lane >> 4) & 1) * 4 + ((F.lane >> 3) & 1) * 2 + ((F.lane >> 2) & 1), h = gi & 3; float r;
	v_mul_f32_e32 v93, v93, v197
	v_mul_f32_e32 v91, v91, v199
	v_fmac_f32_e32 v93, v92, v196
	v_fmac_f32_e32 v91, v90, v198
	v_add_f32_e32 v90, v93, v91
	s_waitcnt lgkmcnt(6)
	v_mul_f32_e32 v95, v95, v201
	v_mul_f32_e32 v89, v89, v203
	v_add_f32_e32 v178, 0, v90
	v_fmac_f32_e32 v95, v94, v200
	v_fmac_f32_e32 v89, v88, v202
	v_add_f32_e32 v88, v95, v89
	v_add_f32_e32 v88, v178, v88
	s_waitcnt lgkmcnt(5)
	v_mul_f32_e32 v85, v85, v205
	v_mul_f32_e32 v83, v83, v207
	v_fmac_f32_e32 v85, v84, v204
	v_fmac_f32_e32 v83, v82, v206
	v_add_f32_e32 v82, v85, v83
	s_waitcnt lgkmcnt(4)
	v_mul_f32_e32 v87, v87, v209
	v_mul_f32_e32 v79, v79, v211
	v_add_f32_e32 v88, v88, v82
	v_fmac_f32_e32 v87, v86, v208
	v_fmac_f32_e32 v79, v78, v210
	v_add_f32_e32 v78, v87, v79
	v_add_f32_e32 v78, v88, v78
	s_waitcnt lgkmcnt(3)
	v_mul_f32_e32 v77, v77, v213
	v_mul_f32_e32 v75, v75, v215
	v_fmac_f32_e32 v77, v76, v212
	v_fmac_f32_e32 v75, v74, v214
	v_add_f32_e32 v74, v77, v75
	s_waitcnt lgkmcnt(2)
	v_mul_f32_e32 v79, v81, v217
	v_mul_f32_e32 v73, v73, v219
	v_add_f32_e32 v78, v78, v74
	v_fmac_f32_e32 v79, v80, v216
	v_fmac_f32_e32 v73, v72, v218
	v_add_f32_e32 v72, v79, v73
	v_add_f32_e32 v72, v78, v72
	s_waitcnt lgkmcnt(1)
	v_mul_f32_e32 v69, v69, v221
	v_mul_f32_e32 v65, v65, v223
	v_fmac_f32_e32 v69, v68, v220
	v_fmac_f32_e32 v65, v64, v222
	v_add_f32_e32 v64, v69, v65
	s_waitcnt lgkmcnt(0)
	v_mul_f32_e32 v65, v71, v225
	v_mul_f32_e32 v67, v67, v227
	v_fmac_f32_e32 v65, v70, v224
	v_fmac_f32_e32 v67, v66, v226
	v_add_f32_e32 v64, v72, v64
	v_add_f32_e32 v65, v65, v67
	v_add_f32_e32 v64, v64, v65
	v_cndmask_b32_e64 v65, v47, v175, s[4:5]
	ds_bpermute_b32 v65, v98, v65
	v_cndmask_b32_e64 v66, v96, v176, s[4:5]
	ds_bpermute_b32 v66, v98, v66
	v_cndmask_b32_e64 v67, v97, v177, s[4:5]
	ds_bpermute_b32 v67, v98, v67
	v_cndmask_b32_e64 v47, v175, v47, s[4:5]
	s_waitcnt lgkmcnt(2)
	v_add_f32_e32 v47, v47, v65
	v_cndmask_b32_e64 v65, v176, v96, s[4:5]
	s_waitcnt lgkmcnt(1)
	v_add_f32_e32 v65, v65, v66
	v_cndmask_b32_e64 v66, v177, v97, s[4:5]
	s_waitcnt lgkmcnt(0)
	v_add_f32_e32 v66, v66, v67
	v_cndmask_b32_e64 v67, v170, v186, s[4:5]
	ds_bpermute_b32 v67, v98, v67
	v_cndmask_b32_e64 v69, v171, v187, s[4:5]
	ds_bpermute_b32 v69, v98, v69
	v_cndmask_b32_e64 v70, v172, v188, s[4:5]
	ds_bpermute_b32 v70, v98, v70
	v_cndmask_b32_e64 v68, v186, v170, s[4:5]
	s_waitcnt lgkmcnt(2)
	v_add_f32_e32 v67, v68, v67
	v_cndmask_b32_e64 v68, v187, v171, s[4:5]
	s_waitcnt lgkmcnt(1)
	v_add_f32_e32 v68, v68, v69
	v_cndmask_b32_e64 v69, v188, v172, s[4:5]
	s_waitcnt lgkmcnt(0)
	v_add_f32_e32 v69, v69, v70
	v_cndmask_b32_e64 v70, v173, v189, s[4:5]
	v_cndmask_b32_e64 v72, v174, v64, s[4:5]
	ds_bpermute_b32 v70, v98, v70
	ds_bpermute_b32 v72, v98, v72
	v_cndmask_b32_e64 v71, v189, v173, s[4:5]
	v_cndmask_b32_e64 v64, v64, v174, s[4:5]
	v_cndmask_b32_e64 v73, v47, v68, s[8:9]
	s_waitcnt lgkmcnt(1)
	v_add_f32_e32 v70, v71, v70
	s_waitcnt lgkmcnt(0)
	v_add_f32_e32 v64, v64, v72
	v_cndmask_b32_e64 v47, v68, v47, s[8:9]
	v_cndmask_b32_e64 v68, v65, v69, s[8:9]
	v_cndmask_b32_e64 v65, v69, v65, s[8:9]
	v_cndmask_b32_e64 v69, v66, v70, s[8:9]
	v_cndmask_b32_e64 v71, v67, v64, s[8:9]
	ds_swizzle_b32 v73, v73 offset:swizzle(SWAP,16)
	ds_swizzle_b32 v68, v68 offset:swizzle(SWAP,16)
	ds_swizzle_b32 v69, v69 offset:swizzle(SWAP,16)
	ds_swizzle_b32 v71, v71 offset:swizzle(SWAP,16)
	v_cndmask_b32_e64 v66, v70, v66, s[8:9]
	v_cndmask_b32_e64 v64, v64, v67, s[8:9]
	s_waitcnt lgkmcnt(3)
	v_add_f32_e32 v47, v47, v73
	s_waitcnt lgkmcnt(2)
	v_add_f32_e32 v65, v65, v68
	s_waitcnt lgkmcnt(1)
	v_add_f32_e32 v66, v66, v69
	s_waitcnt lgkmcnt(0)
	v_add_f32_e32 v64, v64, v71
	v_cndmask_b32_e64 v67, v47, v66, s[10:11]
	v_cndmask_b32_e64 v68, v65, v64, s[10:11]
	ds_swizzle_b32 v67, v67 offset:swizzle(SWAP,8)
	ds_swizzle_b32 v68, v68 offset:swizzle(SWAP,8)
	v_cndmask_b32_e64 v47, v66, v47, s[10:11]
	v_cndmask_b32_e64 v64, v64, v65, s[10:11]
	s_waitcnt lgkmcnt(1)
	v_add_f32_e32 v47, v47, v67
	s_waitcnt lgkmcnt(0)
	v_add_f32_e32 v64, v64, v68
	v_cndmask_b32_e64 v65, v47, v64, s[12:13]
	ds_swizzle_b32 v65, v65 offset:swizzle(SWAP,4)
	v_cndmask_b32_e64 v47, v64, v47, s[12:13]
	s_waitcnt lgkmcnt(0)
	v_add_f32_e32 v47, v47, v65
	s_nop 1
	v_add_f32_dpp v47, v47, v47 quad_perm:[2,3,0,1] row_mask:0xf bank_mask:0xf bound_ctrl:1
	s_nop 1
	v_mov_b32_dpp v64, v47 quad_perm:[1,0,3,2] row_mask:0xf bank_mask:0xf bound_ctrl:1
	s_and_saveexec_b64 s[20:21], s[14:15]
	s_cbranch_execz .LBB0_1647
	v_add_f32_e32 v47, v47, v64
	s_and_saveexec_b64 s[24:25], s[16:17]
	s_xor_b64 s[24:25], exec, s[24:25]
	s_cbranch_execz .LBB0_1659
	s_and_saveexec_b64 s[26:27], s[6:7]
	s_xor_b64 s[26:27], exec, s[26:27]
	s_cbranch_execz .LBB0_1656
	s_and_saveexec_b64 s[28:29], s[18:19]
	s_xor_b64 s[28:29], exec, s[28:29]
	s_cbranch_execz .LBB0_1653
	v_mov_b32_e32 v64, v190
	v_add_f32_e32 v64, v47, v64

.LBB0_1704:
	global_load_dword v1, v0, s[10:11] sc1
	s_waitcnt vmcnt(0)
	v_cmp_eq_u32_e32 vcc, 0, v1
	s_cbranch_vccnz .LBB0_1706
	s_mov_b64 s[18:19], -1
	s_mov_b64 s[22:23], -1
	s_branch .LBB0_1700
	s_nop 0
	s_nop 0
	s_nop 0
	s_nop 0
	s_nop 0
	s_nop 0
	s_nop 0
	s_nop 0
	s_nop 0
	s_nop 0
	s_nop 0
	s_nop 0
	s_nop 0
	s_nop 0
	s_nop 0
	s_nop 0
	s_nop 0
	s_nop 0
	s_nop 0
	s_nop 0
	s_nop 0
	s_nop 0
	s_nop 0
	s_nop 0
	s_nop 0
	s_nop 0
	s_nop 0
	s_nop 0
	s_nop 0
	s_nop 0
	s_nop 0
	s_nop 0
	s_nop 0
	s_nop 0
	s_nop 0
	s_nop 0
	s_nop 0
	s_nop 0
	s_nop 0
	s_nop 0
	s_nop 0
	s_nop 0
	s_nop 0
	s_nop 0
	s_nop 0
	s_nop 0
	s_nop 0
	s_nop 0
	s_nop 0
	s_nop 0
	s_nop 0
	s_nop 0
	s_nop 0
	s_nop 0
	s_nop 0
	s_nop 0
	s_nop 0
	s_nop 0
	s_nop 0
	s_nop 0
	s_nop 0
.LBB0_1706:
	s_cmp_lt_u32 s3, 0x40001
	s_mov_b64 s[18:19], 0
	s_cselect_b64 s[20:21], -1, 0
	s_mov_b64 s[22:23], -1
	s_and_b64 vcc, exec, s[20:21]
	s_cbranch_vccnz .LBB0_1703
	s_branch .LBB0_1700
	s_nop 0
	s_nop 0
	s_nop 0

; DI unsigned pk2(float lo, float hi) { const f32x2 v = {lo, hi}; return __builtin_bit_cast(unsigned, __builtin_convertvector(v, bf16x2_t)); }
; template <int MODE, bool SB  > DI void norm_phase(const Params& P, const Frame& F, int L, const void* src_, const float* gain, bool combine) {
;     ...
;     for (int row = r_lo + F.wave; row < r_hi; row += NWAVES) {
;         f32x4 v[8];
; #pragma unroll
;         for (int j = 0; j < 8; ++j) { if constexpr (SB) v[j] = (f32x4){bflo(vb[j].x), bfhi(vb[j].x), bflo(vb[j].y), bfhi(vb[j].y)}; else v[j] = vn[j]; }
;         { const int rnx = (row + NWAVES < r_hi) ? row + NWAVES : row;
; #pragma unroll
;           for (int j = 0; j < 8; ++j) { if constexpr (SB) vb[j] = *(const u32x2*)(srcb + (size_t)rnx * D + 4 * F.lane + 256 * j); else vn[j] = *(const f32x4*)(src + (size_t)rnx * D + 4 * F.lane + 256 * j); } }
;         if (MODE == 3 && combine) {
;             const int* SLOT = (const int*)(ws + WS_SLOT); const float* TOPW = (const float*)(ws + WS_TOPW); const bf16* Y = (const bf16*)(ws + WS_T + T_YPERM);
;             const int s1 = SLOT[row * 2], s2 = SLOT[row * 2 + 1]; const float w1 = TOPW[row * 2], w2 = TOPW[row * 2 + 1];
;             u32x2 ya[8], yb[8];
; #pragma unroll
;             for (int j = 0; j < 8; ++j) { ya[j] = *(const u32x2*)(Y + (size_t)s1 * D + 4 * F.lane + 256 * j); yb[j] = *(const u32x2*)(Y + (size_t)s2 * D + 4 * F.lane + 256 * j); }
; #pragma unroll
;             for (int j = 0; j < 8; ++j) { const f32x4 y1 = (f32x4){bflo(ya[j].x), bfhi(ya[j].x), bflo(ya[j].y), bfhi(ya[j].y)}, y2 = (f32x4){bflo(yb[j].x), bfhi(yb[j].x), bflo(yb[j].y), bfhi(yb[j].y)};
;                 v[j] = v[j] + w1 * y1 + w2 * y2;
;                 const u32x2 hb = {pk2(v[j][0], v[j][1]), pk2(v[j][2], v[j][3])}; *(u32x2*)(const_cast<bf16*>(srcb) + (size_t)row * D + 4 * F.lane + 256 * j) = hb;
;                 v[j] = (f32x4){bflo(hb.x), bfhi(hb.x), bflo(hb.y), bfhi(hb.y)}; }
;         }
;         float ss = 0.f;
; #pragma unroll
;         for (int j = 0; j < 8; ++j) ss += (v[j][0] * v[j][0] + v[j][1] * v[j][1]) + (v[j][2] * v[j][2] + v[j][3] * v[j][3]);
;         const float rstd = 1.0f / sqrtf(wave_sum(ss) * (1.0f / D) + EPS);
; #pragma unroll
;         for (int j = 0; j < 8; ++j) v[j] = v[j] * rstd * g[j];
.LBB0_2879:
	s_waitcnt vmcnt(0)
	v_and_b32_e32 v57, 0xffff0000, v46
	v_and_b32_e32 v56, 0xffff0000, v44
	v_and_b32_e32 v61, 0xffff0000, v47
	v_and_b32_e32 v60, 0xffff0000, v45
	v_lshlrev_b32_e32 v80, 16, v38
	v_and_b32_e32 v98, 0xffff0000, v38
	v_lshlrev_b32_e32 v78, 16, v39
	v_and_b32_e32 v79, 0xffff0000, v39
	v_lshlrev_b32_e32 v55, 16, v46
	v_lshlrev_b32_e32 v54, 16, v44
	v_lshlrev_b32_e32 v59, 16, v47
	v_lshlrev_b32_e32 v58, 16, v45
	v_pk_mul_f32 v[38:39], v[56:57], v[56:57]
	v_pk_mul_f32 v[44:45], v[60:61], v[60:61]
	v_pk_fma_f32 v[38:39], v[54:55], v[54:55], v[38:39]
	v_pk_fma_f32 v[44:45], v[58:59], v[58:59], v[44:45]
	v_and_b32_e32 v71, 0xffff0000, v43
	v_pk_add_f32 v[38:39], v[38:39], v[44:45]
	v_and_b32_e32 v70, 0xffff0000, v42
	v_lshlrev_b32_e32 v62, 16, v40
	v_and_b32_e32 v63, 0xffff0000, v40
	v_lshlrev_b32_e32 v66, 16, v48
	v_pk_add_f32 v[38:39], v[38:39], v[38:39] op_sel_hi:[0,1]
	v_lshlrev_b32_e32 v65, 16, v43
	v_lshlrev_b32_e32 v64, 16, v42
	v_pk_mul_f32 v[42:43], v[70:71], v[70:71]
	v_lshlrev_b32_e32 v72, 16, v41
	v_pk_fma_f32 v[42:43], v[64:65], v[64:65], v[42:43]
	v_mul_f32_e32 v67, v62, v62
	v_mul_f32_e32 v45, v63, v63
	v_and_b32_e32 v73, 0xffff0000, v41
	v_mul_f32_e32 v38, v72, v72
	v_mov_b32_e32 v44, v66
	v_and_b32_e32 v93, 0xffff0000, v48
	v_lshlrev_b32_e32 v68, 16, v49
	v_and_b32_e32 v69, 0xffff0000, v49
	v_pk_add_f32 v[42:43], v[42:43], v[42:43] op_sel_hi:[0,1]
	v_pk_fma_f32 v[40:41], v[72:73], v[72:73], v[38:39] op_sel_hi:[1,1,0]
	v_pk_add_f32 v[44:45], v[66:67], v[44:45]
	v_mul_f32_e32 v40, v93, v93
	v_mul_f32_e32 v42, v68, v68
	v_mul_f32_e32 v38, v69, v69
	v_mul_f32_e32 v46, v66, v66
	v_mov_b32_e32 v47, v45
	v_pk_add_f32 v[40:41], v[46:47], v[40:41]
	v_pk_add_f32 v[38:39], v[42:43], v[38:39]
	v_and_b32_e32 v83, 0xffff0000, v53
	v_pk_add_f32 v[38:39], v[40:41], v[38:39]
	v_and_b32_e32 v82, 0xffff0000, v52
	v_lshlrev_b32_e32 v74, 16, v50
	v_and_b32_e32 v75, 0xffff0000, v50
	v_pk_add_f32 v[38:39], v[38:39], v[38:39] op_sel_hi:[0,1]
	v_lshlrev_b32_e32 v77, 16, v53
	v_lshlrev_b32_e32 v76, 16, v52
	v_pk_mul_f32 v[40:41], v[82:83], v[82:83]
	v_lshlrev_b32_e32 v84, 16, v51
	v_pk_fma_f32 v[40:41], v[76:77], v[76:77], v[40:41]
	v_mul_f32_e32 v81, v74, v74
	v_mul_f32_e32 v43, v75, v75
	v_and_b32_e32 v85, 0xffff0000, v51
	v_mul_f32_e32 v38, v84, v84
	v_mov_b32_e32 v42, v80
	v_pk_add_f32 v[40:41], v[40:41], v[40:41] op_sel_hi:[0,1]
	v_pk_fma_f32 v[44:45], v[84:85], v[84:85], v[38:39] op_sel_hi:[1,1,0]
	v_pk_add_f32 v[42:43], v[80:81], v[42:43]
	v_mul_f32_e32 v44, v98, v98
	v_mul_f32_e32 v40, v78, v78
	v_mul_f32_e32 v38, v79, v79
	v_mul_f32_e32 v46, v80, v80
	v_mov_b32_e32 v47, v43
	v_pk_add_f32 v[42:43], v[46:47], v[44:45]
	v_pk_add_f32 v[38:39], v[40:41], v[38:39]
	s_mov_b32 s12, s0
	v_pk_add_f32 v[38:39], v[42:43], v[38:39]
	s_add_i32 s0, s0, 8
	v_add_f32_e32 v38, v38, v39
	s_cmp_ge_i32 s0, s3
	s_cselect_b64 s[10:11], -1, 0
	v_add_f32_dpp v38, v38, v38 quad_perm:[1,0,3,2] row_mask:0xf bank_mask:0xf bound_ctrl:1
	s_cmp_lt_i32 s0, s3
	s_cselect_b32 s8, s0, s12
	v_add_f32_dpp v38, v38, v38 quad_perm:[2,3,0,1] row_mask:0xf bank_mask:0xf bound_ctrl:1
	ds_swizzle_b32 v39, v38 offset:swizzle(SWAP,4)
	s_ashr_i32 s9, s8, 31
	s_lshl_b64 s[8:9], s[8:9], 12
	v_lshl_add_u64 v[86:87], v[34:35], 0, s[8:9]
	global_load_dwordx2 v[46:47], v[86:87], off
	global_load_dwordx2 v[44:45], v[86:87], off offset:512
	global_load_dwordx2 v[42:43], v[86:87], off offset:1024
	global_load_dwordx2 v[40:41], v[86:87], off offset:1536
	s_waitcnt lgkmcnt(0)
	v_add_f32_e32 v38, v38, v39
	s_nop 1
	v_mov_b32_dpp v39, v38 row_ror:8 row_mask:0xf bank_mask:0xf
	v_mov_b32_e32 v96, v59
	v_mov_b32_e32 v59, v60
	v_mov_b32_e32 v97, v61
	v_mov_b32_e32 v99, 0
	s_waitcnt lgkmcnt(0)
	v_add_f32_e32 v38, v38, v39
	v_mov_b32_e32 v39, v38
	v_mov_b32_e32 v100, 0
	s_ashr_i32 s13, s12, 31
	s_waitcnt lgkmcnt(0)
	s_nop 1
	v_permlane16_swap_b32_e32 v38, v39
	v_add_f32_e32 v38, v38, v39
	v_mov_b32_e32 v39, v38
	s_waitcnt lgkmcnt(0)
	s_nop 1
	v_permlane32_swap_b32_e32 v38, v39
	v_add_f32_e32 v38, v38, v39
	v_fmamk_f32 v38, v38, 0x3a000000, v89
	v_mul_f32_e32 v39, 0x4f800000, v38
	v_cmp_gt_f32_e32 vcc, s19, v38
	s_nop 1
	v_cndmask_b32_e32 v38, v38, v39, vcc
	v_sqrt_f32_e32 v39, v38
	s_nop 0
	v_add_u32_e32 v48, -1, v39
	v_fma_f32 v49, -v48, v39, v38
	v_cmp_ge_f32_e64 s[8:9], 0, v49
	v_add_u32_e32 v49, 1, v39
	s_nop 0
	v_cndmask_b32_e64 v48, v39, v48, s[8:9]
	v_fma_f32 v39, -v49, v39, v38
	v_cmp_lt_f32_e64 s[8:9], 0, v39
	s_nop 1
	v_cndmask_b32_e64 v39, v48, v49, s[8:9]
	v_mul_f32_e32 v48, 0x37800000, v39
	v_cndmask_b32_e32 v39, v39, v48, vcc
	v_cmp_class_f32_e32 vcc, v38, v90
	s_nop 1
	v_cndmask_b32_e32 v67, v39, v38, vcc
	global_load_dwordx2 v[48:49], v[86:87], off offset:2048
	global_load_dwordx2 v[52:53], v[86:87], off offset:2560
	global_load_dwordx2 v[50:51], v[86:87], off offset:3072
	global_load_dwordx2 v[38:39], v[86:87], off offset:3584
	v_div_scale_f32 v81, s[8:9], v67, v67, 1.0
	v_rcp_f32_e32 v94, v81
	s_lshl_b64 s[8:9], s[12:13], 11
	s_mov_b32 s13, 0
	v_fma_f32 v86, -v81, v94, 1.0
	v_fmac_f32_e32 v94, v86, v94
	v_div_scale_f32 v86, vcc, 1.0, v67, 1.0
	v_mul_f32_e32 v87, v86, v94
	v_fma_f32 v95, -v81, v87, v86
	v_fmac_f32_e32 v87, v95, v94
	v_fma_f32 v81, -v81, v87, v86
	v_div_fmas_f32 v81, v81, v94, v87
	v_div_fixup_f32 v86, v81, v67, 1.0
	v_mov_b32_e32 v94, v55
	v_mov_b32_e32 v95, v57
	v_mov_b32_e32 v55, v56
	v_pk_mul_f32 v[94:95], v[94:95], v[86:87] op_sel_hi:[1,0]
	v_pk_mul_f32 v[56:57], v[54:55], v[86:87] op_sel_hi:[1,0]
	v_pk_mul_f32 v[54:55], v[58:59], v[86:87] op_sel_hi:[1,0]
	v_mov_b32_e32 v58, v64
	v_mov_b32_e32 v59, v70
	v_mov_b32_e32 v70, v65
	v_mov_b32_e32 v67, v93
; DI unsigned pk4_fp8(float a, float b, float c, float d) { unsigned w = 0u; w = __builtin_amdgcn_cvt_pk_fp8_f32(a, b, w, false); w = __builtin_amdgcn_cvt_pk_fp8_f32(c, d, w, true); return w; }
; template <int MODE, bool SB  > DI void norm_phase(const Params& P, const Frame& F, int L, const void* src_, const float* gain, bool combine) {
;     ...
;         for (int j = 0; j < 8; ++j) v[j] = v[j] * rstd * g[j];
;         if (MODE == 4) {
; #pragma unroll
;             for (int j = 0; j < 8; ++j) *(f32x4*)(P.out + (size_t)row * D + 4 * F.lane + 256 * j) = v[j];
;         } else if (MODE == 0 || MODE == 2 || (MODE == 3 && L == 1)) {
;             unsigned* o4 = (unsigned*)((unsigned char*)HN + (size_t)row * D) + F.lane; const float hs = (float)(1 << LS_HN);
; #pragma unroll
;             for (int j = 0; j < 8; ++j) o4[64 * j] = pk4_fp8(v[j][0] * hs, v[j][1] * hs, v[j][2] * hs, v[j][3] * hs);
;     ...
;             int e1 = 0, e2 = 0; float l1 = -INFINITY, l2 = -INFINITY;
	v_pk_mul_f32 v[94:95], v[8:9], v[94:95]
	v_pk_mul_f32 v[60:61], v[86:87], v[58:59] op_sel_hi:[0,1]
	v_pk_mul_f32 v[58:59], v[86:87], v[70:71] op_sel_hi:[0,1]
	v_pk_mul_f32 v[70:71], v[66:67], v[86:87] op_sel_hi:[1,0]
	v_pk_mul_f32 v[56:57], v[0:1], v[56:57]
	v_pk_mul_f32 v[66:67], v[68:69], v[86:87] op_sel_hi:[1,0]
	v_pk_mul_f32 v[68:69], v[16:17], v[70:71]
	v_mov_b32_e32 v70, v76
	v_mov_b32_e32 v71, v82
	v_mov_b32_e32 v82, v77
	v_pk_mul_f32 v[76:77], v[74:75], v[86:87] op_sel_hi:[1,0]
	v_pk_mul_f32 v[74:75], v[84:85], v[86:87] op_sel_hi:[1,0]
	v_mul_f32_e32 v84, 4.0, v94
	v_mul_f32_e32 v85, 4.0, v95
	v_mov_b32_e32 v93, 0
	v_mov_b32_e32 v81, v98
	v_cvt_pk_fp8_f32 v93, v84, v85
	v_mul_f32_e32 v84, 4.0, v56
	v_mul_f32_e32 v85, 4.0, v57
	v_mov_b32_e32 v98, 0
	v_cvt_pk_fp8_f32 v98, v84, v85
	v_pk_mul_f32 v[54:55], v[2:3], v[54:55]
	v_pk_mul_f32 v[60:61], v[4:5], v[60:61]
	v_pk_mul_f32 v[64:65], v[62:63], v[86:87] op_sel_hi:[1,0]
	v_mul_f32_e32 v84, 4.0, v54
	v_mul_f32_e32 v85, 4.0, v55
	v_pk_mul_f32 v[96:97], v[96:97], v[86:87] op_sel_hi:[1,0]
	v_pk_mul_f32 v[64:65], v[12:13], v[64:65]
	v_cvt_pk_fp8_f32 v98, v84, v85 op_sel:[0,0,1]
	v_mul_f32_e32 v84, 4.0, v60
	v_mul_f32_e32 v85, 4.0, v61
	v_pk_mul_f32 v[96:97], v[10:11], v[96:97]
	v_cvt_pk_fp8_f32 v99, v84, v85
	v_mul_f32_e32 v84, 4.0, v64
	v_mul_f32_e32 v85, 4.0, v65
	v_pk_mul_f32 v[62:63], v[72:73], v[86:87] op_sel_hi:[1,0]
	v_pk_mul_f32 v[72:73], v[86:87], v[70:71] op_sel_hi:[0,1]
	v_pk_mul_f32 v[70:71], v[86:87], v[82:83] op_sel_hi:[0,1]
	v_pk_mul_f32 v[80:81], v[80:81], v[86:87] op_sel_hi:[1,0]
	v_pk_mul_f32 v[78:79], v[78:79], v[86:87] op_sel_hi:[1,0]
	v_mul_f32_e32 v86, 4.0, v96
	v_mul_f32_e32 v87, 4.0, v97
	v_cvt_pk_fp8_f32 v100, v84, v85
	v_pk_mul_f32 v[58:59], v[6:7], v[58:59]
	v_cvt_pk_fp8_f32 v93, v86, v87 op_sel:[0,0,1]
	v_pk_mul_f32 v[62:63], v[14:15], v[62:63]
	v_mul_f32_e32 v86, 4.0, v58
	v_mul_f32_e32 v87, 4.0, v59
	v_cvt_pk_fp8_f32 v99, v86, v87 op_sel:[0,0,1]
	v_mul_f32_e32 v84, 4.0, v62
	v_mul_f32_e32 v85, 4.0, v63
	v_lshl_add_u64 v[82:83], v[36:37], 0, s[8:9]
	v_cvt_pk_fp8_f32 v100, v84, v85 op_sel:[0,0,1]
	v_pk_mul_f32 v[72:73], v[20:21], v[72:73]
	global_store_dword v[82:83], v93, off
	global_store_dword v[82:83], v98, off offset:256
	global_store_dword v[82:83], v99, off offset:512
	global_store_dword v[82:83], v100, off offset:768
	v_mul_f32_e32 v84, 4.0, v68
	v_mul_f32_e32 v85, 4.0, v69
	v_mov_b32_e32 v93, 0
	v_cvt_pk_fp8_f32 v93, v84, v85
	v_mul_f32_e32 v84, 4.0, v72
	v_mul_f32_e32 v85, 4.0, v73
	v_mov_b32_e32 v98, 0
	v_cvt_pk_fp8_f32 v98, v84, v85
	v_pk_mul_f32 v[70:71], v[22:23], v[70:71]
	v_pk_mul_f32 v[76:77], v[24:25], v[76:77]
	v_mul_f32_e32 v84, 4.0, v70
	v_mul_f32_e32 v85, 4.0, v71
	v_pk_mul_f32 v[80:81], v[28:29], v[80:81]
	v_cvt_pk_fp8_f32 v98, v84, v85 op_sel:[0,0,1]
	v_mul_f32_e32 v84, 4.0, v76
	v_mul_f32_e32 v85, 4.0, v77
	v_mov_b32_e32 v99, 0
	v_pk_mul_f32 v[66:67], v[18:19], v[66:67]
	v_cvt_pk_fp8_f32 v99, v84, v85
	v_mul_f32_e32 v84, 4.0, v80
	v_mul_f32_e32 v85, 4.0, v81
	v_mov_b32_e32 v100, 0
	v_mul_f32_e32 v86, 4.0, v66
	v_mul_f32_e32 v87, 4.0, v67
	v_cvt_pk_fp8_f32 v100, v84, v85
	v_pk_mul_f32 v[74:75], v[26:27], v[74:75]
	v_cvt_pk_fp8_f32 v93, v86, v87 op_sel:[0,0,1]
	v_pk_mul_f32 v[78:79], v[30:31], v[78:79]
	v_mul_f32_e32 v86, 4.0, v74
	v_mul_f32_e32 v87, 4.0, v75
	v_cvt_pk_fp8_f32 v99, v86, v87 op_sel:[0,0,1]
	v_mul_f32_e32 v84, 4.0, v78
	v_mul_f32_e32 v85, 4.0, v79
	v_cvt_pk_fp8_f32 v100, v84, v85 op_sel:[0,0,1]
	global_store_dword v[82:83], v93, off offset:1024
	global_store_dword v[82:83], v98, off offset:1280
	global_store_dword v[82:83], v99, off offset:1536
	global_store_dword v[82:83], v100, off offset:1792
	v_mov_b32_e32 v84, v94
	v_mov_b32_e32 v85, v56
	v_mov_b32_e32 v56, v95
	v_mov_b32_e32 v86, v96
	v_mov_b32_e32 v87, v54
	v_mov_b32_e32 v54, v97
	v_mov_b32_e32 v95, 0xff800000
	v_mov_b32_e32 v94, v88
	v_mov_b32_e32 v93, 0xff800000
	v_mov_b32_e32 v96, 0
	v_mov_b32_e32 v83, 0
; #define LAS __attribute__((address_space(3)))
; DI float wave_sum(float v) { v += shx<1>(v); v += shx<2>(v); v += shx<4>(v); v += shx<8>(v); v += shx<16>(v); v += shx<32>(v); return v; }
; template <int MODE, bool SB  > DI void norm_phase(const Params& P, const Frame& F, int L, const void* src_, const float* gain, bool combine) {
;     ...
;         if (MODE == 2) {
;             int e1 = 0, e2 = 0; float l1 = -INFINITY, l2 = -INFINITY;
; #pragma unroll 1
;             for (int q = 0; q < 8; ++q) { float s = 0.f;
; #pragma unroll
;                 for (int j = 0; j < 8; ++j) { const f32x4 w = *(const LAS f32x4*)(F.lds + (size_t)(q * D + 256 * j + 4 * F.lane) * 4); s += (v[j][0] * w[0] + v[j][1] * w[1]) + (v[j][2] * w[2] + v[j][3] * w[3]); }
;                 s = wave_sum(s);
;                 if (s > l1) { l2 = l1; e2 = e1; l1 = s; e1 = q; } else if (s > l2) { l2 = s; e2 = q; } }
.LBB0_2880:
	ds_read_b128 v[98:101], v94
	ds_read_b128 v[102:105], v94 offset:1024
	s_waitcnt lgkmcnt(1)
	v_mov_b32_e32 v106, v98
	s_waitcnt lgkmcnt(0)
	v_mov_b32_e32 v107, v102
	v_mov_b32_e32 v102, v99
	v_mov_b32_e32 v99, v104
	v_mov_b32_e32 v104, v101
	v_mov_b32_e32 v98, v100
	v_pk_mul_f32 v[100:101], v[54:55], v[104:105]
	v_pk_mul_f32 v[102:103], v[56:57], v[102:103]
	v_pk_fma_f32 v[104:105], v[86:87], v[98:99], v[100:101]
	ds_read_b128 v[98:101], v94 offset:2048
	v_pk_fma_f32 v[102:103], v[84:85], v[106:107], v[102:103]
	s_nop 0
	v_pk_add_f32 v[102:103], v[102:103], v[104:105]
	s_nop 0
	v_add_f32_e32 v82, 0, v102
	v_add_f32_e32 v110, v82, v103
	ds_read_b128 v[102:105], v94 offset:3072
	s_waitcnt lgkmcnt(1)
	v_pk_mul_f32 v[106:107], v[58:59], v[100:101]
	v_pk_mul_f32 v[108:109], v[60:61], v[98:99]
	ds_read_b128 v[98:101], v94 offset:4096
	v_pk_mov_b32 v[112:113], v[108:109], v[106:107] op_sel:[1,0]
	v_mov_b32_e32 v109, v107
	v_pk_add_f32 v[112:113], v[112:113], v[108:109]
	ds_read_b128 v[106:109], v94 offset:5120
	s_waitcnt lgkmcnt(1)
	v_mul_f32_e32 v111, v68, v98
	v_mul_f32_e32 v82, v69, v99
	v_pk_add_f32 v[98:99], v[112:113], v[112:113] op_sel:[0,1] op_sel_hi:[1,0]
	v_mul_f32_e32 v97, v66, v100
	v_mov_b32_e32 v99, v82
	v_mul_f32_e32 v82, v65, v103
	v_mul_f32_e32 v114, v67, v101
	v_pk_fma_f32 v[100:101], v[64:65], v[102:103], v[82:83] op_sel_hi:[1,1,0]
	v_mul_f32_e32 v82, v63, v105
	v_pk_fma_f32 v[102:103], v[62:63], v[104:105], v[82:83] op_sel_hi:[1,1,0]
	v_mov_b32_e32 v101, v97
	v_mov_b32_e32 v103, v114
	v_pk_add_f32 v[98:99], v[110:111], v[98:99]
	v_pk_add_f32 v[100:101], v[100:101], v[102:103]
	s_waitcnt lgkmcnt(0)
	v_pk_mul_f32 v[108:109], v[70:71], v[108:109]
	v_pk_add_f32 v[110:111], v[98:99], v[100:101]
	ds_read_b128 v[98:101], v94 offset:6144
	ds_read_b128 v[102:105], v94 offset:7168
	v_pk_mul_f32 v[106:107], v[72:73], v[106:107]
	s_waitcnt lgkmcnt(0)
	v_mul_f32_e32 v82, v80, v102
	v_mul_f32_e32 v97, v81, v103
	v_pk_add_f32 v[102:103], v[110:111], v[110:111] op_sel:[0,1] op_sel_hi:[1,0]
	v_pk_mov_b32 v[112:113], v[106:107], v[108:109] op_sel:[1,0]
	v_mov_b32_e32 v107, v109
	v_mov_b32_e32 v103, v82
	v_mul_f32_e32 v82, v77, v99
	v_pk_add_f32 v[106:107], v[112:113], v[106:107]
	v_pk_fma_f32 v[98:99], v[76:77], v[98:99], v[82:83] op_sel_hi:[1,1,0]
	v_mul_f32_e32 v82, v75, v101
	v_mul_f32_e32 v108, v78, v104
	v_mul_f32_e32 v109, v79, v105
	v_pk_add_f32 v[104:105], v[106:107], v[106:107] op_sel:[0,1] op_sel_hi:[1,0]
	v_pk_fma_f32 v[100:101], v[74:75], v[100:101], v[82:83] op_sel_hi:[1,1,0]
	v_mov_b32_e32 v105, v97
	v_mov_b32_e32 v99, v108
	v_mov_b32_e32 v101, v109
	v_pk_add_f32 v[102:103], v[102:103], v[104:105]
	v_pk_add_f32 v[98:99], v[98:99], v[100:101]
	s_nop 0
	v_pk_add_f32 v[98:99], v[102:103], v[98:99]
	s_nop 0
	v_add_f32_e32 v82, v98, v99
	s_nop 1
	v_add_f32_dpp v82, v82, v82 quad_perm:[1,0,3,2] row_mask:0xf bank_mask:0xf bound_ctrl:1
	s_nop 1
	v_add_f32_dpp v82, v82, v82 quad_perm:[2,3,0,1] row_mask:0xf bank_mask:0xf bound_ctrl:1
	ds_swizzle_b32 v97, v82 offset:swizzle(SWAP,4)
	s_waitcnt lgkmcnt(0)
	v_add_f32_e32 v82, v82, v97
	s_nop 1
	v_mov_b32_dpp v97, v82 row_ror:8 row_mask:0xf bank_mask:0xf
	s_waitcnt lgkmcnt(0)
	v_add_f32_e32 v82, v82, v97
	v_mov_b32_e32 v97, v82
	s_waitcnt lgkmcnt(0)
	s_nop 1
	v_permlane16_swap_b32_e32 v82, v97
	v_add_f32_e32 v82, v82, v97
	v_mov_b32_e32 v97, v82
	s_waitcnt lgkmcnt(0)
	s_nop 1
	v_permlane32_swap_b32_e32 v82, v97
	v_add_f32_e32 v97, v82, v97
	v_cmp_ngt_f32_e32 vcc, v97, v93
	v_mov_b32_e32 v82, s13
	s_and_saveexec_b64 s[8:9], vcc
	s_cbranch_execz .LBB0_2884
	v_cmp_gt_f32_e32 vcc, v97, v95
	s_and_saveexec_b64 s[14:15], vcc
	v_mov_b32_e32 v96, s13
	v_mov_b32_e32 v95, v97
	s_or_b64 exec, exec, s[14:15]
	v_mov_b32_e32 v82, v83
	v_mov_b32_e32 v83, v96
	v_mov_b32_e32 v97, v93
	v_mov_b32_e32 v93, v95

.LBB0_2933:
	global_load_dword v1, v0, s[10:11] sc1
	s_waitcnt vmcnt(0)
	v_cmp_eq_u32_e32 vcc, 0, v1
	s_cbranch_vccnz .LBB0_2935
	s_mov_b64 s[18:19], -1
	s_mov_b64 s[22:23], -1
	s_branch .LBB0_2929
	s_nop 0
	s_nop 0
	s_nop 0
	s_nop 0
	s_nop 0
	s_nop 0
	s_nop 0
	s_nop 0
	s_nop 0
	s_nop 0
	s_nop 0
	s_nop 0
	s_nop 0
	s_nop 0
	s_nop 0
	s_nop 0
	s_nop 0
	s_nop 0
	s_nop 0
	s_nop 0
	s_nop 0
	s_nop 0
	s_nop 0
	s_nop 0
	s_nop 0
	s_nop 0
	s_nop 0
	s_nop 0
	s_nop 0
	s_nop 0
	s_nop 0
	s_nop 0
	s_nop 0
	s_nop 0
	s_nop 0
	s_nop 0
	s_nop 0
	s_nop 0
	s_nop 0
	s_nop 0
	s_nop 0
	s_nop 0
	s_nop 0
	s_nop 0
	s_nop 0
	s_nop 0
	s_nop 0
	s_nop 0
	s_nop 0
	s_nop 0
	s_nop 0
	s_nop 0
	s_nop 0
	s_nop 0
	s_nop 0
	s_nop 0
	s_nop 0
	s_nop 0
.LBB0_2935:
	s_cmp_lt_u32 s3, 0x40001
	s_mov_b64 s[18:19], 0
	s_cselect_b64 s[20:21], -1, 0
	s_mov_b64 s[22:23], -1
	s_and_b64 vcc, exec, s[20:21]
	s_cbranch_vccnz .LBB0_2932
	s_branch .LBB0_2929
	s_nop 0
	s_nop 0
	s_nop 0
	s_nop 0
	s_nop 0
	s_nop 0
	s_nop 0
	s_nop 0
	s_nop 0
	s_nop 0
	s_nop 0

; DI unsigned pk2(float lo, float hi) { const f32x2 v = {lo, hi}; return __builtin_bit_cast(unsigned, __builtin_convertvector(v, bf16x2_t)); }
; template <int MODE, bool SB  > DI void norm_phase(const Params& P, const Frame& F, int L, const void* src_, const float* gain, bool combine) {
;     ...
;     for (int row = r_lo + F.wave; row < r_hi; row += NWAVES) {
;         f32x4 v[8];
; #pragma unroll
;         for (int j = 0; j < 8; ++j) { if constexpr (SB) v[j] = (f32x4){bflo(vb[j].x), bfhi(vb[j].x), bflo(vb[j].y), bfhi(vb[j].y)}; else v[j] = vn[j]; }
;         { const int rnx = (row + NWAVES < r_hi) ? row + NWAVES : row;
; #pragma unroll
;           for (int j = 0; j < 8; ++j) { if constexpr (SB) vb[j] = *(const u32x2*)(srcb + (size_t)rnx * D + 4 * F.lane + 256 * j); else vn[j] = *(const f32x4*)(src + (size_t)rnx * D + 4 * F.lane + 256 * j); } }
;         if (MODE == 3 && combine) {
;             const int* SLOT = (const int*)(ws + WS_SLOT); const float* TOPW = (const float*)(ws + WS_TOPW); const bf16* Y = (const bf16*)(ws + WS_T + T_YPERM);
;             const int s1 = SLOT[row * 2], s2 = SLOT[row * 2 + 1]; const float w1 = TOPW[row * 2], w2 = TOPW[row * 2 + 1];
;             u32x2 ya[8], yb[8];
; #pragma unroll
;             for (int j = 0; j < 8; ++j) { ya[j] = *(const u32x2*)(Y + (size_t)s1 * D + 4 * F.lane + 256 * j); yb[j] = *(const u32x2*)(Y + (size_t)s2 * D + 4 * F.lane + 256 * j); }
; #pragma unroll
;             for (int j = 0; j < 8; ++j) { const f32x4 y1 = (f32x4){bflo(ya[j].x), bfhi(ya[j].x), bflo(ya[j].y), bfhi(ya[j].y)}, y2 = (f32x4){bflo(yb[j].x), bfhi(yb[j].x), bflo(yb[j].y), bfhi(yb[j].y)};
;                 v[j] = v[j] + w1 * y1 + w2 * y2;
;                 const u32x2 hb = {pk2(v[j][0], v[j][1]), pk2(v[j][2], v[j][3])}; *(u32x2*)(const_cast<bf16*>(srcb) + (size_t)row * D + 4 * F.lane + 256 * j) = hb;
;                 v[j] = (f32x4){bflo(hb.x), bfhi(hb.x), bflo(hb.y), bfhi(hb.y)}; }
;         }
.LBB0_3245:
	s_add_i32 s23, s4, 8
	s_cmp_lt_i32 s23, s3
	s_cselect_b64 s[14:15], -1, 0
	s_and_b64 s[24:25], s[14:15], exec
	s_cselect_b32 s4, s23, s4
	s_waitcnt vmcnt(7)
	v_lshlrev_b32_e32 v72, 16, v76
	v_and_b32_e32 v73, 0xffff0000, v76
	v_lshlrev_b32_e32 v74, 16, v77
	v_and_b32_e32 v75, 0xffff0000, v77
	v_lshl_add_u64 v[76:77], s[54:55], 0, v[42:43]
	s_ashr_i32 s7, s6, 31
	s_ashr_i32 s5, s4, 31
	v_add_co_u32_e32 v98, vcc, s20, v76
	s_lshl_b64 s[24:25], s[6:7], 2
	s_lshl_b64 s[4:5], s[4:5], 12
	s_waitcnt vmcnt(6)
	v_lshlrev_b32_e32 v68, 16, v78
	v_and_b32_e32 v69, 0xffff0000, v78
	v_lshlrev_b32_e32 v70, 16, v79
	v_and_b32_e32 v71, 0xffff0000, v79
	v_lshl_add_u64 v[78:79], s[54:55], 0, v[40:41]
	v_addc_co_u32_e32 v99, vcc, 0, v77, vcc
	v_lshl_add_u64 v[100:101], v[32:33], 0, s[4:5]
	s_add_u32 s4, s16, s24
	v_add_co_u32_e32 v92, vcc, s22, v78
	s_addc_u32 s5, s17, s25
	s_waitcnt vmcnt(0)
	v_lshlrev_b32_e32 v44, 16, v90
	v_and_b32_e32 v45, 0xffff0000, v90
	v_lshlrev_b32_e32 v46, 16, v91
	v_and_b32_e32 v47, 0xffff0000, v91
	v_lshlrev_b32_e32 v48, 16, v88
	v_and_b32_e32 v49, 0xffff0000, v88
	v_lshlrev_b32_e32 v50, 16, v89
	v_and_b32_e32 v51, 0xffff0000, v89
	v_lshlrev_b32_e32 v52, 16, v86
	v_and_b32_e32 v53, 0xffff0000, v86
	v_lshlrev_b32_e32 v54, 16, v87
	v_and_b32_e32 v55, 0xffff0000, v87
	v_lshlrev_b32_e32 v56, 16, v84
	v_and_b32_e32 v57, 0xffff0000, v84
	v_lshlrev_b32_e32 v58, 16, v85
	v_and_b32_e32 v59, 0xffff0000, v85
	v_lshlrev_b32_e32 v60, 16, v82
	v_and_b32_e32 v61, 0xffff0000, v82
	v_lshlrev_b32_e32 v62, 16, v83
	v_and_b32_e32 v63, 0xffff0000, v83
	v_lshlrev_b32_e32 v64, 16, v80
	v_and_b32_e32 v65, 0xffff0000, v80
	v_lshlrev_b32_e32 v66, 16, v81
	v_and_b32_e32 v67, 0xffff0000, v81
	v_addc_co_u32_e32 v93, vcc, 0, v79, vcc
	global_load_dwordx2 v[90:91], v[100:101], off
	global_load_dwordx2 v[88:89], v[100:101], off offset:512
	global_load_dwordx2 v[86:87], v[100:101], off offset:1024
	global_load_dwordx2 v[84:85], v[100:101], off offset:1536
	global_load_dwordx2 v[82:83], v[100:101], off offset:2048
	global_load_dwordx2 v[80:81], v[100:101], off offset:2560
	global_load_dwordx2 v[78:79], v[100:101], off offset:3072
	global_load_dwordx2 v[76:77], v[100:101], off offset:3584
	s_add_i32 s26, s6, 1
	global_load_dwordx2 v[100:101], v95, s[4:5]
	s_ashr_i32 s27, s26, 31
	s_add_u32 s4, s18, s24
	s_addc_u32 s5, s19, s25
	s_lshl_b64 s[24:25], s[26:27], 2
	global_load_dword v102, v95, s[4:5]
	s_add_u32 s4, s18, s24
	s_addc_u32 s5, s19, s25
	global_load_dword v104, v95, s[4:5]
	v_mov_b32_e32 v168, 0
	v_mov_b32_e32 v169, 0
	v_mov_b32_e32 v170, 0
	v_mov_b32_e32 v171, 0
	v_mov_b32_e32 v172, 0
	v_mov_b32_e32 v173, 0
	v_mov_b32_e32 v174, 0
	v_mov_b32_e32 v175, 0
	v_lshl_add_u64 v[40:41], v[40:41], 0, s[10:11]
	v_lshl_add_u64 v[42:43], v[42:43], 0, s[12:13]
	s_add_i32 s6, s6, 16
	s_waitcnt vmcnt(2)
	v_ashrrev_i32_e32 v107, 31, v100
	v_mov_b32_e32 v106, v100
	v_ashrrev_i32_e32 v109, 31, v101
	v_mov_b32_e32 v108, v101
	v_lshlrev_b64 v[100:101], 12, v[106:107]
	v_lshlrev_b64 v[106:107], 12, v[108:109]
	v_lshl_add_u64 v[100:101], v[34:35], 0, v[100:101]
	v_lshl_add_u64 v[106:107], v[34:35], 0, v[106:107]
	global_load_dwordx2 v[108:109], v[100:101], off
	global_load_dwordx2 v[110:111], v[106:107], off
	global_load_dwordx2 v[112:113], v[100:101], off offset:512
	global_load_dwordx2 v[114:115], v[106:107], off offset:512
	global_load_dwordx2 v[116:117], v[100:101], off offset:1024
	global_load_dwordx2 v[118:119], v[106:107], off offset:1024
	global_load_dwordx2 v[120:121], v[100:101], off offset:1536
	global_load_dwordx2 v[122:123], v[106:107], off offset:1536
	global_load_dwordx2 v[124:125], v[100:101], off offset:2048
	global_load_dwordx2 v[126:127], v[106:107], off offset:2048
	global_load_dwordx2 v[128:129], v[100:101], off offset:2560
	global_load_dwordx2 v[130:131], v[106:107], off offset:2560
	global_load_dwordx2 v[132:133], v[100:101], off offset:3072
	global_load_dwordx2 v[134:135], v[106:107], off offset:3072
	s_nop 0
	global_load_dwordx2 v[100:101], v[100:101], off offset:3584
	s_nop 0
	global_load_dwordx2 v[106:107], v[106:107], off offset:3584
	s_waitcnt vmcnt(15)
	v_lshlrev_b32_e32 v136, 16, v108
	v_and_b32_e32 v137, 0xffff0000, v108
	v_lshlrev_b32_e32 v108, 16, v109
	v_and_b32_e32 v109, 0xffff0000, v109
	s_waitcnt vmcnt(13)
	v_lshlrev_b32_e32 v140, 16, v112
	v_and_b32_e32 v141, 0xffff0000, v112
	v_lshlrev_b32_e32 v112, 16, v113
	v_and_b32_e32 v113, 0xffff0000, v113
	v_lshlrev_b32_e32 v138, 16, v110
	v_and_b32_e32 v139, 0xffff0000, v110
	v_lshlrev_b32_e32 v110, 16, v111
	v_and_b32_e32 v111, 0xffff0000, v111
	s_waitcnt vmcnt(12)
	v_lshlrev_b32_e32 v142, 16, v114
	v_and_b32_e32 v143, 0xffff0000, v114
	v_lshlrev_b32_e32 v114, 16, v115
	v_and_b32_e32 v115, 0xffff0000, v115
	s_waitcnt vmcnt(11)
	v_lshlrev_b32_e32 v144, 16, v116
	v_and_b32_e32 v145, 0xffff0000, v116
	v_lshlrev_b32_e32 v116, 16, v117
	v_and_b32_e32 v117, 0xffff0000, v117
	s_waitcnt vmcnt(9)
	v_lshlrev_b32_e32 v148, 16, v120
	v_and_b32_e32 v149, 0xffff0000, v120
	v_lshlrev_b32_e32 v120, 16, v121
	v_and_b32_e32 v121, 0xffff0000, v121
	s_waitcnt vmcnt(3)
	v_lshlrev_b32_e32 v160, 16, v132
	v_and_b32_e32 v161, 0xffff0000, v132
	v_lshlrev_b32_e32 v132, 16, v133
	v_and_b32_e32 v133, 0xffff0000, v133
	s_waitcnt vmcnt(1)
; DI unsigned pk2(float lo, float hi) { const f32x2 v = {lo, hi}; return __builtin_bit_cast(unsigned, __builtin_convertvector(v, bf16x2_t)); }
; template <int MODE, bool SB  > DI void norm_phase(const Params& P, const Frame& F, int L, const void* src_, const float* gain, bool combine) {
;     ...
;         if (MODE == 3 && combine) {
;             const int* SLOT = (const int*)(ws + WS_SLOT); const float* TOPW = (const float*)(ws + WS_TOPW); const bf16* Y = (const bf16*)(ws + WS_T + T_YPERM);
;             const int s1 = SLOT[row * 2], s2 = SLOT[row * 2 + 1]; const float w1 = TOPW[row * 2], w2 = TOPW[row * 2 + 1];
;             u32x2 ya[8], yb[8];
; #pragma unroll
;             for (int j = 0; j < 8; ++j) { ya[j] = *(const u32x2*)(Y + (size_t)s1 * D + 4 * F.lane + 256 * j); yb[j] = *(const u32x2*)(Y + (size_t)s2 * D + 4 * F.lane + 256 * j); }
; #pragma unroll
;             for (int j = 0; j < 8; ++j) { const f32x4 y1 = (f32x4){bflo(ya[j].x), bfhi(ya[j].x), bflo(ya[j].y), bfhi(ya[j].y)}, y2 = (f32x4){bflo(yb[j].x), bfhi(yb[j].x), bflo(yb[j].y), bfhi(yb[j].y)};
;                 v[j] = v[j] + w1 * y1 + w2 * y2;
;                 const u32x2 hb = {pk2(v[j][0], v[j][1]), pk2(v[j][2], v[j][3])}; *(u32x2*)(const_cast<bf16*>(srcb) + (size_t)row * D + 4 * F.lane + 256 * j) = hb;
;                 v[j] = (f32x4){bflo(hb.x), bfhi(hb.x), bflo(hb.y), bfhi(hb.y)}; }
;         }
;         float ss = 0.f;
; #pragma unroll
;         for (int j = 0; j < 8; ++j) ss += (v[j][0] * v[j][0] + v[j][1] * v[j][1]) + (v[j][2] * v[j][2] + v[j][3] * v[j][3]);
	v_lshlrev_b32_e32 v164, 16, v100
	v_and_b32_e32 v165, 0xffff0000, v100
	v_pk_fma_f32 v[44:45], v[102:103], v[136:137], v[44:45] op_sel_hi:[0,1,1]
	v_pk_fma_f32 v[46:47], v[102:103], v[108:109], v[46:47] op_sel_hi:[0,1,1]
	v_pk_fma_f32 v[48:49], v[102:103], v[140:141], v[48:49] op_sel_hi:[0,1,1]
	v_pk_fma_f32 v[50:51], v[102:103], v[112:113], v[50:51] op_sel_hi:[0,1,1]
	v_lshlrev_b32_e32 v146, 16, v118
	v_and_b32_e32 v147, 0xffff0000, v118
	v_lshlrev_b32_e32 v118, 16, v119
	v_and_b32_e32 v119, 0xffff0000, v119
	v_lshlrev_b32_e32 v150, 16, v122
	v_and_b32_e32 v151, 0xffff0000, v122
	v_lshlrev_b32_e32 v122, 16, v123
	v_and_b32_e32 v123, 0xffff0000, v123
	v_lshlrev_b32_e32 v152, 16, v124
	v_and_b32_e32 v153, 0xffff0000, v124
	v_lshlrev_b32_e32 v156, 16, v128
	v_and_b32_e32 v157, 0xffff0000, v128
	v_lshlrev_b32_e32 v162, 16, v134
	v_and_b32_e32 v163, 0xffff0000, v134
	v_lshlrev_b32_e32 v134, 16, v135
	v_and_b32_e32 v135, 0xffff0000, v135
	s_waitcnt vmcnt(0)
	v_lshlrev_b32_e32 v166, 16, v106
	v_and_b32_e32 v167, 0xffff0000, v106
	v_pk_fma_f32 v[52:53], v[102:103], v[144:145], v[52:53] op_sel_hi:[0,1,1]
	v_pk_fma_f32 v[54:55], v[102:103], v[116:117], v[54:55] op_sel_hi:[0,1,1]
	v_pk_fma_f32 v[56:57], v[102:103], v[148:149], v[56:57] op_sel_hi:[0,1,1]
	v_pk_fma_f32 v[58:59], v[102:103], v[120:121], v[58:59] op_sel_hi:[0,1,1]
	v_pk_fma_f32 v[68:69], v[102:103], v[160:161], v[68:69] op_sel_hi:[0,1,1]
	v_pk_fma_f32 v[70:71], v[102:103], v[132:133], v[70:71] op_sel_hi:[0,1,1]
	v_pk_fma_f32 v[72:73], v[102:103], v[164:165], v[72:73] op_sel_hi:[0,1,1]
	v_pk_fma_f32 v[46:47], v[104:105], v[110:111], v[46:47] op_sel_hi:[0,1,1]
	v_pk_fma_f32 v[44:45], v[104:105], v[138:139], v[44:45] op_sel_hi:[0,1,1]
	v_pk_fma_f32 v[50:51], v[104:105], v[114:115], v[50:51] op_sel_hi:[0,1,1]
	v_pk_fma_f32 v[48:49], v[104:105], v[142:143], v[48:49] op_sel_hi:[0,1,1]
	v_lshlrev_b32_e32 v154, 16, v126
	v_and_b32_e32 v155, 0xffff0000, v126
	v_lshlrev_b32_e32 v158, 16, v130
	v_and_b32_e32 v159, 0xffff0000, v130
	v_pk_fma_f32 v[60:61], v[102:103], v[152:153], v[60:61] op_sel_hi:[0,1,1]
	v_pk_fma_f32 v[64:65], v[102:103], v[156:157], v[64:65] op_sel_hi:[0,1,1]
	v_pk_fma_f32 v[54:55], v[104:105], v[118:119], v[54:55] op_sel_hi:[0,1,1]
	v_pk_fma_f32 v[52:53], v[104:105], v[146:147], v[52:53] op_sel_hi:[0,1,1]
	v_pk_fma_f32 v[58:59], v[104:105], v[122:123], v[58:59] op_sel_hi:[0,1,1]
	v_pk_fma_f32 v[56:57], v[104:105], v[150:151], v[56:57] op_sel_hi:[0,1,1]
	v_pk_fma_f32 v[70:71], v[104:105], v[134:135], v[70:71] op_sel_hi:[0,1,1]
	v_pk_fma_f32 v[68:69], v[104:105], v[162:163], v[68:69] op_sel_hi:[0,1,1]
	v_pk_fma_f32 v[72:73], v[104:105], v[166:167], v[72:73] op_sel_hi:[0,1,1]
	v_cvt_pk_bf16_f32 v44, v44, v45
	v_cvt_pk_bf16_f32 v45, v46, v47
	v_cvt_pk_bf16_f32 v46, v48, v49
	v_cvt_pk_bf16_f32 v47, v50, v51
	v_lshlrev_b32_e32 v124, 16, v125
	v_and_b32_e32 v125, 0xffff0000, v125
	v_lshlrev_b32_e32 v128, 16, v129
	v_and_b32_e32 v129, 0xffff0000, v129
	v_lshlrev_b32_e32 v100, 16, v101
	v_and_b32_e32 v101, 0xffff0000, v101
	v_pk_fma_f32 v[60:61], v[104:105], v[154:155], v[60:61] op_sel_hi:[0,1,1]
	v_pk_fma_f32 v[64:65], v[104:105], v[158:159], v[64:65] op_sel_hi:[0,1,1]
	v_cvt_pk_bf16_f32 v48, v52, v53
	v_cvt_pk_bf16_f32 v49, v54, v55
	v_cvt_pk_bf16_f32 v50, v56, v57
	v_cvt_pk_bf16_f32 v51, v58, v59
	v_cvt_pk_bf16_f32 v56, v68, v69
	v_cvt_pk_bf16_f32 v57, v70, v71
	v_cvt_pk_bf16_f32 v58, v72, v73
	global_store_dwordx2 v[98:99], v[44:45], off
	global_store_dwordx2 v[98:99], v[46:47], off offset:512
	global_store_dwordx2 v[98:99], v[48:49], off offset:1024
	global_store_dwordx2 v[98:99], v[50:51], off offset:1536
	v_lshlrev_b32_e32 v68, 16, v44
	v_and_b32_e32 v69, 0xffff0000, v44
	v_lshlrev_b32_e32 v44, 16, v45
	v_and_b32_e32 v45, 0xffff0000, v45
	v_lshlrev_b32_e32 v71, 16, v47
	v_lshlrev_b32_e32 v70, 16, v46
	v_and_b32_e32 v47, 0xffff0000, v47
	v_and_b32_e32 v46, 0xffff0000, v46
	v_lshlrev_b32_e32 v126, 16, v127
	v_and_b32_e32 v127, 0xffff0000, v127
	v_lshlrev_b32_e32 v130, 16, v131
	v_and_b32_e32 v131, 0xffff0000, v131
	v_lshlrev_b32_e32 v106, 16, v107
	v_and_b32_e32 v107, 0xffff0000, v107
	v_pk_fma_f32 v[62:63], v[102:103], v[124:125], v[62:63] op_sel_hi:[0,1,1]
	v_pk_fma_f32 v[66:67], v[102:103], v[128:129], v[66:67] op_sel_hi:[0,1,1]
	v_pk_fma_f32 v[74:75], v[102:103], v[100:101], v[74:75] op_sel_hi:[0,1,1]
	v_cvt_pk_bf16_f32 v52, v60, v61
	v_cvt_pk_bf16_f32 v54, v64, v65
	v_lshlrev_b32_e32 v61, 16, v50
	v_lshlrev_b32_e32 v65, 16, v58
	v_and_b32_e32 v73, 0xffff0000, v48
	v_mul_f32_e32 v60, v45, v45
	v_pk_mul_f32 v[102:103], v[46:47], v[46:47]
	v_mul_f32_e32 v64, v69, v69
	v_pk_fma_f32 v[62:63], v[104:105], v[126:127], v[62:63] op_sel_hi:[0,1,1]
	v_pk_fma_f32 v[66:67], v[104:105], v[130:131], v[66:67] op_sel_hi:[0,1,1]
	v_pk_fma_f32 v[74:75], v[104:105], v[106:107], v[74:75] op_sel_hi:[0,1,1]
	v_lshlrev_b32_e32 v72, 16, v48
	v_lshlrev_b32_e32 v48, 16, v49
	v_and_b32_e32 v49, 0xffff0000, v49
	v_mov_b32_e32 v105, v61
	v_mul_f32_e32 v104, v73, v73
	v_mov_b32_e32 v116, v70
	v_mov_b32_e32 v117, v46
	v_mov_b32_e32 v46, v71
	v_pk_fma_f32 v[122:123], v[44:45], v[44:45], v[60:61] op_sel_hi:[1,1,0]
	v_pk_fma_f32 v[70:71], v[70:71], v[70:71], v[102:103]
	v_pk_fma_f32 v[102:103], v[68:69], v[68:69], v[64:65] op_sel_hi:[1,1,0]
	v_cvt_pk_bf16_f32 v53, v62, v63
	v_and_b32_e32 v63, 0xffff0000, v50
	v_lshlrev_b32_e32 v50, 16, v51
	v_and_b32_e32 v51, 0xffff0000, v51
	v_mul_f32_e32 v106, v49, v49
	v_mov_b32_e32 v107, v65
	v_pk_fma_f32 v[124:125], v[72:73], v[72:73], v[104:105] op_sel_hi:[1,1,0]
	v_mov_b32_e32 v60, v102
	v_mov_b32_e32 v104, v122
	v_mul_f32_e32 v113, v63, v63
	v_mul_f32_e32 v115, v50, v50
; DI unsigned pk2(float lo, float hi) { const f32x2 v = {lo, hi}; return __builtin_bit_cast(unsigned, __builtin_convertvector(v, bf16x2_t)); }
; DI float wave_sum(float v) { v += shx<1>(v); v += shx<2>(v); v += shx<4>(v); v += shx<8>(v); v += shx<16>(v); v += shx<32>(v); return v; }
; template <int MODE, bool SB  > DI void norm_phase(const Params& P, const Frame& F, int L, const void* src_, const float* gain, bool combine) {
;     ...
;                 const u32x2 hb = {pk2(v[j][0], v[j][1]), pk2(v[j][2], v[j][3])}; *(u32x2*)(const_cast<bf16*>(srcb) + (size_t)row * D + 4 * F.lane + 256 * j) = hb;
;                 v[j] = (f32x4){bflo(hb.x), bfhi(hb.x), bflo(hb.y), bfhi(hb.y)}; }
;         }
;         float ss = 0.f;
; #pragma unroll
;         for (int j = 0; j < 8; ++j) ss += (v[j][0] * v[j][0] + v[j][1] * v[j][1]) + (v[j][2] * v[j][2] + v[j][3] * v[j][3]);
;         const float rstd = 1.0f / sqrtf(wave_sum(ss) * (1.0f / D) + EPS);
	v_mul_f32_e32 v128, v51, v51
	v_mov_b32_e32 v62, v61
	v_pk_fma_f32 v[126:127], v[48:49], v[48:49], v[106:107] op_sel_hi:[1,1,0]
	v_pk_add_f32 v[102:103], v[102:103], v[122:123]
	v_pk_add_f32 v[70:71], v[70:71], v[70:71] op_sel:[0,1] op_sel_hi:[1,0]
	v_pk_mul_f32 v[60:61], v[60:61], v[104:105]
	v_cvt_pk_bf16_f32 v55, v66, v67
	v_cvt_pk_bf16_f32 v59, v74, v75
	global_store_dwordx2 v[98:99], v[52:53], off offset:2048
	global_store_dwordx2 v[98:99], v[54:55], off offset:2560
	global_store_dwordx2 v[98:99], v[56:57], off offset:3072
	global_store_dwordx2 v[98:99], v[58:59], off offset:3584
	v_lshlrev_b32_e32 v75, 16, v53
	v_lshlrev_b32_e32 v74, 16, v52
	v_and_b32_e32 v53, 0xffff0000, v53
	v_and_b32_e32 v52, 0xffff0000, v52
	v_mov_b32_e32 v125, v115
	v_mov_b32_e32 v127, v128
	v_mov_b32_e32 v71, v113
	v_mov_b32_e32 v103, v61
	v_pk_mul_f32 v[108:109], v[52:53], v[52:53]
	v_pk_add_f32 v[104:105], v[124:125], v[126:127]
	v_pk_add_f32 v[60:61], v[102:103], v[70:71]
	v_lshlrev_b32_e32 v99, 16, v55
	v_lshlrev_b32_e32 v98, 16, v54
	v_and_b32_e32 v55, 0xffff0000, v55
	v_and_b32_e32 v54, 0xffff0000, v54
	v_mov_b32_e32 v118, v74
	v_mov_b32_e32 v119, v52
	v_mov_b32_e32 v52, v75
	v_pk_fma_f32 v[74:75], v[74:75], v[74:75], v[108:109]
	v_pk_add_f32 v[60:61], v[60:61], v[104:105]
	v_lshlrev_b32_e32 v100, 16, v56
	v_and_b32_e32 v101, 0xffff0000, v56
	v_lshlrev_b32_e32 v56, 16, v57
	v_and_b32_e32 v57, 0xffff0000, v57
	v_pk_mul_f32 v[110:111], v[54:55], v[54:55]
	v_pk_add_f32 v[74:75], v[74:75], v[74:75] op_sel:[0,1] op_sel_hi:[1,0]
	v_pk_add_f32 v[60:61], v[60:61], v[60:61] op_sel:[0,1] op_sel_hi:[1,0]
	v_and_b32_e32 v67, 0xffff0000, v58
	v_lshlrev_b32_e32 v58, 16, v59
	v_and_b32_e32 v59, 0xffff0000, v59
	v_mul_f32_e32 v112, v101, v101
	v_mul_f32_e32 v114, v57, v57
	v_mov_b32_e32 v120, v98
	v_mov_b32_e32 v121, v54
	v_mov_b32_e32 v54, v99
	v_pk_fma_f32 v[98:99], v[98:99], v[98:99], v[110:111]
	v_mov_b32_e32 v106, v74
	v_mov_b32_e32 v64, v60
	v_mul_f32_e32 v129, v67, v67
	v_mul_f32_e32 v130, v58, v58
	v_mul_f32_e32 v131, v59, v59
	v_mov_b32_e32 v66, v65
	v_pk_fma_f32 v[108:109], v[100:101], v[100:101], v[112:113] op_sel_hi:[1,1,0]
	v_pk_fma_f32 v[110:111], v[56:57], v[56:57], v[114:115] op_sel_hi:[1,1,0]
	v_pk_add_f32 v[98:99], v[98:99], v[98:99] op_sel:[0,1] op_sel_hi:[1,0]
	v_pk_add_f32 v[60:61], v[60:61], v[74:75]
	v_pk_mul_f32 v[64:65], v[64:65], v[106:107]
	v_mov_b32_e32 v109, v130
	v_mov_b32_e32 v111, v131
	v_mov_b32_e32 v99, v129
	v_mov_b32_e32 v61, v65
	v_pk_add_f32 v[108:109], v[108:109], v[110:111]
	v_pk_add_f32 v[60:61], v[60:61], v[98:99]
	s_nop 0
	v_pk_add_f32 v[60:61], v[60:61], v[108:109]
	s_nop 0
	v_add_f32_e32 v60, v60, v61
	s_nop 1
	v_add_f32_dpp v60, v60, v60 quad_perm:[1,0,3,2] row_mask:0xf bank_mask:0xf bound_ctrl:1
	s_nop 1
	v_add_f32_dpp v60, v60, v60 quad_perm:[2,3,0,1] row_mask:0xf bank_mask:0xf bound_ctrl:1
	ds_swizzle_b32 v61, v60 offset:swizzle(SWAP,4)
	s_waitcnt lgkmcnt(0)
	v_add_f32_e32 v60, v60, v61
	s_nop 1
	v_mov_b32_dpp v61, v60 row_ror:8 row_mask:0xf bank_mask:0xf
	s_waitcnt lgkmcnt(0)
	v_add_f32_e32 v60, v60, v61
	v_mov_b32_e32 v61, v60
	s_waitcnt lgkmcnt(0)
	s_nop 1
	v_permlane16_swap_b32_e32 v60, v61
	v_add_f32_e32 v60, v60, v61
	v_mov_b32_e32 v61, v60
	s_waitcnt lgkmcnt(0)
; DI unsigned pk2(float lo, float hi) { const f32x2 v = {lo, hi}; return __builtin_bit_cast(unsigned, __builtin_convertvector(v, bf16x2_t)); }
; DI unsigned pk4_fp8(float a, float b, float c, float d) { unsigned w = 0u; w = __builtin_amdgcn_cvt_pk_fp8_f32(a, b, w, false); w = __builtin_amdgcn_cvt_pk_fp8_f32(c, d, w, true); return w; }
; DI float wave_sum(float v) { v += shx<1>(v); v += shx<2>(v); v += shx<4>(v); v += shx<8>(v); v += shx<16>(v); v += shx<32>(v); return v; }
; template <int MODE, bool SB  > DI void norm_phase(const Params& P, const Frame& F, int L, const void* src_, const float* gain, bool combine) {
;     ...
;         const float rstd = 1.0f / sqrtf(wave_sum(ss) * (1.0f / D) + EPS);
; #pragma unroll
;         for (int j = 0; j < 8; ++j) v[j] = v[j] * rstd * g[j];
;         if (MODE == 4) {
; #pragma unroll
;             for (int j = 0; j < 8; ++j) *(f32x4*)(P.out + (size_t)row * D + 4 * F.lane + 256 * j) = v[j];
;         } else if (MODE == 0 || MODE == 2 || (MODE == 3 && L == 1)) {
;             unsigned* o4 = (unsigned*)((unsigned char*)HN + (size_t)row * D) + F.lane; const float hs = (float)(1 << LS_HN);
; #pragma unroll
;             for (int j = 0; j < 8; ++j) o4[64 * j] = pk4_fp8(v[j][0] * hs, v[j][1] * hs, v[j][2] * hs, v[j][3] * hs);
;     ...
;         if (MODE == 3) { const f32x4 pv = *(const f32x4*)(P.in[I_P] + ((size_t)L * M + row) * PLE + 4 * F.lane);
;             *((unsigned long long*)((bf16*)(ws + WS_T + T_PB) + (size_t)row * PLE) + F.lane) = (unsigned long long)pk2(pv[0], pv[1]) | ((unsigned long long)pk2(pv[2], pv[3]) << 32); }
	s_nop 1
	v_permlane32_swap_b32_e32 v60, v61
	v_add_f32_e32 v60, v60, v61
	v_fmamk_f32 v60, v60, 0x3a000000, v96
	v_mul_f32_e32 v61, 0x4f800000, v60
	v_cmp_gt_f32_e32 vcc, s21, v60
	s_nop 1
	v_cndmask_b32_e32 v60, v60, v61, vcc
	v_sqrt_f32_e32 v61, v60
	s_nop 0
	v_add_u32_e32 v64, -1, v61
	v_add_u32_e32 v65, 1, v61
	v_fma_f32 v70, -v64, v61, v60
	v_fma_f32 v71, -v65, v61, v60
	v_cmp_ge_f32_e64 s[4:5], 0, v70
	s_nop 1
	v_cndmask_b32_e64 v61, v61, v64, s[4:5]
	v_cmp_lt_f32_e64 s[4:5], 0, v71
	s_nop 1
	v_cndmask_b32_e64 v61, v61, v65, s[4:5]
	v_mul_f32_e32 v64, 0x37800000, v61
	v_cndmask_b32_e32 v61, v61, v64, vcc
	v_cmp_class_f32_e32 vcc, v60, v97
	s_nop 1
	v_cndmask_b32_e32 v60, v61, v60, vcc
	v_div_scale_f32 v61, s[4:5], v60, v60, 1.0
	v_rcp_f32_e32 v65, v61
	v_div_scale_f32 v64, vcc, 1.0, v60, 1.0
	s_mov_b32 s4, s23
	v_fma_f32 v70, -v61, v65, 1.0
	v_fmac_f32_e32 v65, v70, v65
	v_mul_f32_e32 v70, v64, v65
	v_fma_f32 v71, -v61, v70, v64
	v_fmac_f32_e32 v70, v71, v65
	v_fma_f32 v61, -v61, v70, v64
	v_div_fmas_f32 v61, v61, v65, v70
	v_div_fixup_f32 v60, v61, v60, 1.0
	v_pk_mul_f32 v[64:65], v[60:61], v[68:69] op_sel_hi:[0,1]
	v_pk_mul_f32 v[44:45], v[60:61], v[44:45] op_sel_hi:[0,1]
	v_pk_mul_f32 v[68:69], v[60:61], v[116:117] op_sel_hi:[0,1]
	v_pk_mul_f32 v[46:47], v[60:61], v[46:47] op_sel_hi:[0,1]
	v_pk_mul_f32 v[70:71], v[60:61], v[72:73] op_sel_hi:[0,1]
	v_pk_mul_f32 v[48:49], v[60:61], v[48:49] op_sel_hi:[0,1]
	v_pk_mul_f32 v[62:63], v[62:63], v[60:61] op_sel_hi:[1,0]
	v_pk_mul_f32 v[50:51], v[50:51], v[60:61] op_sel_hi:[1,0]
	v_pk_mul_f32 v[72:73], v[60:61], v[118:119] op_sel_hi:[0,1]
	v_pk_mul_f32 v[52:53], v[60:61], v[52:53] op_sel_hi:[0,1]
	v_pk_mul_f32 v[74:75], v[60:61], v[120:121] op_sel_hi:[0,1]
	v_pk_mul_f32 v[54:55], v[60:61], v[54:55] op_sel_hi:[0,1]
	v_pk_mul_f32 v[98:99], v[60:61], v[100:101] op_sel_hi:[0,1]
	v_pk_mul_f32 v[56:57], v[60:61], v[56:57] op_sel_hi:[0,1]
	v_pk_mul_f32 v[66:67], v[66:67], v[60:61] op_sel_hi:[1,0]
	v_pk_mul_f32 v[58:59], v[58:59], v[60:61] op_sel_hi:[1,0]
	v_pk_mul_f32 v[60:61], v[8:9], v[64:65]
	v_pk_mul_f32 v[64:65], v[0:1], v[68:69]
	v_mul_f32_e32 v60, 4.0, v60
	v_mul_f32_e32 v61, 4.0, v61
	v_pk_mul_f32 v[68:69], v[4:5], v[70:71]
	v_mul_f32_e32 v64, 4.0, v64
	v_mul_f32_e32 v65, 4.0, v65
	v_cvt_pk_fp8_f32 v168, v60, v61
	v_pk_mul_f32 v[62:63], v[12:13], v[62:63]
	v_mul_f32_e32 v68, 4.0, v68
	v_mul_f32_e32 v69, 4.0, v69
	v_cvt_pk_fp8_f32 v169, v64, v65
	v_pk_mul_f32 v[44:45], v[10:11], v[44:45]
	v_pk_mul_f32 v[70:71], v[16:17], v[72:73]
	v_pk_mul_f32 v[72:73], v[20:21], v[74:75]
	v_pk_mul_f32 v[74:75], v[24:25], v[98:99]
	v_pk_mul_f32 v[66:67], v[28:29], v[66:67]
	v_mul_f32_e32 v62, 4.0, v62
	v_mul_f32_e32 v63, 4.0, v63
	v_cvt_pk_fp8_f32 v170, v68, v69
	v_pk_mul_f32 v[46:47], v[2:3], v[46:47]
	v_mul_f32_e32 v44, 4.0, v44
	v_mul_f32_e32 v45, 4.0, v45
	v_mul_f32_e32 v70, 4.0, v70
	v_mul_f32_e32 v71, 4.0, v71
	v_mul_f32_e32 v72, 4.0, v72
	v_mul_f32_e32 v73, 4.0, v73
	v_mul_f32_e32 v74, 4.0, v74
	v_mul_f32_e32 v75, 4.0, v75
	v_mul_f32_e32 v66, 4.0, v66
	v_mul_f32_e32 v67, 4.0, v67
	v_cvt_pk_fp8_f32 v171, v62, v63
	v_pk_mul_f32 v[48:49], v[6:7], v[48:49]
	v_mul_f32_e32 v46, 4.0, v46
	v_mul_f32_e32 v47, 4.0, v47
	v_cvt_pk_fp8_f32 v172, v70, v71
	v_cvt_pk_fp8_f32 v173, v72, v73
	v_cvt_pk_fp8_f32 v174, v74, v75
	v_cvt_pk_fp8_f32 v175, v66, v67
	v_cvt_pk_fp8_f32 v168, v44, v45 op_sel:[0,0,1]
	v_pk_mul_f32 v[50:51], v[14:15], v[50:51]
	v_mul_f32_e32 v48, 4.0, v48
	v_mul_f32_e32 v49, 4.0, v49
	v_cvt_pk_fp8_f32 v169, v46, v47 op_sel:[0,0,1]
	v_pk_mul_f32 v[52:53], v[18:19], v[52:53]
	v_pk_mul_f32 v[54:55], v[22:23], v[54:55]
	v_pk_mul_f32 v[56:57], v[26:27], v[56:57]
	v_pk_mul_f32 v[58:59], v[30:31], v[58:59]
	v_mul_f32_e32 v50, 4.0, v50
	v_mul_f32_e32 v51, 4.0, v51
	v_cvt_pk_fp8_f32 v170, v48, v49 op_sel:[0,0,1]
	v_mul_f32_e32 v52, 4.0, v52
	v_mul_f32_e32 v53, 4.0, v53
	v_mul_f32_e32 v54, 4.0, v54
	v_mul_f32_e32 v55, 4.0, v55
	v_mul_f32_e32 v56, 4.0, v56
	v_mul_f32_e32 v57, 4.0, v57
	v_mul_f32_e32 v58, 4.0, v58
	v_mul_f32_e32 v59, 4.0, v59
	v_cvt_pk_fp8_f32 v171, v50, v51 op_sel:[0,0,1]
	v_cvt_pk_fp8_f32 v172, v52, v53 op_sel:[0,0,1]
	v_cvt_pk_fp8_f32 v173, v54, v55 op_sel:[0,0,1]
	v_cvt_pk_fp8_f32 v174, v56, v57 op_sel:[0,0,1]
	v_cvt_pk_fp8_f32 v175, v58, v59 op_sel:[0,0,1]
	global_store_dword v[92:93], v168, off
	global_store_dword v[92:93], v169, off offset:256
	global_store_dword v[92:93], v170, off offset:512
	global_store_dword v[92:93], v171, off offset:768
	global_store_dword v[92:93], v172, off offset:1024
	global_store_dword v[92:93], v173, off offset:1280
	global_store_dword v[92:93], v174, off offset:1536
	global_store_dword v[92:93], v175, off offset:1792
	global_load_dwordx4 v[44:47], v[38:39], off
	v_lshl_add_u64 v[48:49], s[54:55], 0, v[36:37]
	v_lshl_add_u64 v[36:37], v[36:37], 0, s[8:9]
	s_and_b64 vcc, s[14:15], exec
	v_lshl_add_u64 v[38:39], v[38:39], 0, s[0:1]
	s_waitcnt vmcnt(0)
	v_cvt_pk_bf16_f32 v44, v44, v45
	v_cvt_pk_bf16_f32 v45, v46, v47
	global_store_dwordx2 v[48:49], v[44:45], off
	s_cbranch_vccnz .LBB0_3245

; DI unsigned pk2(float lo, float hi) { const f32x2 v = {lo, hi}; return __builtin_bit_cast(unsigned, __builtin_convertvector(v, bf16x2_t)); }
; DI float wave_sum(float v) { v += shx<1>(v); v += shx<2>(v); v += shx<4>(v); v += shx<8>(v); v += shx<16>(v); v += shx<32>(v); return v; }
; template <int MODE, bool SB  > DI void norm_phase(const Params& P, const Frame& F, int L, const void* src_, const float* gain, bool combine) {
;     ...
;     for (int row = r_lo + F.wave; row < r_hi; row += NWAVES) {
;         f32x4 v[8];
; #pragma unroll
;         for (int j = 0; j < 8; ++j) { if constexpr (SB) v[j] = (f32x4){bflo(vb[j].x), bfhi(vb[j].x), bflo(vb[j].y), bfhi(vb[j].y)}; else v[j] = vn[j]; }
;         { const int rnx = (row + NWAVES < r_hi) ? row + NWAVES : row;
; #pragma unroll
;           for (int j = 0; j < 8; ++j) { if constexpr (SB) vb[j] = *(const u32x2*)(srcb + (size_t)rnx * D + 4 * F.lane + 256 * j); else vn[j] = *(const f32x4*)(src + (size_t)rnx * D + 4 * F.lane + 256 * j); } }
;         if (MODE == 3 && combine) {
;             const int* SLOT = (const int*)(ws + WS_SLOT); const float* TOPW = (const float*)(ws + WS_TOPW); const bf16* Y = (const bf16*)(ws + WS_T + T_YPERM);
;             const int s1 = SLOT[row * 2], s2 = SLOT[row * 2 + 1]; const float w1 = TOPW[row * 2], w2 = TOPW[row * 2 + 1];
;             u32x2 ya[8], yb[8];
; #pragma unroll
;             for (int j = 0; j < 8; ++j) { ya[j] = *(const u32x2*)(Y + (size_t)s1 * D + 4 * F.lane + 256 * j); yb[j] = *(const u32x2*)(Y + (size_t)s2 * D + 4 * F.lane + 256 * j); }
; #pragma unroll
;             for (int j = 0; j < 8; ++j) { const f32x4 y1 = (f32x4){bflo(ya[j].x), bfhi(ya[j].x), bflo(ya[j].y), bfhi(ya[j].y)}, y2 = (f32x4){bflo(yb[j].x), bfhi(yb[j].x), bflo(yb[j].y), bfhi(yb[j].y)};
;                 v[j] = v[j] + w1 * y1 + w2 * y2;
;                 const u32x2 hb = {pk2(v[j][0], v[j][1]), pk2(v[j][2], v[j][3])}; *(u32x2*)(const_cast<bf16*>(srcb) + (size_t)row * D + 4 * F.lane + 256 * j) = hb;
;                 v[j] = (f32x4){bflo(hb.x), bfhi(hb.x), bflo(hb.y), bfhi(hb.y)}; }
;         }
;         float ss = 0.f;
; #pragma unroll
;         for (int j = 0; j < 8; ++j) ss += (v[j][0] * v[j][0] + v[j][1] * v[j][1]) + (v[j][2] * v[j][2] + v[j][3] * v[j][3]);
;         const float rstd = 1.0f / sqrtf(wave_sum(ss) * (1.0f / D) + EPS);
.LBB0_3407:
	s_add_i32 s2, s6, 8
	s_waitcnt vmcnt(3)
	v_lshlrev_b32_e32 v42, 16, v40
	v_and_b32_e32 v43, 0xffff0000, v40
	v_lshlrev_b32_e32 v40, 16, v62
	v_and_b32_e32 v67, 0xffff0000, v62
	v_lshlrev_b32_e32 v46, 16, v63
	v_and_b32_e32 v47, 0xffff0000, v63
	v_lshlrev_b32_e32 v38, 16, v36
	v_and_b32_e32 v39, 0xffff0000, v36
	v_lshlrev_b32_e32 v36, 16, v60
	v_and_b32_e32 v89, 0xffff0000, v60
	v_lshlrev_b32_e32 v44, 16, v61
	v_and_b32_e32 v45, 0xffff0000, v61
	s_waitcnt vmcnt(0)
	v_and_b32_e32 v61, 0xffff0000, v58
	v_and_b32_e32 v60, 0xffff0000, v54
	v_and_b32_e32 v63, 0xffff0000, v59
	v_and_b32_e32 v62, 0xffff0000, v55
	s_cmp_lt_i32 s2, s8
	v_lshlrev_b32_e32 v49, 16, v58
	v_lshlrev_b32_e32 v48, 16, v54
	v_lshlrev_b32_e32 v51, 16, v59
	v_lshlrev_b32_e32 v50, 16, v55
	v_lshlrev_b32_e32 v69, 16, v53
	v_lshlrev_b32_e32 v68, 16, v52
	v_and_b32_e32 v53, 0xffff0000, v53
	v_and_b32_e32 v52, 0xffff0000, v52
	v_pk_mul_f32 v[72:73], v[60:61], v[60:61]
	v_pk_mul_f32 v[74:75], v[62:63], v[62:63]
	s_cselect_b64 s[4:5], -1, 0
	v_lshlrev_b32_e32 v54, 16, v41
	v_pk_mul_f32 v[76:77], v[52:53], v[52:53]
	v_pk_fma_f32 v[72:73], v[48:49], v[48:49], v[72:73]
	v_pk_fma_f32 v[74:75], v[50:51], v[50:51], v[74:75]
	s_and_b64 s[4:5], s[4:5], exec
	v_and_b32_e32 v55, 0xffff0000, v41
	v_lshlrev_b32_e32 v71, 16, v57
	v_lshlrev_b32_e32 v70, 16, v56
	v_and_b32_e32 v57, 0xffff0000, v57
	v_and_b32_e32 v56, 0xffff0000, v56
	v_lshlrev_b32_e32 v58, 16, v37
	v_mul_f32_e32 v41, v42, v42
	v_mul_f32_e32 v79, v43, v43
	v_mul_f32_e32 v80, v54, v54
	v_mov_b32_e32 v78, v40
	v_mov_b32_e32 v92, v49
	v_mov_b32_e32 v93, v61
	v_mov_b32_e32 v96, v68
	v_mov_b32_e32 v97, v52
	v_mov_b32_e32 v52, v69
	v_pk_fma_f32 v[68:69], v[68:69], v[68:69], v[76:77]
	v_mov_b32_e32 v49, v60
	v_pk_add_f32 v[60:61], v[72:73], v[74:75]
	s_cselect_b32 s10, s2, s6
	v_and_b32_e32 v59, 0xffff0000, v37
	v_pk_mul_f32 v[84:85], v[56:57], v[56:57]
	v_mul_f32_e32 v37, v38, v38
	v_mul_f32_e32 v87, v39, v39
	v_mul_f32_e32 v88, v58, v58
	v_mov_b32_e32 v86, v36
	v_mov_b32_e32 v94, v51
	v_mov_b32_e32 v95, v63
	v_pk_fma_f32 v[76:77], v[54:55], v[54:55], v[80:81] op_sel_hi:[1,1,0]
	v_pk_add_f32 v[78:79], v[40:41], v[78:79]
	v_mov_b32_e32 v51, v62
	v_pk_add_f32 v[62:63], v[68:69], v[68:69] op_sel_hi:[0,1]
	v_pk_add_f32 v[60:61], v[60:61], v[60:61] op_sel_hi:[0,1]
	s_ashr_i32 s11, s10, 31
	v_mul_f32_e32 v82, v40, v40
	v_mov_b32_e32 v98, v70
	v_mov_b32_e32 v99, v56
	v_mov_b32_e32 v56, v71
	v_pk_fma_f32 v[70:71], v[70:71], v[70:71], v[84:85]
	v_pk_fma_f32 v[80:81], v[58:59], v[58:59], v[88:89] op_sel_hi:[1,1,0]
	v_pk_add_f32 v[84:85], v[36:37], v[86:87]
	v_mul_f32_e32 v76, v67, v67
	v_mov_b32_e32 v83, v79
	v_mul_f32_e32 v62, v46, v46
	s_mov_b32 s6, s2
	v_mul_f32_e32 v60, v47, v47
	s_lshl_b64 s[2:3], s[10:11], 12
	v_mul_f32_e32 v90, v36, v36
	v_pk_add_f32 v[68:69], v[70:71], v[70:71] op_sel_hi:[0,1]
	v_mul_f32_e32 v80, v89, v89
	v_mov_b32_e32 v91, v85
	v_pk_add_f32 v[70:71], v[82:83], v[76:77]
	v_pk_add_f32 v[60:61], v[62:63], v[60:61]
	v_lshl_add_u64 v[74:75], v[32:33], 0, s[2:3]
	v_pk_add_f32 v[72:73], v[90:91], v[80:81]
	v_pk_add_f32 v[70:71], v[70:71], v[60:61]
	global_load_dwordx2 v[76:77], v[74:75], off
	global_load_dwordx2 v[78:79], v[74:75], off offset:512
	global_load_dwordx2 v[80:81], v[74:75], off offset:1024
	global_load_dwordx2 v[82:83], v[74:75], off offset:1536
	global_load_dwordx2 v[62:63], v[74:75], off offset:2048
	global_load_dwordx2 v[84:85], v[74:75], off offset:2560
	global_load_dwordx2 v[86:87], v[74:75], off offset:3072
	global_load_dwordx2 v[60:61], v[74:75], off offset:3584
	v_pk_add_f32 v[70:71], v[70:71], v[70:71] op_sel_hi:[0,1]
	v_mul_f32_e32 v68, v44, v44
	v_mul_f32_e32 v70, v45, v45
	v_pk_add_f32 v[68:69], v[68:69], v[70:71]
	v_mov_b32_e32 v41, v67
	v_pk_add_f32 v[68:69], v[72:73], v[68:69]
	v_mov_b32_e32 v37, v89
	v_add_f32_e32 v67, v68, v69
	s_nop 1
	v_add_f32_dpp v67, v67, v67 quad_perm:[1,0,3,2] row_mask:0xf bank_mask:0xf bound_ctrl:1
	s_nop 1
	v_add_f32_dpp v67, v67, v67 quad_perm:[2,3,0,1] row_mask:0xf bank_mask:0xf bound_ctrl:1
	ds_swizzle_b32 v68, v67 offset:swizzle(SWAP,4)
	s_waitcnt lgkmcnt(0)
; DI float wave_sum(float v) { v += shx<1>(v); v += shx<2>(v); v += shx<4>(v); v += shx<8>(v); v += shx<16>(v); v += shx<32>(v); return v; }
; template <int MODE, bool SB  > DI void norm_phase(const Params& P, const Frame& F, int L, const void* src_, const float* gain, bool combine) {
;     ...
;         const float rstd = 1.0f / sqrtf(wave_sum(ss) * (1.0f / D) + EPS);
; #pragma unroll
;         for (int j = 0; j < 8; ++j) v[j] = v[j] * rstd * g[j];
;         if (MODE == 4) {
; #pragma unroll
;             for (int j = 0; j < 8; ++j) *(f32x4*)(P.out + (size_t)row * D + 4 * F.lane + 256 * j) = v[j];
	v_add_f32_e32 v67, v67, v68
	s_nop 1
	v_mov_b32_dpp v68, v67 row_ror:8 row_mask:0xf bank_mask:0xf
	s_waitcnt lgkmcnt(0)
	v_add_f32_e32 v67, v67, v68
	v_mov_b32_e32 v68, v67
	s_waitcnt lgkmcnt(0)
	s_nop 1
	v_permlane16_swap_b32_e32 v67, v68
	v_add_f32_e32 v67, v67, v68
	v_mov_b32_e32 v68, v67
	s_waitcnt lgkmcnt(0)
	s_nop 1
	v_permlane32_swap_b32_e32 v67, v68
	v_add_f32_e32 v67, v67, v68
	v_fmamk_f32 v67, v67, 0x3a000000, v65
	v_mul_f32_e32 v68, 0x4f800000, v67
	v_cmp_gt_f32_e32 vcc, s7, v67
	s_nop 1
	v_cndmask_b32_e32 v67, v67, v68, vcc
	v_sqrt_f32_e32 v68, v67
	s_nop 0
	v_add_u32_e32 v69, -1, v68
	v_add_u32_e32 v70, 1, v68
	v_fma_f32 v71, -v69, v68, v67
	v_fma_f32 v72, -v70, v68, v67
	v_cmp_ge_f32_e64 s[2:3], 0, v71
	s_nop 1
	v_cndmask_b32_e64 v68, v68, v69, s[2:3]
	v_cmp_lt_f32_e64 s[2:3], 0, v72
	s_nop 1
	v_cndmask_b32_e64 v68, v68, v70, s[2:3]
	v_mul_f32_e32 v69, 0x37800000, v68
	v_cndmask_b32_e32 v68, v68, v69, vcc
	v_cmp_class_f32_e32 vcc, v67, v66
	s_nop 1
	v_cndmask_b32_e32 v67, v68, v67, vcc
	v_div_scale_f32 v68, s[2:3], v67, v67, 1.0
	v_rcp_f32_e32 v70, v68
	v_div_scale_f32 v69, vcc, 1.0, v67, 1.0
	v_fma_f32 v71, -v68, v70, 1.0
	v_fmac_f32_e32 v70, v71, v70
	v_mul_f32_e32 v71, v69, v70
	v_fma_f32 v72, -v68, v71, v69
	v_fmac_f32_e32 v71, v72, v70
	v_fma_f32 v68, -v68, v71, v69
	v_div_fmas_f32 v68, v68, v70, v71
	v_div_fixup_f32 v68, v68, v67, 1.0
	v_pk_mul_f32 v[70:71], v[92:93], v[68:69] op_sel_hi:[1,0]
	v_pk_mul_f32 v[72:73], v[94:95], v[68:69] op_sel_hi:[1,0]
	v_pk_mul_f32 v[48:49], v[48:49], v[68:69] op_sel_hi:[1,0]
	v_pk_mul_f32 v[50:51], v[50:51], v[68:69] op_sel_hi:[1,0]
	v_pk_mul_f32 v[52:53], v[68:69], v[52:53] op_sel_hi:[0,1]
	v_pk_mul_f32 v[54:55], v[54:55], v[68:69] op_sel_hi:[1,0]
	v_pk_mul_f32 v[90:91], v[40:41], v[68:69] op_sel_hi:[1,0]
	v_pk_mul_f32 v[92:93], v[46:47], v[68:69] op_sel_hi:[1,0]
	v_pk_mul_f32 v[94:95], v[68:69], v[98:99] op_sel_hi:[0,1]
	v_pk_mul_f32 v[56:57], v[68:69], v[56:57] op_sel_hi:[0,1]
	v_pk_mul_f32 v[74:75], v[68:69], v[96:97] op_sel_hi:[0,1]
	v_pk_mul_f32 v[88:89], v[42:43], v[68:69] op_sel_hi:[1,0]
	v_pk_mul_f32 v[96:97], v[38:39], v[68:69] op_sel_hi:[1,0]
	v_pk_mul_f32 v[98:99], v[58:59], v[68:69] op_sel_hi:[1,0]
	v_pk_mul_f32 v[100:101], v[36:37], v[68:69] op_sel_hi:[1,0]
	v_pk_mul_f32 v[102:103], v[44:45], v[68:69] op_sel_hi:[1,0]
	v_pk_mul_f32 v[38:39], v[2:3], v[72:73]
	v_pk_mul_f32 v[36:37], v[0:1], v[70:71]
	v_pk_mul_f32 v[42:43], v[6:7], v[50:51]
	v_pk_mul_f32 v[40:41], v[4:5], v[48:49]
	v_pk_mul_f32 v[46:47], v[10:11], v[52:53]
	v_pk_mul_f32 v[50:51], v[14:15], v[54:55]
	v_pk_mul_f32 v[54:55], v[18:19], v[92:93]
	v_pk_mul_f32 v[52:53], v[16:17], v[90:91]
	v_pk_mul_f32 v[58:59], v[22:23], v[56:57]
	v_pk_mul_f32 v[56:57], v[20:21], v[94:95]
	v_pk_mul_f32 v[44:45], v[8:9], v[74:75]
	v_pk_mul_f32 v[48:49], v[12:13], v[88:89]
	v_pk_mul_f32 v[70:71], v[26:27], v[98:99]
	v_pk_mul_f32 v[68:69], v[24:25], v[96:97]
	v_pk_mul_f32 v[74:75], v[30:31], v[102:103]
	v_pk_mul_f32 v[72:73], v[28:29], v[100:101]
	global_store_dwordx4 v[34:35], v[36:39], off offset:-4096
	global_store_dwordx4 v[34:35], v[40:43], off offset:-3072
	global_store_dwordx4 v[34:35], v[44:47], off offset:-2048
	global_store_dwordx4 v[34:35], v[48:51], off offset:-1024
	global_store_dwordx4 v[34:35], v[52:55], off
	global_store_dwordx4 v[34:35], v[56:59], off offset:1024
	global_store_dwordx4 v[34:35], v[68:71], off offset:2048
	global_store_dwordx4 v[34:35], v[72:75], off offset:3072
	v_lshl_add_u64 v[34:35], v[34:35], 0, s[0:1]
	s_waitcnt vmcnt(9)
	v_mov_b64_e32 v[36:37], v[86:87]
	v_mov_b64_e32 v[56:57], v[84:85]
	v_mov_b64_e32 v[40:41], v[82:83]
	v_mov_b64_e32 v[52:53], v[80:81]
	v_mov_b64_e32 v[54:55], v[78:79]
	v_mov_b64_e32 v[58:59], v[76:77]
	s_mov_b64 vcc, s[4:5]
	s_cbranch_vccnz .LBB0_3407
